# hand-written post phases with non-temporal row loads; indexer interleave; stick-breaking load hoist
# speedup vs baseline: 1.0027x; 1.0027x over previous
.Lmp_V1:
	global_load_dwordx2 v[128:129], v162, s[56:57] nt
	global_load_dwordx2 v[130:131], v162, s[56:57] offset:512 nt
	global_load_dwordx2 v[132:133], v162, s[56:57] offset:1024 nt
	global_load_dwordx2 v[134:135], v162, s[56:57] offset:1536 nt
	global_load_dwordx2 v[136:137], v162, s[56:57] offset:2048 nt
	global_load_dwordx2 v[138:139], v162, s[56:57] offset:2560 nt
	global_load_dwordx2 v[140:141], v162, s[56:57] offset:3072 nt
	global_load_dwordx2 v[142:143], v162, s[56:57] offset:3584 nt
	global_load_dwordx2 v[144:145], v162, s[58:59] nt
	global_load_dwordx2 v[146:147], v162, s[58:59] offset:512 nt
	global_load_dwordx2 v[148:149], v162, s[58:59] offset:1024 nt
	global_load_dwordx2 v[150:151], v162, s[58:59] offset:1536 nt
	global_load_dwordx2 v[152:153], v162, s[58:59] offset:2048 nt
	global_load_dwordx2 v[154:155], v162, s[58:59] offset:2560 nt
	global_load_dwordx2 v[156:157], v162, s[58:59] offset:3072 nt
	global_load_dwordx2 v[158:159], v162, s[58:59] offset:3584 nt
	s_add_u32 s58, s58, 0x8000
	s_addc_u32 s59, s59, 0
	s_add_u32 s56, s56, 0x8000
	s_addc_u32 s57, s57, 0
	global_load_dwordx2 v[166:167], v162, s[56:57] nt
	global_load_dwordx2 v[168:169], v162, s[56:57] offset:512 nt
	global_load_dwordx2 v[170:171], v162, s[56:57] offset:1024 nt
	global_load_dwordx2 v[172:173], v162, s[56:57] offset:1536 nt
	global_load_dwordx2 v[174:175], v162, s[56:57] offset:2048 nt
	global_load_dwordx2 v[176:177], v162, s[56:57] offset:2560 nt
	global_load_dwordx2 v[178:179], v162, s[56:57] offset:3072 nt
	global_load_dwordx2 v[180:181], v162, s[56:57] offset:3584 nt
	global_load_dwordx2 v[182:183], v162, s[58:59] nt
	global_load_dwordx2 v[184:185], v162, s[58:59] offset:512 nt
	global_load_dwordx2 v[186:187], v162, s[58:59] offset:1024 nt
	global_load_dwordx2 v[188:189], v162, s[58:59] offset:1536 nt
	global_load_dwordx2 v[190:191], v162, s[58:59] offset:2048 nt
	global_load_dwordx2 v[192:193], v162, s[58:59] offset:2560 nt
	global_load_dwordx2 v[194:195], v162, s[58:59] offset:3072 nt
	global_load_dwordx2 v[196:197], v162, s[58:59] offset:3584 nt
	s_add_u32 s58, s58, 0x8000
	s_addc_u32 s59, s59, 0
	s_add_u32 s56, s56, 0x8000
	s_addc_u32 s57, s57, 0
	s_waitcnt vmcnt(16)
.Lmp_V1_loop:
	s_waitcnt vmcnt(32)
	v_mov_b32_e32 v250, 0
	v_mov_b32_e32 v251, 0
	v_lshlrev_b32_e32 v246, 16, v128
	v_and_b32_e32 v247, 0xffff0000, v128
	v_lshlrev_b32_e32 v248, 16, v129
	v_and_b32_e32 v249, 0xffff0000, v129
	v_fmac_f32_e32 v250, v246, v246
	v_fmac_f32_e32 v251, v247, v247
	v_fmac_f32_e32 v250, v248, v248
	v_fmac_f32_e32 v251, v249, v249
	v_lshlrev_b32_e32 v246, 16, v130
	v_and_b32_e32 v247, 0xffff0000, v130
	v_lshlrev_b32_e32 v248, 16, v131
	v_and_b32_e32 v249, 0xffff0000, v131
	v_fmac_f32_e32 v250, v246, v246
	v_fmac_f32_e32 v251, v247, v247
	v_fmac_f32_e32 v250, v248, v248
	v_fmac_f32_e32 v251, v249, v249
	v_lshlrev_b32_e32 v246, 16, v132
	v_and_b32_e32 v247, 0xffff0000, v132
	v_lshlrev_b32_e32 v248, 16, v133
	v_and_b32_e32 v249, 0xffff0000, v133
	v_fmac_f32_e32 v250, v246, v246
	v_fmac_f32_e32 v251, v247, v247
	v_fmac_f32_e32 v250, v248, v248
	v_fmac_f32_e32 v251, v249, v249
	v_lshlrev_b32_e32 v246, 16, v134
	v_and_b32_e32 v247, 0xffff0000, v134
	v_lshlrev_b32_e32 v248, 16, v135
	v_and_b32_e32 v249, 0xffff0000, v135
	v_fmac_f32_e32 v250, v246, v246
	v_fmac_f32_e32 v251, v247, v247
	v_fmac_f32_e32 v250, v248, v248
	v_fmac_f32_e32 v251, v249, v249
	v_lshlrev_b32_e32 v246, 16, v136
	v_and_b32_e32 v247, 0xffff0000, v136
	v_lshlrev_b32_e32 v248, 16, v137
	v_and_b32_e32 v249, 0xffff0000, v137
	v_fmac_f32_e32 v250, v246, v246
	v_fmac_f32_e32 v251, v247, v247
	v_fmac_f32_e32 v250, v248, v248
	v_fmac_f32_e32 v251, v249, v249
	v_lshlrev_b32_e32 v246, 16, v138
	v_and_b32_e32 v247, 0xffff0000, v138
	v_lshlrev_b32_e32 v248, 16, v139
	v_and_b32_e32 v249, 0xffff0000, v139
	v_fmac_f32_e32 v250, v246, v246
	v_fmac_f32_e32 v251, v247, v247
	v_fmac_f32_e32 v250, v248, v248
	v_fmac_f32_e32 v251, v249, v249
	v_lshlrev_b32_e32 v246, 16, v140
	v_and_b32_e32 v247, 0xffff0000, v140
	v_lshlrev_b32_e32 v248, 16, v141
	v_and_b32_e32 v249, 0xffff0000, v141
	v_fmac_f32_e32 v250, v246, v246
	v_fmac_f32_e32 v251, v247, v247
	v_fmac_f32_e32 v250, v248, v248
	v_fmac_f32_e32 v251, v249, v249
	v_lshlrev_b32_e32 v246, 16, v142
	v_and_b32_e32 v247, 0xffff0000, v142
	v_lshlrev_b32_e32 v248, 16, v143
	v_and_b32_e32 v249, 0xffff0000, v143
	v_fmac_f32_e32 v250, v246, v246
	v_fmac_f32_e32 v251, v247, v247
	v_fmac_f32_e32 v250, v248, v248
	v_fmac_f32_e32 v251, v249, v249
	v_add_f32_e32 v250, v250, v251
	s_nop 1
	v_add_f32_dpp v218, v250, v250 quad_perm:[1,0,3,2] row_mask:0xf bank_mask:0xf bound_ctrl:1
	s_nop 1
	v_add_f32_dpp v218, v218, v218 quad_perm:[2,3,0,1] row_mask:0xf bank_mask:0xf bound_ctrl:1
	s_nop 1
	v_add_f32_dpp v218, v218, v218 row_ror:4 row_mask:0xf bank_mask:0xf bound_ctrl:1
	s_nop 1
	v_add_f32_dpp v218, v218, v218 row_ror:8 row_mask:0xf bank_mask:0xf bound_ctrl:1
	s_nop 1
	v_readlane_b32 s8, v218, 0
	v_readlane_b32 s9, v218, 16
	v_readlane_b32 s10, v218, 32
	v_readlane_b32 s11, v218, 48
	s_nop 1
	v_mov_b32_e32 v218, s8
	v_add_f32_e32 v218, s9, v218
	v_mov_b32_e32 v219, s10
	v_add_f32_e32 v219, s11, v219
	v_add_f32_e32 v218, v218, v219
	v_mul_f32_e32 v218, 0x3a000000, v218
	v_add_f32_e32 v218, 0x358637bd, v218
	v_rsq_f32_e32 v218, v218
	s_nop 0
	v_lshlrev_b32_e32 v246, 16, v128
	v_and_b32_e32 v247, 0xffff0000, v128
	v_lshlrev_b32_e32 v248, 16, v129
	v_and_b32_e32 v249, 0xffff0000, v129
	v_mul_f32_e32 v246, v246, v218
	v_mul_f32_e32 v247, v247, v218
	v_mul_f32_e32 v248, v248, v218
	v_mul_f32_e32 v249, v249, v218
	v_lshlrev_b32_e32 v0, 16, v144
	v_and_b32_e32 v1, 0xffff0000, v144
	v_lshlrev_b32_e32 v2, 16, v145
	v_and_b32_e32 v3, 0xffff0000, v145
	v_fmac_f32_e32 v0, v246, v32
	v_fmac_f32_e32 v1, v247, v33
	v_fmac_f32_e32 v2, v248, v34
	v_fmac_f32_e32 v3, v249, v35
	v_lshlrev_b32_e32 v246, 16, v130
	v_and_b32_e32 v247, 0xffff0000, v130
	v_lshlrev_b32_e32 v248, 16, v131
	v_and_b32_e32 v249, 0xffff0000, v131
	v_mul_f32_e32 v246, v246, v218
	v_mul_f32_e32 v247, v247, v218
	v_mul_f32_e32 v248, v248, v218
	v_mul_f32_e32 v249, v249, v218
	v_lshlrev_b32_e32 v4, 16, v146
	v_and_b32_e32 v5, 0xffff0000, v146
	v_lshlrev_b32_e32 v6, 16, v147
	v_and_b32_e32 v7, 0xffff0000, v147
	v_fmac_f32_e32 v4, v246, v36
	v_fmac_f32_e32 v5, v247, v37
	v_fmac_f32_e32 v6, v248, v38
	v_fmac_f32_e32 v7, v249, v39
	v_lshlrev_b32_e32 v246, 16, v132
	v_and_b32_e32 v247, 0xffff0000, v132
	v_lshlrev_b32_e32 v248, 16, v133
	v_and_b32_e32 v249, 0xffff0000, v133
	v_mul_f32_e32 v246, v246, v218
	v_mul_f32_e32 v247, v247, v218
	v_mul_f32_e32 v248, v248, v218
	v_mul_f32_e32 v249, v249, v218
	v_lshlrev_b32_e32 v8, 16, v148
	v_and_b32_e32 v9, 0xffff0000, v148
	v_lshlrev_b32_e32 v10, 16, v149
	v_and_b32_e32 v11, 0xffff0000, v149
	v_fmac_f32_e32 v8, v246, v40
	v_fmac_f32_e32 v9, v247, v41
	v_fmac_f32_e32 v10, v248, v42
	v_fmac_f32_e32 v11, v249, v43
	v_lshlrev_b32_e32 v246, 16, v134
	v_and_b32_e32 v247, 0xffff0000, v134
	v_lshlrev_b32_e32 v248, 16, v135
	v_and_b32_e32 v249, 0xffff0000, v135
	v_mul_f32_e32 v246, v246, v218
	v_mul_f32_e32 v247, v247, v218
	v_mul_f32_e32 v248, v248, v218
	v_mul_f32_e32 v249, v249, v218
	v_lshlrev_b32_e32 v12, 16, v150
	v_and_b32_e32 v13, 0xffff0000, v150
	v_lshlrev_b32_e32 v14, 16, v151
	v_and_b32_e32 v15, 0xffff0000, v151
	v_fmac_f32_e32 v12, v246, v44
	v_fmac_f32_e32 v13, v247, v45
	v_fmac_f32_e32 v14, v248, v46
	v_fmac_f32_e32 v15, v249, v47
	v_lshlrev_b32_e32 v246, 16, v136
	v_and_b32_e32 v247, 0xffff0000, v136
	v_lshlrev_b32_e32 v248, 16, v137
	v_and_b32_e32 v249, 0xffff0000, v137
	v_mul_f32_e32 v246, v246, v218
	v_mul_f32_e32 v247, v247, v218
	v_mul_f32_e32 v248, v248, v218
	v_mul_f32_e32 v249, v249, v218
	v_lshlrev_b32_e32 v16, 16, v152
	v_and_b32_e32 v17, 0xffff0000, v152
	v_lshlrev_b32_e32 v18, 16, v153
	v_and_b32_e32 v19, 0xffff0000, v153
	v_fmac_f32_e32 v16, v246, v48
	v_fmac_f32_e32 v17, v247, v49
	v_fmac_f32_e32 v18, v248, v50
	v_fmac_f32_e32 v19, v249, v51
	v_lshlrev_b32_e32 v246, 16, v138
	v_and_b32_e32 v247, 0xffff0000, v138
	v_lshlrev_b32_e32 v248, 16, v139
	v_and_b32_e32 v249, 0xffff0000, v139
	v_mul_f32_e32 v246, v246, v218
	v_mul_f32_e32 v247, v247, v218
	v_mul_f32_e32 v248, v248, v218
	v_mul_f32_e32 v249, v249, v218
	v_lshlrev_b32_e32 v20, 16, v154
	v_and_b32_e32 v21, 0xffff0000, v154
	v_lshlrev_b32_e32 v22, 16, v155
	v_and_b32_e32 v23, 0xffff0000, v155
	v_fmac_f32_e32 v20, v246, v52
	v_fmac_f32_e32 v21, v247, v53
	v_fmac_f32_e32 v22, v248, v54
	v_fmac_f32_e32 v23, v249, v55
	v_lshlrev_b32_e32 v246, 16, v140
	v_and_b32_e32 v247, 0xffff0000, v140
	v_lshlrev_b32_e32 v248, 16, v141
	v_and_b32_e32 v249, 0xffff0000, v141
	v_mul_f32_e32 v246, v246, v218
	v_mul_f32_e32 v247, v247, v218
	v_mul_f32_e32 v248, v248, v218
	v_mul_f32_e32 v249, v249, v218
	v_lshlrev_b32_e32 v24, 16, v156
	v_and_b32_e32 v25, 0xffff0000, v156
	v_lshlrev_b32_e32 v26, 16, v157
	v_and_b32_e32 v27, 0xffff0000, v157
	v_fmac_f32_e32 v24, v246, v56
	v_fmac_f32_e32 v25, v247, v57
	v_fmac_f32_e32 v26, v248, v58
	v_fmac_f32_e32 v27, v249, v59
	v_lshlrev_b32_e32 v246, 16, v142
	v_and_b32_e32 v247, 0xffff0000, v142
	v_lshlrev_b32_e32 v248, 16, v143
	v_and_b32_e32 v249, 0xffff0000, v143
	v_mul_f32_e32 v246, v246, v218
	v_mul_f32_e32 v247, v247, v218
	v_mul_f32_e32 v248, v248, v218
	v_mul_f32_e32 v249, v249, v218
	v_lshlrev_b32_e32 v28, 16, v158
	v_and_b32_e32 v29, 0xffff0000, v158
	v_lshlrev_b32_e32 v30, 16, v159
	v_and_b32_e32 v31, 0xffff0000, v159
	v_fmac_f32_e32 v28, v246, v60
	v_fmac_f32_e32 v29, v247, v61
	v_fmac_f32_e32 v30, v248, v62
	v_fmac_f32_e32 v31, v249, v63
	global_load_dwordx2 v[128:129], v162, s[56:57] nt
	global_load_dwordx2 v[130:131], v162, s[56:57] offset:512 nt
	global_load_dwordx2 v[132:133], v162, s[56:57] offset:1024 nt
	global_load_dwordx2 v[134:135], v162, s[56:57] offset:1536 nt
	global_load_dwordx2 v[136:137], v162, s[56:57] offset:2048 nt
	global_load_dwordx2 v[138:139], v162, s[56:57] offset:2560 nt
	global_load_dwordx2 v[140:141], v162, s[56:57] offset:3072 nt
	global_load_dwordx2 v[142:143], v162, s[56:57] offset:3584 nt
	global_load_dwordx2 v[144:145], v162, s[58:59] nt
	global_load_dwordx2 v[146:147], v162, s[58:59] offset:512 nt
	global_load_dwordx2 v[148:149], v162, s[58:59] offset:1024 nt
	global_load_dwordx2 v[150:151], v162, s[58:59] offset:1536 nt
	global_load_dwordx2 v[152:153], v162, s[58:59] offset:2048 nt
	global_load_dwordx2 v[154:155], v162, s[58:59] offset:2560 nt
	global_load_dwordx2 v[156:157], v162, s[58:59] offset:3072 nt
	global_load_dwordx2 v[158:159], v162, s[58:59] offset:3584 nt
	s_add_u32 s58, s58, 0x8000
	s_addc_u32 s59, s59, 0
	s_add_u32 s56, s56, 0x8000
	s_addc_u32 s57, s57, 0
	v_mov_b32_e32 v250, 0
	v_mov_b32_e32 v251, 0
	v_cvt_pk_bf16_f32 v238, v0, v1
	v_cvt_pk_bf16_f32 v239, v2, v3
	v_fmac_f32_e32 v250, v0, v0
	v_fmac_f32_e32 v251, v1, v1
	v_fmac_f32_e32 v250, v2, v2
	v_fmac_f32_e32 v251, v3, v3
	global_store_dwordx2 v162, v[238:239], s[70:71]
	v_cvt_pk_bf16_f32 v240, v4, v5
	v_cvt_pk_bf16_f32 v241, v6, v7
	v_fmac_f32_e32 v250, v4, v4
	v_fmac_f32_e32 v251, v5, v5
	v_fmac_f32_e32 v250, v6, v6
	v_fmac_f32_e32 v251, v7, v7
	global_store_dwordx2 v162, v[240:241], s[70:71] offset:512
	v_cvt_pk_bf16_f32 v242, v8, v9
	v_cvt_pk_bf16_f32 v243, v10, v11
	v_fmac_f32_e32 v250, v8, v8
	v_fmac_f32_e32 v251, v9, v9
	v_fmac_f32_e32 v250, v10, v10
	v_fmac_f32_e32 v251, v11, v11
	global_store_dwordx2 v162, v[242:243], s[70:71] offset:1024
	v_cvt_pk_bf16_f32 v244, v12, v13
	v_cvt_pk_bf16_f32 v245, v14, v15
	v_fmac_f32_e32 v250, v12, v12
	v_fmac_f32_e32 v251, v13, v13
	v_fmac_f32_e32 v250, v14, v14
	v_fmac_f32_e32 v251, v15, v15
	global_store_dwordx2 v162, v[244:245], s[70:71] offset:1536
	v_cvt_pk_bf16_f32 v238, v16, v17
	v_cvt_pk_bf16_f32 v239, v18, v19
	v_fmac_f32_e32 v250, v16, v16
	v_fmac_f32_e32 v251, v17, v17
	v_fmac_f32_e32 v250, v18, v18
	v_fmac_f32_e32 v251, v19, v19
	global_store_dwordx2 v162, v[238:239], s[70:71] offset:2048
	v_cvt_pk_bf16_f32 v240, v20, v21
	v_cvt_pk_bf16_f32 v241, v22, v23
	v_fmac_f32_e32 v250, v20, v20
	v_fmac_f32_e32 v251, v21, v21
	v_fmac_f32_e32 v250, v22, v22
	v_fmac_f32_e32 v251, v23, v23
	global_store_dwordx2 v162, v[240:241], s[70:71] offset:2560
	v_cvt_pk_bf16_f32 v242, v24, v25
	v_cvt_pk_bf16_f32 v243, v26, v27
	v_fmac_f32_e32 v250, v24, v24
	v_fmac_f32_e32 v251, v25, v25
	v_fmac_f32_e32 v250, v26, v26
	v_fmac_f32_e32 v251, v27, v27
	global_store_dwordx2 v162, v[242:243], s[70:71] offset:3072
	v_cvt_pk_bf16_f32 v244, v28, v29
	v_cvt_pk_bf16_f32 v245, v30, v31
	v_fmac_f32_e32 v250, v28, v28
	v_fmac_f32_e32 v251, v29, v29
	v_fmac_f32_e32 v250, v30, v30
	v_fmac_f32_e32 v251, v31, v31
	global_store_dwordx2 v162, v[244:245], s[70:71] offset:3584
	s_add_u32 s70, s70, 0x8000
	s_addc_u32 s71, s71, 0
	v_add_f32_e32 v250, v250, v251
	s_nop 1
	v_add_f32_dpp v218, v250, v250 quad_perm:[1,0,3,2] row_mask:0xf bank_mask:0xf bound_ctrl:1
	s_nop 1
	v_add_f32_dpp v218, v218, v218 quad_perm:[2,3,0,1] row_mask:0xf bank_mask:0xf bound_ctrl:1
	s_nop 1
	v_add_f32_dpp v218, v218, v218 row_ror:4 row_mask:0xf bank_mask:0xf bound_ctrl:1
	s_nop 1
	v_add_f32_dpp v218, v218, v218 row_ror:8 row_mask:0xf bank_mask:0xf bound_ctrl:1
	s_nop 1
	v_readlane_b32 s8, v218, 0
	v_readlane_b32 s9, v218, 16
	v_readlane_b32 s10, v218, 32
	v_readlane_b32 s11, v218, 48
	s_nop 1
	v_mov_b32_e32 v218, s8
	v_add_f32_e32 v218, s9, v218
	v_mov_b32_e32 v219, s10
	v_add_f32_e32 v219, s11, v219
	v_add_f32_e32 v218, v218, v219
	v_mul_f32_e32 v218, 0x3a000000, v218
	v_add_f32_e32 v218, 0x358637bd, v218
	v_rsq_f32_e32 v218, v218
	s_nop 0
	v_mul_f32_e32 v246, v0, v218
	v_mul_f32_e32 v247, v1, v218
	v_mul_f32_e32 v248, v2, v218
	v_mul_f32_e32 v249, v3, v218
	v_fma_f32 v246, v246, v64, v96
	v_fma_f32 v247, v247, v65, v97
	v_fma_f32 v248, v248, v66, v98
	v_fma_f32 v249, v249, v67, v99
	v_cvt_pk_bf16_f32 v238, v246, v247
	v_cvt_pk_bf16_f32 v239, v248, v249
	global_store_dwordx2 v162, v[238:239], s[72:73]
	v_mul_f32_e32 v246, v4, v218
	v_mul_f32_e32 v247, v5, v218
	v_mul_f32_e32 v248, v6, v218
	v_mul_f32_e32 v249, v7, v218
	v_fma_f32 v246, v246, v68, v100
	v_fma_f32 v247, v247, v69, v101
	v_fma_f32 v248, v248, v70, v102
	v_fma_f32 v249, v249, v71, v103
	v_cvt_pk_bf16_f32 v240, v246, v247
	v_cvt_pk_bf16_f32 v241, v248, v249
	global_store_dwordx2 v162, v[240:241], s[72:73] offset:512
	v_mul_f32_e32 v246, v8, v218
	v_mul_f32_e32 v247, v9, v218
	v_mul_f32_e32 v248, v10, v218
	v_mul_f32_e32 v249, v11, v218
	v_fma_f32 v246, v246, v72, v104
	v_fma_f32 v247, v247, v73, v105
	v_fma_f32 v248, v248, v74, v106
	v_fma_f32 v249, v249, v75, v107
	v_cvt_pk_bf16_f32 v242, v246, v247
	v_cvt_pk_bf16_f32 v243, v248, v249
	global_store_dwordx2 v162, v[242:243], s[72:73] offset:1024
	v_mul_f32_e32 v246, v12, v218
	v_mul_f32_e32 v247, v13, v218
	v_mul_f32_e32 v248, v14, v218
	v_mul_f32_e32 v249, v15, v218
	v_fma_f32 v246, v246, v76, v108
	v_fma_f32 v247, v247, v77, v109
	v_fma_f32 v248, v248, v78, v110
	v_fma_f32 v249, v249, v79, v111
	v_cvt_pk_bf16_f32 v244, v246, v247
	v_cvt_pk_bf16_f32 v245, v248, v249
	global_store_dwordx2 v162, v[244:245], s[72:73] offset:1536
	v_mul_f32_e32 v246, v16, v218
	v_mul_f32_e32 v247, v17, v218
	v_mul_f32_e32 v248, v18, v218
	v_mul_f32_e32 v249, v19, v218
	v_fma_f32 v246, v246, v80, v112
	v_fma_f32 v247, v247, v81, v113
	v_fma_f32 v248, v248, v82, v114
	v_fma_f32 v249, v249, v83, v115
	v_cvt_pk_bf16_f32 v238, v246, v247
	v_cvt_pk_bf16_f32 v239, v248, v249
	global_store_dwordx2 v162, v[238:239], s[72:73] offset:2048
	v_mul_f32_e32 v246, v20, v218
	v_mul_f32_e32 v247, v21, v218
	v_mul_f32_e32 v248, v22, v218
	v_mul_f32_e32 v249, v23, v218
	v_fma_f32 v246, v246, v84, v116
	v_fma_f32 v247, v247, v85, v117
	v_fma_f32 v248, v248, v86, v118
	v_fma_f32 v249, v249, v87, v119
	v_cvt_pk_bf16_f32 v240, v246, v247
	v_cvt_pk_bf16_f32 v241, v248, v249
	global_store_dwordx2 v162, v[240:241], s[72:73] offset:2560
	v_mul_f32_e32 v246, v24, v218
	v_mul_f32_e32 v247, v25, v218
	v_mul_f32_e32 v248, v26, v218
	v_mul_f32_e32 v249, v27, v218
	v_fma_f32 v246, v246, v88, v120
	v_fma_f32 v247, v247, v89, v121
	v_fma_f32 v248, v248, v90, v122
	v_fma_f32 v249, v249, v91, v123
	v_cvt_pk_bf16_f32 v242, v246, v247
	v_cvt_pk_bf16_f32 v243, v248, v249
	global_store_dwordx2 v162, v[242:243], s[72:73] offset:3072
	v_mul_f32_e32 v246, v28, v218
	v_mul_f32_e32 v247, v29, v218
	v_mul_f32_e32 v248, v30, v218
	v_mul_f32_e32 v249, v31, v218
	v_fma_f32 v246, v246, v92, v124
	v_fma_f32 v247, v247, v93, v125
	v_fma_f32 v248, v248, v94, v126
	v_fma_f32 v249, v249, v95, v127
	v_cvt_pk_bf16_f32 v244, v246, v247
	v_cvt_pk_bf16_f32 v245, v248, v249
	global_store_dwordx2 v162, v[244:245], s[72:73] offset:3584
	s_add_u32 s72, s72, 0x8000
	s_addc_u32 s73, s73, 0
	s_waitcnt vmcnt(32)
	v_mov_b32_e32 v250, 0
	v_mov_b32_e32 v251, 0
	v_lshlrev_b32_e32 v246, 16, v166
	v_and_b32_e32 v247, 0xffff0000, v166
	v_lshlrev_b32_e32 v248, 16, v167
	v_and_b32_e32 v249, 0xffff0000, v167
	v_fmac_f32_e32 v250, v246, v246
	v_fmac_f32_e32 v251, v247, v247
	v_fmac_f32_e32 v250, v248, v248
	v_fmac_f32_e32 v251, v249, v249
	v_lshlrev_b32_e32 v246, 16, v168
	v_and_b32_e32 v247, 0xffff0000, v168
	v_lshlrev_b32_e32 v248, 16, v169
	v_and_b32_e32 v249, 0xffff0000, v169
	v_fmac_f32_e32 v250, v246, v246
	v_fmac_f32_e32 v251, v247, v247
	v_fmac_f32_e32 v250, v248, v248
	v_fmac_f32_e32 v251, v249, v249
	v_lshlrev_b32_e32 v246, 16, v170
	v_and_b32_e32 v247, 0xffff0000, v170
	v_lshlrev_b32_e32 v248, 16, v171
	v_and_b32_e32 v249, 0xffff0000, v171
	v_fmac_f32_e32 v250, v246, v246
	v_fmac_f32_e32 v251, v247, v247
	v_fmac_f32_e32 v250, v248, v248
	v_fmac_f32_e32 v251, v249, v249
	v_lshlrev_b32_e32 v246, 16, v172
	v_and_b32_e32 v247, 0xffff0000, v172
	v_lshlrev_b32_e32 v248, 16, v173
	v_and_b32_e32 v249, 0xffff0000, v173
	v_fmac_f32_e32 v250, v246, v246
	v_fmac_f32_e32 v251, v247, v247
	v_fmac_f32_e32 v250, v248, v248
	v_fmac_f32_e32 v251, v249, v249
	v_lshlrev_b32_e32 v246, 16, v174
	v_and_b32_e32 v247, 0xffff0000, v174
	v_lshlrev_b32_e32 v248, 16, v175
	v_and_b32_e32 v249, 0xffff0000, v175
	v_fmac_f32_e32 v250, v246, v246
	v_fmac_f32_e32 v251, v247, v247
	v_fmac_f32_e32 v250, v248, v248
	v_fmac_f32_e32 v251, v249, v249
	v_lshlrev_b32_e32 v246, 16, v176
	v_and_b32_e32 v247, 0xffff0000, v176
	v_lshlrev_b32_e32 v248, 16, v177
	v_and_b32_e32 v249, 0xffff0000, v177
	v_fmac_f32_e32 v250, v246, v246
	v_fmac_f32_e32 v251, v247, v247
	v_fmac_f32_e32 v250, v248, v248
	v_fmac_f32_e32 v251, v249, v249
	v_lshlrev_b32_e32 v246, 16, v178
	v_and_b32_e32 v247, 0xffff0000, v178
	v_lshlrev_b32_e32 v248, 16, v179
	v_and_b32_e32 v249, 0xffff0000, v179
	v_fmac_f32_e32 v250, v246, v246
	v_fmac_f32_e32 v251, v247, v247
	v_fmac_f32_e32 v250, v248, v248
	v_fmac_f32_e32 v251, v249, v249
	v_lshlrev_b32_e32 v246, 16, v180
	v_and_b32_e32 v247, 0xffff0000, v180
	v_lshlrev_b32_e32 v248, 16, v181
	v_and_b32_e32 v249, 0xffff0000, v181
	v_fmac_f32_e32 v250, v246, v246
	v_fmac_f32_e32 v251, v247, v247
	v_fmac_f32_e32 v250, v248, v248
	v_fmac_f32_e32 v251, v249, v249
	v_add_f32_e32 v250, v250, v251
	s_nop 1
	v_add_f32_dpp v218, v250, v250 quad_perm:[1,0,3,2] row_mask:0xf bank_mask:0xf bound_ctrl:1
	s_nop 1
	v_add_f32_dpp v218, v218, v218 quad_perm:[2,3,0,1] row_mask:0xf bank_mask:0xf bound_ctrl:1
	s_nop 1
	v_add_f32_dpp v218, v218, v218 row_ror:4 row_mask:0xf bank_mask:0xf bound_ctrl:1
	s_nop 1
	v_add_f32_dpp v218, v218, v218 row_ror:8 row_mask:0xf bank_mask:0xf bound_ctrl:1
	s_nop 1
	v_readlane_b32 s8, v218, 0
	v_readlane_b32 s9, v218, 16
	v_readlane_b32 s10, v218, 32
	v_readlane_b32 s11, v218, 48
	s_nop 1
	v_mov_b32_e32 v218, s8
	v_add_f32_e32 v218, s9, v218
	v_mov_b32_e32 v219, s10
	v_add_f32_e32 v219, s11, v219
	v_add_f32_e32 v218, v218, v219
	v_mul_f32_e32 v218, 0x3a000000, v218
	v_add_f32_e32 v218, 0x358637bd, v218
	v_rsq_f32_e32 v218, v218
	s_nop 0
	v_lshlrev_b32_e32 v246, 16, v166
	v_and_b32_e32 v247, 0xffff0000, v166
	v_lshlrev_b32_e32 v248, 16, v167
	v_and_b32_e32 v249, 0xffff0000, v167
	v_mul_f32_e32 v246, v246, v218
	v_mul_f32_e32 v247, v247, v218
	v_mul_f32_e32 v248, v248, v218
	v_mul_f32_e32 v249, v249, v218
	v_lshlrev_b32_e32 v0, 16, v182
	v_and_b32_e32 v1, 0xffff0000, v182
	v_lshlrev_b32_e32 v2, 16, v183
	v_and_b32_e32 v3, 0xffff0000, v183
	v_fmac_f32_e32 v0, v246, v32
	v_fmac_f32_e32 v1, v247, v33
	v_fmac_f32_e32 v2, v248, v34
	v_fmac_f32_e32 v3, v249, v35
	v_lshlrev_b32_e32 v246, 16, v168
	v_and_b32_e32 v247, 0xffff0000, v168
	v_lshlrev_b32_e32 v248, 16, v169
	v_and_b32_e32 v249, 0xffff0000, v169
	v_mul_f32_e32 v246, v246, v218
	v_mul_f32_e32 v247, v247, v218
	v_mul_f32_e32 v248, v248, v218
	v_mul_f32_e32 v249, v249, v218
	v_lshlrev_b32_e32 v4, 16, v184
	v_and_b32_e32 v5, 0xffff0000, v184
	v_lshlrev_b32_e32 v6, 16, v185
	v_and_b32_e32 v7, 0xffff0000, v185
	v_fmac_f32_e32 v4, v246, v36
	v_fmac_f32_e32 v5, v247, v37
	v_fmac_f32_e32 v6, v248, v38
	v_fmac_f32_e32 v7, v249, v39
	v_lshlrev_b32_e32 v246, 16, v170
	v_and_b32_e32 v247, 0xffff0000, v170
	v_lshlrev_b32_e32 v248, 16, v171
	v_and_b32_e32 v249, 0xffff0000, v171
	v_mul_f32_e32 v246, v246, v218
	v_mul_f32_e32 v247, v247, v218
	v_mul_f32_e32 v248, v248, v218
	v_mul_f32_e32 v249, v249, v218
	v_lshlrev_b32_e32 v8, 16, v186
	v_and_b32_e32 v9, 0xffff0000, v186
	v_lshlrev_b32_e32 v10, 16, v187
	v_and_b32_e32 v11, 0xffff0000, v187
	v_fmac_f32_e32 v8, v246, v40
	v_fmac_f32_e32 v9, v247, v41
	v_fmac_f32_e32 v10, v248, v42
	v_fmac_f32_e32 v11, v249, v43
	v_lshlrev_b32_e32 v246, 16, v172
	v_and_b32_e32 v247, 0xffff0000, v172
	v_lshlrev_b32_e32 v248, 16, v173
	v_and_b32_e32 v249, 0xffff0000, v173
	v_mul_f32_e32 v246, v246, v218
	v_mul_f32_e32 v247, v247, v218
	v_mul_f32_e32 v248, v248, v218
	v_mul_f32_e32 v249, v249, v218
	v_lshlrev_b32_e32 v12, 16, v188
	v_and_b32_e32 v13, 0xffff0000, v188
	v_lshlrev_b32_e32 v14, 16, v189
	v_and_b32_e32 v15, 0xffff0000, v189
	v_fmac_f32_e32 v12, v246, v44
	v_fmac_f32_e32 v13, v247, v45
	v_fmac_f32_e32 v14, v248, v46
	v_fmac_f32_e32 v15, v249, v47
	v_lshlrev_b32_e32 v246, 16, v174
	v_and_b32_e32 v247, 0xffff0000, v174
	v_lshlrev_b32_e32 v248, 16, v175
	v_and_b32_e32 v249, 0xffff0000, v175
	v_mul_f32_e32 v246, v246, v218
	v_mul_f32_e32 v247, v247, v218
	v_mul_f32_e32 v248, v248, v218
	v_mul_f32_e32 v249, v249, v218
	v_lshlrev_b32_e32 v16, 16, v190
	v_and_b32_e32 v17, 0xffff0000, v190
	v_lshlrev_b32_e32 v18, 16, v191
	v_and_b32_e32 v19, 0xffff0000, v191
	v_fmac_f32_e32 v16, v246, v48
	v_fmac_f32_e32 v17, v247, v49
	v_fmac_f32_e32 v18, v248, v50
	v_fmac_f32_e32 v19, v249, v51
	v_lshlrev_b32_e32 v246, 16, v176
	v_and_b32_e32 v247, 0xffff0000, v176
	v_lshlrev_b32_e32 v248, 16, v177
	v_and_b32_e32 v249, 0xffff0000, v177
	v_mul_f32_e32 v246, v246, v218
	v_mul_f32_e32 v247, v247, v218
	v_mul_f32_e32 v248, v248, v218
	v_mul_f32_e32 v249, v249, v218
	v_lshlrev_b32_e32 v20, 16, v192
	v_and_b32_e32 v21, 0xffff0000, v192
	v_lshlrev_b32_e32 v22, 16, v193
	v_and_b32_e32 v23, 0xffff0000, v193
	v_fmac_f32_e32 v20, v246, v52
	v_fmac_f32_e32 v21, v247, v53
	v_fmac_f32_e32 v22, v248, v54
	v_fmac_f32_e32 v23, v249, v55
	v_lshlrev_b32_e32 v246, 16, v178
	v_and_b32_e32 v247, 0xffff0000, v178
	v_lshlrev_b32_e32 v248, 16, v179
	v_and_b32_e32 v249, 0xffff0000, v179
	v_mul_f32_e32 v246, v246, v218
	v_mul_f32_e32 v247, v247, v218
	v_mul_f32_e32 v248, v248, v218
	v_mul_f32_e32 v249, v249, v218
	v_lshlrev_b32_e32 v24, 16, v194
	v_and_b32_e32 v25, 0xffff0000, v194
	v_lshlrev_b32_e32 v26, 16, v195
	v_and_b32_e32 v27, 0xffff0000, v195
	v_fmac_f32_e32 v24, v246, v56
	v_fmac_f32_e32 v25, v247, v57
	v_fmac_f32_e32 v26, v248, v58
	v_fmac_f32_e32 v27, v249, v59
	v_lshlrev_b32_e32 v246, 16, v180
	v_and_b32_e32 v247, 0xffff0000, v180
	v_lshlrev_b32_e32 v248, 16, v181
	v_and_b32_e32 v249, 0xffff0000, v181
	v_mul_f32_e32 v246, v246, v218
	v_mul_f32_e32 v247, v247, v218
	v_mul_f32_e32 v248, v248, v218
	v_mul_f32_e32 v249, v249, v218
	v_lshlrev_b32_e32 v28, 16, v196
	v_and_b32_e32 v29, 0xffff0000, v196
	v_lshlrev_b32_e32 v30, 16, v197
	v_and_b32_e32 v31, 0xffff0000, v197
	v_fmac_f32_e32 v28, v246, v60
	v_fmac_f32_e32 v29, v247, v61
	v_fmac_f32_e32 v30, v248, v62
	v_fmac_f32_e32 v31, v249, v63
	global_load_dwordx2 v[166:167], v162, s[56:57] nt
	global_load_dwordx2 v[168:169], v162, s[56:57] offset:512 nt
	global_load_dwordx2 v[170:171], v162, s[56:57] offset:1024 nt
	global_load_dwordx2 v[172:173], v162, s[56:57] offset:1536 nt
	global_load_dwordx2 v[174:175], v162, s[56:57] offset:2048 nt
	global_load_dwordx2 v[176:177], v162, s[56:57] offset:2560 nt
	global_load_dwordx2 v[178:179], v162, s[56:57] offset:3072 nt
	global_load_dwordx2 v[180:181], v162, s[56:57] offset:3584 nt
	global_load_dwordx2 v[182:183], v162, s[58:59] nt
	global_load_dwordx2 v[184:185], v162, s[58:59] offset:512 nt
	global_load_dwordx2 v[186:187], v162, s[58:59] offset:1024 nt
	global_load_dwordx2 v[188:189], v162, s[58:59] offset:1536 nt
	global_load_dwordx2 v[190:191], v162, s[58:59] offset:2048 nt
	global_load_dwordx2 v[192:193], v162, s[58:59] offset:2560 nt
	global_load_dwordx2 v[194:195], v162, s[58:59] offset:3072 nt
	global_load_dwordx2 v[196:197], v162, s[58:59] offset:3584 nt
	s_add_u32 s58, s58, 0x8000
	s_addc_u32 s59, s59, 0
	s_add_u32 s56, s56, 0x8000
	s_addc_u32 s57, s57, 0
	v_mov_b32_e32 v250, 0
	v_mov_b32_e32 v251, 0
	v_cvt_pk_bf16_f32 v238, v0, v1
	v_cvt_pk_bf16_f32 v239, v2, v3
	v_fmac_f32_e32 v250, v0, v0
	v_fmac_f32_e32 v251, v1, v1
	v_fmac_f32_e32 v250, v2, v2
	v_fmac_f32_e32 v251, v3, v3
	global_store_dwordx2 v162, v[238:239], s[70:71]
	v_cvt_pk_bf16_f32 v240, v4, v5
	v_cvt_pk_bf16_f32 v241, v6, v7
	v_fmac_f32_e32 v250, v4, v4
	v_fmac_f32_e32 v251, v5, v5
	v_fmac_f32_e32 v250, v6, v6
	v_fmac_f32_e32 v251, v7, v7
	global_store_dwordx2 v162, v[240:241], s[70:71] offset:512
	v_cvt_pk_bf16_f32 v242, v8, v9
	v_cvt_pk_bf16_f32 v243, v10, v11
	v_fmac_f32_e32 v250, v8, v8
	v_fmac_f32_e32 v251, v9, v9
	v_fmac_f32_e32 v250, v10, v10
	v_fmac_f32_e32 v251, v11, v11
	global_store_dwordx2 v162, v[242:243], s[70:71] offset:1024
	v_cvt_pk_bf16_f32 v244, v12, v13
	v_cvt_pk_bf16_f32 v245, v14, v15
	v_fmac_f32_e32 v250, v12, v12
	v_fmac_f32_e32 v251, v13, v13
	v_fmac_f32_e32 v250, v14, v14
	v_fmac_f32_e32 v251, v15, v15
	global_store_dwordx2 v162, v[244:245], s[70:71] offset:1536
	v_cvt_pk_bf16_f32 v238, v16, v17
	v_cvt_pk_bf16_f32 v239, v18, v19
	v_fmac_f32_e32 v250, v16, v16
	v_fmac_f32_e32 v251, v17, v17
	v_fmac_f32_e32 v250, v18, v18
	v_fmac_f32_e32 v251, v19, v19
	global_store_dwordx2 v162, v[238:239], s[70:71] offset:2048
	v_cvt_pk_bf16_f32 v240, v20, v21
	v_cvt_pk_bf16_f32 v241, v22, v23
	v_fmac_f32_e32 v250, v20, v20
	v_fmac_f32_e32 v251, v21, v21
	v_fmac_f32_e32 v250, v22, v22
	v_fmac_f32_e32 v251, v23, v23
	global_store_dwordx2 v162, v[240:241], s[70:71] offset:2560
	v_cvt_pk_bf16_f32 v242, v24, v25
	v_cvt_pk_bf16_f32 v243, v26, v27
	v_fmac_f32_e32 v250, v24, v24
	v_fmac_f32_e32 v251, v25, v25
	v_fmac_f32_e32 v250, v26, v26
	v_fmac_f32_e32 v251, v27, v27
	global_store_dwordx2 v162, v[242:243], s[70:71] offset:3072
	v_cvt_pk_bf16_f32 v244, v28, v29
	v_cvt_pk_bf16_f32 v245, v30, v31
	v_fmac_f32_e32 v250, v28, v28
	v_fmac_f32_e32 v251, v29, v29
	v_fmac_f32_e32 v250, v30, v30
	v_fmac_f32_e32 v251, v31, v31
	global_store_dwordx2 v162, v[244:245], s[70:71] offset:3584
	s_add_u32 s70, s70, 0x8000
	s_addc_u32 s71, s71, 0
	v_add_f32_e32 v250, v250, v251
	s_nop 1
	v_add_f32_dpp v218, v250, v250 quad_perm:[1,0,3,2] row_mask:0xf bank_mask:0xf bound_ctrl:1
	s_nop 1
	v_add_f32_dpp v218, v218, v218 quad_perm:[2,3,0,1] row_mask:0xf bank_mask:0xf bound_ctrl:1
	s_nop 1
	v_add_f32_dpp v218, v218, v218 row_ror:4 row_mask:0xf bank_mask:0xf bound_ctrl:1
	s_nop 1
	v_add_f32_dpp v218, v218, v218 row_ror:8 row_mask:0xf bank_mask:0xf bound_ctrl:1
	s_nop 1
	v_readlane_b32 s8, v218, 0
	v_readlane_b32 s9, v218, 16
	v_readlane_b32 s10, v218, 32
	v_readlane_b32 s11, v218, 48
	s_nop 1
	v_mov_b32_e32 v218, s8
	v_add_f32_e32 v218, s9, v218
	v_mov_b32_e32 v219, s10
	v_add_f32_e32 v219, s11, v219
	v_add_f32_e32 v218, v218, v219
	v_mul_f32_e32 v218, 0x3a000000, v218
	v_add_f32_e32 v218, 0x358637bd, v218
	v_rsq_f32_e32 v218, v218
	s_nop 0
	v_mul_f32_e32 v246, v0, v218
	v_mul_f32_e32 v247, v1, v218
	v_mul_f32_e32 v248, v2, v218
	v_mul_f32_e32 v249, v3, v218
	v_fma_f32 v246, v246, v64, v96
	v_fma_f32 v247, v247, v65, v97
	v_fma_f32 v248, v248, v66, v98
	v_fma_f32 v249, v249, v67, v99
	v_cvt_pk_bf16_f32 v238, v246, v247
	v_cvt_pk_bf16_f32 v239, v248, v249
	global_store_dwordx2 v162, v[238:239], s[72:73]
	v_mul_f32_e32 v246, v4, v218
	v_mul_f32_e32 v247, v5, v218
	v_mul_f32_e32 v248, v6, v218
	v_mul_f32_e32 v249, v7, v218
	v_fma_f32 v246, v246, v68, v100
	v_fma_f32 v247, v247, v69, v101
	v_fma_f32 v248, v248, v70, v102
	v_fma_f32 v249, v249, v71, v103
	v_cvt_pk_bf16_f32 v240, v246, v247
	v_cvt_pk_bf16_f32 v241, v248, v249
	global_store_dwordx2 v162, v[240:241], s[72:73] offset:512
	v_mul_f32_e32 v246, v8, v218
	v_mul_f32_e32 v247, v9, v218
	v_mul_f32_e32 v248, v10, v218
	v_mul_f32_e32 v249, v11, v218
	v_fma_f32 v246, v246, v72, v104
	v_fma_f32 v247, v247, v73, v105
	v_fma_f32 v248, v248, v74, v106
	v_fma_f32 v249, v249, v75, v107
	v_cvt_pk_bf16_f32 v242, v246, v247
	v_cvt_pk_bf16_f32 v243, v248, v249
	global_store_dwordx2 v162, v[242:243], s[72:73] offset:1024
	v_mul_f32_e32 v246, v12, v218
	v_mul_f32_e32 v247, v13, v218
	v_mul_f32_e32 v248, v14, v218
	v_mul_f32_e32 v249, v15, v218
	v_fma_f32 v246, v246, v76, v108
	v_fma_f32 v247, v247, v77, v109
	v_fma_f32 v248, v248, v78, v110
	v_fma_f32 v249, v249, v79, v111
	v_cvt_pk_bf16_f32 v244, v246, v247
	v_cvt_pk_bf16_f32 v245, v248, v249
	global_store_dwordx2 v162, v[244:245], s[72:73] offset:1536
	v_mul_f32_e32 v246, v16, v218
	v_mul_f32_e32 v247, v17, v218
	v_mul_f32_e32 v248, v18, v218
	v_mul_f32_e32 v249, v19, v218
	v_fma_f32 v246, v246, v80, v112
	v_fma_f32 v247, v247, v81, v113
	v_fma_f32 v248, v248, v82, v114
	v_fma_f32 v249, v249, v83, v115
	v_cvt_pk_bf16_f32 v238, v246, v247
	v_cvt_pk_bf16_f32 v239, v248, v249
	global_store_dwordx2 v162, v[238:239], s[72:73] offset:2048
	v_mul_f32_e32 v246, v20, v218
	v_mul_f32_e32 v247, v21, v218
	v_mul_f32_e32 v248, v22, v218
	v_mul_f32_e32 v249, v23, v218
	v_fma_f32 v246, v246, v84, v116
	v_fma_f32 v247, v247, v85, v117
	v_fma_f32 v248, v248, v86, v118
	v_fma_f32 v249, v249, v87, v119
	v_cvt_pk_bf16_f32 v240, v246, v247
	v_cvt_pk_bf16_f32 v241, v248, v249
	global_store_dwordx2 v162, v[240:241], s[72:73] offset:2560
	v_mul_f32_e32 v246, v24, v218
	v_mul_f32_e32 v247, v25, v218
	v_mul_f32_e32 v248, v26, v218
	v_mul_f32_e32 v249, v27, v218
	v_fma_f32 v246, v246, v88, v120
	v_fma_f32 v247, v247, v89, v121
	v_fma_f32 v248, v248, v90, v122
	v_fma_f32 v249, v249, v91, v123
	v_cvt_pk_bf16_f32 v242, v246, v247
	v_cvt_pk_bf16_f32 v243, v248, v249
	global_store_dwordx2 v162, v[242:243], s[72:73] offset:3072
	v_mul_f32_e32 v246, v28, v218
	v_mul_f32_e32 v247, v29, v218
	v_mul_f32_e32 v248, v30, v218
	v_mul_f32_e32 v249, v31, v218
	v_fma_f32 v246, v246, v92, v124
	v_fma_f32 v247, v247, v93, v125
	v_fma_f32 v248, v248, v94, v126
	v_fma_f32 v249, v249, v95, v127
	v_cvt_pk_bf16_f32 v244, v246, v247
	v_cvt_pk_bf16_f32 v245, v248, v249
	global_store_dwordx2 v162, v[244:245], s[72:73] offset:3584
	s_add_u32 s72, s72, 0x8000
	s_addc_u32 s73, s73, 0
	s_add_u32 s76, s76, 1
	s_cmp_lt_u32 s76, 7
	s_cbranch_scc1 .Lmp_V1_loop
	s_waitcnt vmcnt(32)
	v_mov_b32_e32 v250, 0
	v_mov_b32_e32 v251, 0
	v_lshlrev_b32_e32 v246, 16, v128
	v_and_b32_e32 v247, 0xffff0000, v128
	v_lshlrev_b32_e32 v248, 16, v129
	v_and_b32_e32 v249, 0xffff0000, v129
	v_fmac_f32_e32 v250, v246, v246
	v_fmac_f32_e32 v251, v247, v247
	v_fmac_f32_e32 v250, v248, v248
	v_fmac_f32_e32 v251, v249, v249
	v_lshlrev_b32_e32 v246, 16, v130
	v_and_b32_e32 v247, 0xffff0000, v130
	v_lshlrev_b32_e32 v248, 16, v131
	v_and_b32_e32 v249, 0xffff0000, v131
	v_fmac_f32_e32 v250, v246, v246
	v_fmac_f32_e32 v251, v247, v247
	v_fmac_f32_e32 v250, v248, v248
	v_fmac_f32_e32 v251, v249, v249
	v_lshlrev_b32_e32 v246, 16, v132
	v_and_b32_e32 v247, 0xffff0000, v132
	v_lshlrev_b32_e32 v248, 16, v133
	v_and_b32_e32 v249, 0xffff0000, v133
	v_fmac_f32_e32 v250, v246, v246
	v_fmac_f32_e32 v251, v247, v247
	v_fmac_f32_e32 v250, v248, v248
	v_fmac_f32_e32 v251, v249, v249
	v_lshlrev_b32_e32 v246, 16, v134
	v_and_b32_e32 v247, 0xffff0000, v134
	v_lshlrev_b32_e32 v248, 16, v135
	v_and_b32_e32 v249, 0xffff0000, v135
	v_fmac_f32_e32 v250, v246, v246
	v_fmac_f32_e32 v251, v247, v247
	v_fmac_f32_e32 v250, v248, v248
	v_fmac_f32_e32 v251, v249, v249
	v_lshlrev_b32_e32 v246, 16, v136
	v_and_b32_e32 v247, 0xffff0000, v136
	v_lshlrev_b32_e32 v248, 16, v137
	v_and_b32_e32 v249, 0xffff0000, v137
	v_fmac_f32_e32 v250, v246, v246
	v_fmac_f32_e32 v251, v247, v247
	v_fmac_f32_e32 v250, v248, v248
	v_fmac_f32_e32 v251, v249, v249
	v_lshlrev_b32_e32 v246, 16, v138
	v_and_b32_e32 v247, 0xffff0000, v138
	v_lshlrev_b32_e32 v248, 16, v139
	v_and_b32_e32 v249, 0xffff0000, v139
	v_fmac_f32_e32 v250, v246, v246
	v_fmac_f32_e32 v251, v247, v247
	v_fmac_f32_e32 v250, v248, v248
	v_fmac_f32_e32 v251, v249, v249
	v_lshlrev_b32_e32 v246, 16, v140
	v_and_b32_e32 v247, 0xffff0000, v140
	v_lshlrev_b32_e32 v248, 16, v141
	v_and_b32_e32 v249, 0xffff0000, v141
	v_fmac_f32_e32 v250, v246, v246
	v_fmac_f32_e32 v251, v247, v247
	v_fmac_f32_e32 v250, v248, v248
	v_fmac_f32_e32 v251, v249, v249
	v_lshlrev_b32_e32 v246, 16, v142
	v_and_b32_e32 v247, 0xffff0000, v142
	v_lshlrev_b32_e32 v248, 16, v143
	v_and_b32_e32 v249, 0xffff0000, v143
	v_fmac_f32_e32 v250, v246, v246
	v_fmac_f32_e32 v251, v247, v247
	v_fmac_f32_e32 v250, v248, v248
	v_fmac_f32_e32 v251, v249, v249
	v_add_f32_e32 v250, v250, v251
	s_nop 1
	v_add_f32_dpp v218, v250, v250 quad_perm:[1,0,3,2] row_mask:0xf bank_mask:0xf bound_ctrl:1
	s_nop 1
	v_add_f32_dpp v218, v218, v218 quad_perm:[2,3,0,1] row_mask:0xf bank_mask:0xf bound_ctrl:1
	s_nop 1
	v_add_f32_dpp v218, v218, v218 row_ror:4 row_mask:0xf bank_mask:0xf bound_ctrl:1
	s_nop 1
	v_add_f32_dpp v218, v218, v218 row_ror:8 row_mask:0xf bank_mask:0xf bound_ctrl:1
	s_nop 1
	v_readlane_b32 s8, v218, 0
	v_readlane_b32 s9, v218, 16
	v_readlane_b32 s10, v218, 32
	v_readlane_b32 s11, v218, 48
	s_nop 1
	v_mov_b32_e32 v218, s8
	v_add_f32_e32 v218, s9, v218
	v_mov_b32_e32 v219, s10
	v_add_f32_e32 v219, s11, v219
	v_add_f32_e32 v218, v218, v219
	v_mul_f32_e32 v218, 0x3a000000, v218
	v_add_f32_e32 v218, 0x358637bd, v218
	v_rsq_f32_e32 v218, v218
	s_nop 0
	v_lshlrev_b32_e32 v246, 16, v128
	v_and_b32_e32 v247, 0xffff0000, v128
	v_lshlrev_b32_e32 v248, 16, v129
	v_and_b32_e32 v249, 0xffff0000, v129
	v_mul_f32_e32 v246, v246, v218
	v_mul_f32_e32 v247, v247, v218
	v_mul_f32_e32 v248, v248, v218
	v_mul_f32_e32 v249, v249, v218
	v_lshlrev_b32_e32 v0, 16, v144
	v_and_b32_e32 v1, 0xffff0000, v144
	v_lshlrev_b32_e32 v2, 16, v145
	v_and_b32_e32 v3, 0xffff0000, v145
	v_fmac_f32_e32 v0, v246, v32
	v_fmac_f32_e32 v1, v247, v33
	v_fmac_f32_e32 v2, v248, v34
	v_fmac_f32_e32 v3, v249, v35
	v_lshlrev_b32_e32 v246, 16, v130
	v_and_b32_e32 v247, 0xffff0000, v130
	v_lshlrev_b32_e32 v248, 16, v131
	v_and_b32_e32 v249, 0xffff0000, v131
	v_mul_f32_e32 v246, v246, v218
	v_mul_f32_e32 v247, v247, v218
	v_mul_f32_e32 v248, v248, v218
	v_mul_f32_e32 v249, v249, v218
	v_lshlrev_b32_e32 v4, 16, v146
	v_and_b32_e32 v5, 0xffff0000, v146
	v_lshlrev_b32_e32 v6, 16, v147
	v_and_b32_e32 v7, 0xffff0000, v147
	v_fmac_f32_e32 v4, v246, v36
	v_fmac_f32_e32 v5, v247, v37
	v_fmac_f32_e32 v6, v248, v38
	v_fmac_f32_e32 v7, v249, v39
	v_lshlrev_b32_e32 v246, 16, v132
	v_and_b32_e32 v247, 0xffff0000, v132
	v_lshlrev_b32_e32 v248, 16, v133
	v_and_b32_e32 v249, 0xffff0000, v133
	v_mul_f32_e32 v246, v246, v218
	v_mul_f32_e32 v247, v247, v218
	v_mul_f32_e32 v248, v248, v218
	v_mul_f32_e32 v249, v249, v218
	v_lshlrev_b32_e32 v8, 16, v148
	v_and_b32_e32 v9, 0xffff0000, v148
	v_lshlrev_b32_e32 v10, 16, v149
	v_and_b32_e32 v11, 0xffff0000, v149
	v_fmac_f32_e32 v8, v246, v40
	v_fmac_f32_e32 v9, v247, v41
	v_fmac_f32_e32 v10, v248, v42
	v_fmac_f32_e32 v11, v249, v43
	v_lshlrev_b32_e32 v246, 16, v134
	v_and_b32_e32 v247, 0xffff0000, v134
	v_lshlrev_b32_e32 v248, 16, v135
	v_and_b32_e32 v249, 0xffff0000, v135
	v_mul_f32_e32 v246, v246, v218
	v_mul_f32_e32 v247, v247, v218
	v_mul_f32_e32 v248, v248, v218
	v_mul_f32_e32 v249, v249, v218
	v_lshlrev_b32_e32 v12, 16, v150
	v_and_b32_e32 v13, 0xffff0000, v150
	v_lshlrev_b32_e32 v14, 16, v151
	v_and_b32_e32 v15, 0xffff0000, v151
	v_fmac_f32_e32 v12, v246, v44
	v_fmac_f32_e32 v13, v247, v45
	v_fmac_f32_e32 v14, v248, v46
	v_fmac_f32_e32 v15, v249, v47
	v_lshlrev_b32_e32 v246, 16, v136
	v_and_b32_e32 v247, 0xffff0000, v136
	v_lshlrev_b32_e32 v248, 16, v137
	v_and_b32_e32 v249, 0xffff0000, v137
	v_mul_f32_e32 v246, v246, v218
	v_mul_f32_e32 v247, v247, v218
	v_mul_f32_e32 v248, v248, v218
	v_mul_f32_e32 v249, v249, v218
	v_lshlrev_b32_e32 v16, 16, v152
	v_and_b32_e32 v17, 0xffff0000, v152
	v_lshlrev_b32_e32 v18, 16, v153
	v_and_b32_e32 v19, 0xffff0000, v153
	v_fmac_f32_e32 v16, v246, v48
	v_fmac_f32_e32 v17, v247, v49
	v_fmac_f32_e32 v18, v248, v50
	v_fmac_f32_e32 v19, v249, v51
	v_lshlrev_b32_e32 v246, 16, v138
	v_and_b32_e32 v247, 0xffff0000, v138
	v_lshlrev_b32_e32 v248, 16, v139
	v_and_b32_e32 v249, 0xffff0000, v139
	v_mul_f32_e32 v246, v246, v218
	v_mul_f32_e32 v247, v247, v218
	v_mul_f32_e32 v248, v248, v218
	v_mul_f32_e32 v249, v249, v218
	v_lshlrev_b32_e32 v20, 16, v154
	v_and_b32_e32 v21, 0xffff0000, v154
	v_lshlrev_b32_e32 v22, 16, v155
	v_and_b32_e32 v23, 0xffff0000, v155
	v_fmac_f32_e32 v20, v246, v52
	v_fmac_f32_e32 v21, v247, v53
	v_fmac_f32_e32 v22, v248, v54
	v_fmac_f32_e32 v23, v249, v55
	v_lshlrev_b32_e32 v246, 16, v140
	v_and_b32_e32 v247, 0xffff0000, v140
	v_lshlrev_b32_e32 v248, 16, v141
	v_and_b32_e32 v249, 0xffff0000, v141
	v_mul_f32_e32 v246, v246, v218
	v_mul_f32_e32 v247, v247, v218
	v_mul_f32_e32 v248, v248, v218
	v_mul_f32_e32 v249, v249, v218
	v_lshlrev_b32_e32 v24, 16, v156
	v_and_b32_e32 v25, 0xffff0000, v156
	v_lshlrev_b32_e32 v26, 16, v157
	v_and_b32_e32 v27, 0xffff0000, v157
	v_fmac_f32_e32 v24, v246, v56
	v_fmac_f32_e32 v25, v247, v57
	v_fmac_f32_e32 v26, v248, v58
	v_fmac_f32_e32 v27, v249, v59
	v_lshlrev_b32_e32 v246, 16, v142
	v_and_b32_e32 v247, 0xffff0000, v142
	v_lshlrev_b32_e32 v248, 16, v143
	v_and_b32_e32 v249, 0xffff0000, v143
	v_mul_f32_e32 v246, v246, v218
	v_mul_f32_e32 v247, v247, v218
	v_mul_f32_e32 v248, v248, v218
	v_mul_f32_e32 v249, v249, v218
	v_lshlrev_b32_e32 v28, 16, v158
	v_and_b32_e32 v29, 0xffff0000, v158
	v_lshlrev_b32_e32 v30, 16, v159
	v_and_b32_e32 v31, 0xffff0000, v159
	v_fmac_f32_e32 v28, v246, v60
	v_fmac_f32_e32 v29, v247, v61
	v_fmac_f32_e32 v30, v248, v62
	v_fmac_f32_e32 v31, v249, v63
	v_mov_b32_e32 v250, 0
	v_mov_b32_e32 v251, 0
	v_cvt_pk_bf16_f32 v238, v0, v1
	v_cvt_pk_bf16_f32 v239, v2, v3
	v_fmac_f32_e32 v250, v0, v0
	v_fmac_f32_e32 v251, v1, v1
	v_fmac_f32_e32 v250, v2, v2
	v_fmac_f32_e32 v251, v3, v3
	global_store_dwordx2 v162, v[238:239], s[70:71]
	v_cvt_pk_bf16_f32 v240, v4, v5
	v_cvt_pk_bf16_f32 v241, v6, v7
	v_fmac_f32_e32 v250, v4, v4
	v_fmac_f32_e32 v251, v5, v5
	v_fmac_f32_e32 v250, v6, v6
	v_fmac_f32_e32 v251, v7, v7
	global_store_dwordx2 v162, v[240:241], s[70:71] offset:512
	v_cvt_pk_bf16_f32 v242, v8, v9
	v_cvt_pk_bf16_f32 v243, v10, v11
	v_fmac_f32_e32 v250, v8, v8
	v_fmac_f32_e32 v251, v9, v9
	v_fmac_f32_e32 v250, v10, v10
	v_fmac_f32_e32 v251, v11, v11
	global_store_dwordx2 v162, v[242:243], s[70:71] offset:1024
	v_cvt_pk_bf16_f32 v244, v12, v13
	v_cvt_pk_bf16_f32 v245, v14, v15
	v_fmac_f32_e32 v250, v12, v12
	v_fmac_f32_e32 v251, v13, v13
	v_fmac_f32_e32 v250, v14, v14
	v_fmac_f32_e32 v251, v15, v15
	global_store_dwordx2 v162, v[244:245], s[70:71] offset:1536
	v_cvt_pk_bf16_f32 v238, v16, v17
	v_cvt_pk_bf16_f32 v239, v18, v19
	v_fmac_f32_e32 v250, v16, v16
	v_fmac_f32_e32 v251, v17, v17
	v_fmac_f32_e32 v250, v18, v18
	v_fmac_f32_e32 v251, v19, v19
	global_store_dwordx2 v162, v[238:239], s[70:71] offset:2048
	v_cvt_pk_bf16_f32 v240, v20, v21
	v_cvt_pk_bf16_f32 v241, v22, v23
	v_fmac_f32_e32 v250, v20, v20
	v_fmac_f32_e32 v251, v21, v21
	v_fmac_f32_e32 v250, v22, v22
	v_fmac_f32_e32 v251, v23, v23
	global_store_dwordx2 v162, v[240:241], s[70:71] offset:2560
	v_cvt_pk_bf16_f32 v242, v24, v25
	v_cvt_pk_bf16_f32 v243, v26, v27
	v_fmac_f32_e32 v250, v24, v24
	v_fmac_f32_e32 v251, v25, v25
	v_fmac_f32_e32 v250, v26, v26
	v_fmac_f32_e32 v251, v27, v27
	global_store_dwordx2 v162, v[242:243], s[70:71] offset:3072
	v_cvt_pk_bf16_f32 v244, v28, v29
	v_cvt_pk_bf16_f32 v245, v30, v31
	v_fmac_f32_e32 v250, v28, v28
	v_fmac_f32_e32 v251, v29, v29
	v_fmac_f32_e32 v250, v30, v30
	v_fmac_f32_e32 v251, v31, v31
	global_store_dwordx2 v162, v[244:245], s[70:71] offset:3584
	s_add_u32 s70, s70, 0x8000
	s_addc_u32 s71, s71, 0
	v_add_f32_e32 v250, v250, v251
	s_nop 1
	v_add_f32_dpp v218, v250, v250 quad_perm:[1,0,3,2] row_mask:0xf bank_mask:0xf bound_ctrl:1
	s_nop 1
	v_add_f32_dpp v218, v218, v218 quad_perm:[2,3,0,1] row_mask:0xf bank_mask:0xf bound_ctrl:1
	s_nop 1
	v_add_f32_dpp v218, v218, v218 row_ror:4 row_mask:0xf bank_mask:0xf bound_ctrl:1
	s_nop 1
	v_add_f32_dpp v218, v218, v218 row_ror:8 row_mask:0xf bank_mask:0xf bound_ctrl:1
	s_nop 1
	v_readlane_b32 s8, v218, 0
	v_readlane_b32 s9, v218, 16
	v_readlane_b32 s10, v218, 32
	v_readlane_b32 s11, v218, 48
	s_nop 1
	v_mov_b32_e32 v218, s8
	v_add_f32_e32 v218, s9, v218
	v_mov_b32_e32 v219, s10
	v_add_f32_e32 v219, s11, v219
	v_add_f32_e32 v218, v218, v219
	v_mul_f32_e32 v218, 0x3a000000, v218
	v_add_f32_e32 v218, 0x358637bd, v218
	v_rsq_f32_e32 v218, v218
	s_nop 0
	v_mul_f32_e32 v246, v0, v218
	v_mul_f32_e32 v247, v1, v218
	v_mul_f32_e32 v248, v2, v218
	v_mul_f32_e32 v249, v3, v218
	v_fma_f32 v246, v246, v64, v96
	v_fma_f32 v247, v247, v65, v97
	v_fma_f32 v248, v248, v66, v98
	v_fma_f32 v249, v249, v67, v99
	v_cvt_pk_bf16_f32 v238, v246, v247
	v_cvt_pk_bf16_f32 v239, v248, v249
	global_store_dwordx2 v162, v[238:239], s[72:73]
	v_mul_f32_e32 v246, v4, v218
	v_mul_f32_e32 v247, v5, v218
	v_mul_f32_e32 v248, v6, v218
	v_mul_f32_e32 v249, v7, v218
	v_fma_f32 v246, v246, v68, v100
	v_fma_f32 v247, v247, v69, v101
	v_fma_f32 v248, v248, v70, v102
	v_fma_f32 v249, v249, v71, v103
	v_cvt_pk_bf16_f32 v240, v246, v247
	v_cvt_pk_bf16_f32 v241, v248, v249
	global_store_dwordx2 v162, v[240:241], s[72:73] offset:512
	v_mul_f32_e32 v246, v8, v218
	v_mul_f32_e32 v247, v9, v218
	v_mul_f32_e32 v248, v10, v218
	v_mul_f32_e32 v249, v11, v218
	v_fma_f32 v246, v246, v72, v104
	v_fma_f32 v247, v247, v73, v105
	v_fma_f32 v248, v248, v74, v106
	v_fma_f32 v249, v249, v75, v107
	v_cvt_pk_bf16_f32 v242, v246, v247
	v_cvt_pk_bf16_f32 v243, v248, v249
	global_store_dwordx2 v162, v[242:243], s[72:73] offset:1024
	v_mul_f32_e32 v246, v12, v218
	v_mul_f32_e32 v247, v13, v218
	v_mul_f32_e32 v248, v14, v218
	v_mul_f32_e32 v249, v15, v218
	v_fma_f32 v246, v246, v76, v108
	v_fma_f32 v247, v247, v77, v109
	v_fma_f32 v248, v248, v78, v110
	v_fma_f32 v249, v249, v79, v111
	v_cvt_pk_bf16_f32 v244, v246, v247
	v_cvt_pk_bf16_f32 v245, v248, v249
	global_store_dwordx2 v162, v[244:245], s[72:73] offset:1536
	v_mul_f32_e32 v246, v16, v218
	v_mul_f32_e32 v247, v17, v218
	v_mul_f32_e32 v248, v18, v218
	v_mul_f32_e32 v249, v19, v218
	v_fma_f32 v246, v246, v80, v112
	v_fma_f32 v247, v247, v81, v113
	v_fma_f32 v248, v248, v82, v114
	v_fma_f32 v249, v249, v83, v115
	v_cvt_pk_bf16_f32 v238, v246, v247
	v_cvt_pk_bf16_f32 v239, v248, v249
	global_store_dwordx2 v162, v[238:239], s[72:73] offset:2048
	v_mul_f32_e32 v246, v20, v218
	v_mul_f32_e32 v247, v21, v218
	v_mul_f32_e32 v248, v22, v218
	v_mul_f32_e32 v249, v23, v218
	v_fma_f32 v246, v246, v84, v116
	v_fma_f32 v247, v247, v85, v117
	v_fma_f32 v248, v248, v86, v118
	v_fma_f32 v249, v249, v87, v119
	v_cvt_pk_bf16_f32 v240, v246, v247
	v_cvt_pk_bf16_f32 v241, v248, v249
	global_store_dwordx2 v162, v[240:241], s[72:73] offset:2560
	v_mul_f32_e32 v246, v24, v218
	v_mul_f32_e32 v247, v25, v218
	v_mul_f32_e32 v248, v26, v218
	v_mul_f32_e32 v249, v27, v218
	v_fma_f32 v246, v246, v88, v120
	v_fma_f32 v247, v247, v89, v121
	v_fma_f32 v248, v248, v90, v122
	v_fma_f32 v249, v249, v91, v123
	v_cvt_pk_bf16_f32 v242, v246, v247
	v_cvt_pk_bf16_f32 v243, v248, v249
	global_store_dwordx2 v162, v[242:243], s[72:73] offset:3072
	v_mul_f32_e32 v246, v28, v218
	v_mul_f32_e32 v247, v29, v218
	v_mul_f32_e32 v248, v30, v218
	v_mul_f32_e32 v249, v31, v218
	v_fma_f32 v246, v246, v92, v124
	v_fma_f32 v247, v247, v93, v125
	v_fma_f32 v248, v248, v94, v126
	v_fma_f32 v249, v249, v95, v127
	v_cvt_pk_bf16_f32 v244, v246, v247
	v_cvt_pk_bf16_f32 v245, v248, v249
	global_store_dwordx2 v162, v[244:245], s[72:73] offset:3584
	s_add_u32 s72, s72, 0x8000
	s_addc_u32 s73, s73, 0
	s_waitcnt vmcnt(32)
	v_mov_b32_e32 v250, 0
	v_mov_b32_e32 v251, 0
	v_lshlrev_b32_e32 v246, 16, v166
	v_and_b32_e32 v247, 0xffff0000, v166
	v_lshlrev_b32_e32 v248, 16, v167
	v_and_b32_e32 v249, 0xffff0000, v167
	v_fmac_f32_e32 v250, v246, v246
	v_fmac_f32_e32 v251, v247, v247
	v_fmac_f32_e32 v250, v248, v248
	v_fmac_f32_e32 v251, v249, v249
	v_lshlrev_b32_e32 v246, 16, v168
	v_and_b32_e32 v247, 0xffff0000, v168
	v_lshlrev_b32_e32 v248, 16, v169
	v_and_b32_e32 v249, 0xffff0000, v169
	v_fmac_f32_e32 v250, v246, v246
	v_fmac_f32_e32 v251, v247, v247
	v_fmac_f32_e32 v250, v248, v248
	v_fmac_f32_e32 v251, v249, v249
	v_lshlrev_b32_e32 v246, 16, v170
	v_and_b32_e32 v247, 0xffff0000, v170
	v_lshlrev_b32_e32 v248, 16, v171
	v_and_b32_e32 v249, 0xffff0000, v171
	v_fmac_f32_e32 v250, v246, v246
	v_fmac_f32_e32 v251, v247, v247
	v_fmac_f32_e32 v250, v248, v248
	v_fmac_f32_e32 v251, v249, v249
	v_lshlrev_b32_e32 v246, 16, v172
	v_and_b32_e32 v247, 0xffff0000, v172
	v_lshlrev_b32_e32 v248, 16, v173
	v_and_b32_e32 v249, 0xffff0000, v173
	v_fmac_f32_e32 v250, v246, v246
	v_fmac_f32_e32 v251, v247, v247
	v_fmac_f32_e32 v250, v248, v248
	v_fmac_f32_e32 v251, v249, v249
	v_lshlrev_b32_e32 v246, 16, v174
	v_and_b32_e32 v247, 0xffff0000, v174
	v_lshlrev_b32_e32 v248, 16, v175
	v_and_b32_e32 v249, 0xffff0000, v175
	v_fmac_f32_e32 v250, v246, v246
	v_fmac_f32_e32 v251, v247, v247
	v_fmac_f32_e32 v250, v248, v248
	v_fmac_f32_e32 v251, v249, v249
	v_lshlrev_b32_e32 v246, 16, v176
	v_and_b32_e32 v247, 0xffff0000, v176
	v_lshlrev_b32_e32 v248, 16, v177
	v_and_b32_e32 v249, 0xffff0000, v177
	v_fmac_f32_e32 v250, v246, v246
	v_fmac_f32_e32 v251, v247, v247
	v_fmac_f32_e32 v250, v248, v248
	v_fmac_f32_e32 v251, v249, v249
	v_lshlrev_b32_e32 v246, 16, v178
	v_and_b32_e32 v247, 0xffff0000, v178
	v_lshlrev_b32_e32 v248, 16, v179
	v_and_b32_e32 v249, 0xffff0000, v179
	v_fmac_f32_e32 v250, v246, v246
	v_fmac_f32_e32 v251, v247, v247
	v_fmac_f32_e32 v250, v248, v248
	v_fmac_f32_e32 v251, v249, v249
	v_lshlrev_b32_e32 v246, 16, v180
	v_and_b32_e32 v247, 0xffff0000, v180
	v_lshlrev_b32_e32 v248, 16, v181
	v_and_b32_e32 v249, 0xffff0000, v181
	v_fmac_f32_e32 v250, v246, v246
	v_fmac_f32_e32 v251, v247, v247
	v_fmac_f32_e32 v250, v248, v248
	v_fmac_f32_e32 v251, v249, v249
	v_add_f32_e32 v250, v250, v251
	s_nop 1
	v_add_f32_dpp v218, v250, v250 quad_perm:[1,0,3,2] row_mask:0xf bank_mask:0xf bound_ctrl:1
	s_nop 1
	v_add_f32_dpp v218, v218, v218 quad_perm:[2,3,0,1] row_mask:0xf bank_mask:0xf bound_ctrl:1
	s_nop 1
	v_add_f32_dpp v218, v218, v218 row_ror:4 row_mask:0xf bank_mask:0xf bound_ctrl:1
	s_nop 1
	v_add_f32_dpp v218, v218, v218 row_ror:8 row_mask:0xf bank_mask:0xf bound_ctrl:1
	s_nop 1
	v_readlane_b32 s8, v218, 0
	v_readlane_b32 s9, v218, 16
	v_readlane_b32 s10, v218, 32
	v_readlane_b32 s11, v218, 48
	s_nop 1
	v_mov_b32_e32 v218, s8
	v_add_f32_e32 v218, s9, v218
	v_mov_b32_e32 v219, s10
	v_add_f32_e32 v219, s11, v219
	v_add_f32_e32 v218, v218, v219
	v_mul_f32_e32 v218, 0x3a000000, v218
	v_add_f32_e32 v218, 0x358637bd, v218
	v_rsq_f32_e32 v218, v218
	s_nop 0
	v_lshlrev_b32_e32 v246, 16, v166
	v_and_b32_e32 v247, 0xffff0000, v166
	v_lshlrev_b32_e32 v248, 16, v167
	v_and_b32_e32 v249, 0xffff0000, v167
	v_mul_f32_e32 v246, v246, v218
	v_mul_f32_e32 v247, v247, v218
	v_mul_f32_e32 v248, v248, v218
	v_mul_f32_e32 v249, v249, v218
	v_lshlrev_b32_e32 v0, 16, v182
	v_and_b32_e32 v1, 0xffff0000, v182
	v_lshlrev_b32_e32 v2, 16, v183
	v_and_b32_e32 v3, 0xffff0000, v183
	v_fmac_f32_e32 v0, v246, v32
	v_fmac_f32_e32 v1, v247, v33
	v_fmac_f32_e32 v2, v248, v34
	v_fmac_f32_e32 v3, v249, v35
	v_lshlrev_b32_e32 v246, 16, v168
	v_and_b32_e32 v247, 0xffff0000, v168
	v_lshlrev_b32_e32 v248, 16, v169
	v_and_b32_e32 v249, 0xffff0000, v169
	v_mul_f32_e32 v246, v246, v218
	v_mul_f32_e32 v247, v247, v218
	v_mul_f32_e32 v248, v248, v218
	v_mul_f32_e32 v249, v249, v218
	v_lshlrev_b32_e32 v4, 16, v184
	v_and_b32_e32 v5, 0xffff0000, v184
	v_lshlrev_b32_e32 v6, 16, v185
	v_and_b32_e32 v7, 0xffff0000, v185
	v_fmac_f32_e32 v4, v246, v36
	v_fmac_f32_e32 v5, v247, v37
	v_fmac_f32_e32 v6, v248, v38
	v_fmac_f32_e32 v7, v249, v39
	v_lshlrev_b32_e32 v246, 16, v170
	v_and_b32_e32 v247, 0xffff0000, v170
	v_lshlrev_b32_e32 v248, 16, v171
	v_and_b32_e32 v249, 0xffff0000, v171
	v_mul_f32_e32 v246, v246, v218
	v_mul_f32_e32 v247, v247, v218
	v_mul_f32_e32 v248, v248, v218
	v_mul_f32_e32 v249, v249, v218
	v_lshlrev_b32_e32 v8, 16, v186
	v_and_b32_e32 v9, 0xffff0000, v186
	v_lshlrev_b32_e32 v10, 16, v187
	v_and_b32_e32 v11, 0xffff0000, v187
	v_fmac_f32_e32 v8, v246, v40
	v_fmac_f32_e32 v9, v247, v41
	v_fmac_f32_e32 v10, v248, v42
	v_fmac_f32_e32 v11, v249, v43
	v_lshlrev_b32_e32 v246, 16, v172
	v_and_b32_e32 v247, 0xffff0000, v172
	v_lshlrev_b32_e32 v248, 16, v173
	v_and_b32_e32 v249, 0xffff0000, v173
	v_mul_f32_e32 v246, v246, v218
	v_mul_f32_e32 v247, v247, v218
	v_mul_f32_e32 v248, v248, v218
	v_mul_f32_e32 v249, v249, v218
	v_lshlrev_b32_e32 v12, 16, v188
	v_and_b32_e32 v13, 0xffff0000, v188
	v_lshlrev_b32_e32 v14, 16, v189
	v_and_b32_e32 v15, 0xffff0000, v189
	v_fmac_f32_e32 v12, v246, v44
	v_fmac_f32_e32 v13, v247, v45
	v_fmac_f32_e32 v14, v248, v46
	v_fmac_f32_e32 v15, v249, v47
	v_lshlrev_b32_e32 v246, 16, v174
	v_and_b32_e32 v247, 0xffff0000, v174
	v_lshlrev_b32_e32 v248, 16, v175
	v_and_b32_e32 v249, 0xffff0000, v175
	v_mul_f32_e32 v246, v246, v218
	v_mul_f32_e32 v247, v247, v218
	v_mul_f32_e32 v248, v248, v218
	v_mul_f32_e32 v249, v249, v218
	v_lshlrev_b32_e32 v16, 16, v190
	v_and_b32_e32 v17, 0xffff0000, v190
	v_lshlrev_b32_e32 v18, 16, v191
	v_and_b32_e32 v19, 0xffff0000, v191
	v_fmac_f32_e32 v16, v246, v48
	v_fmac_f32_e32 v17, v247, v49
	v_fmac_f32_e32 v18, v248, v50
	v_fmac_f32_e32 v19, v249, v51
	v_lshlrev_b32_e32 v246, 16, v176
	v_and_b32_e32 v247, 0xffff0000, v176
	v_lshlrev_b32_e32 v248, 16, v177
	v_and_b32_e32 v249, 0xffff0000, v177
	v_mul_f32_e32 v246, v246, v218
	v_mul_f32_e32 v247, v247, v218
	v_mul_f32_e32 v248, v248, v218
	v_mul_f32_e32 v249, v249, v218
	v_lshlrev_b32_e32 v20, 16, v192
	v_and_b32_e32 v21, 0xffff0000, v192
	v_lshlrev_b32_e32 v22, 16, v193
	v_and_b32_e32 v23, 0xffff0000, v193
	v_fmac_f32_e32 v20, v246, v52
	v_fmac_f32_e32 v21, v247, v53
	v_fmac_f32_e32 v22, v248, v54
	v_fmac_f32_e32 v23, v249, v55
	v_lshlrev_b32_e32 v246, 16, v178
	v_and_b32_e32 v247, 0xffff0000, v178
	v_lshlrev_b32_e32 v248, 16, v179
	v_and_b32_e32 v249, 0xffff0000, v179
	v_mul_f32_e32 v246, v246, v218
	v_mul_f32_e32 v247, v247, v218
	v_mul_f32_e32 v248, v248, v218
	v_mul_f32_e32 v249, v249, v218
	v_lshlrev_b32_e32 v24, 16, v194
	v_and_b32_e32 v25, 0xffff0000, v194
	v_lshlrev_b32_e32 v26, 16, v195
	v_and_b32_e32 v27, 0xffff0000, v195
	v_fmac_f32_e32 v24, v246, v56
	v_fmac_f32_e32 v25, v247, v57
	v_fmac_f32_e32 v26, v248, v58
	v_fmac_f32_e32 v27, v249, v59
	v_lshlrev_b32_e32 v246, 16, v180
	v_and_b32_e32 v247, 0xffff0000, v180
	v_lshlrev_b32_e32 v248, 16, v181
	v_and_b32_e32 v249, 0xffff0000, v181
	v_mul_f32_e32 v246, v246, v218
	v_mul_f32_e32 v247, v247, v218
	v_mul_f32_e32 v248, v248, v218
	v_mul_f32_e32 v249, v249, v218
	v_lshlrev_b32_e32 v28, 16, v196
	v_and_b32_e32 v29, 0xffff0000, v196
	v_lshlrev_b32_e32 v30, 16, v197
	v_and_b32_e32 v31, 0xffff0000, v197
	v_fmac_f32_e32 v28, v246, v60
	v_fmac_f32_e32 v29, v247, v61
	v_fmac_f32_e32 v30, v248, v62
	v_fmac_f32_e32 v31, v249, v63
	v_mov_b32_e32 v250, 0
	v_mov_b32_e32 v251, 0
	v_cvt_pk_bf16_f32 v238, v0, v1
	v_cvt_pk_bf16_f32 v239, v2, v3
	v_fmac_f32_e32 v250, v0, v0
	v_fmac_f32_e32 v251, v1, v1
	v_fmac_f32_e32 v250, v2, v2
	v_fmac_f32_e32 v251, v3, v3
	global_store_dwordx2 v162, v[238:239], s[70:71]
	v_cvt_pk_bf16_f32 v240, v4, v5
	v_cvt_pk_bf16_f32 v241, v6, v7
	v_fmac_f32_e32 v250, v4, v4
	v_fmac_f32_e32 v251, v5, v5
	v_fmac_f32_e32 v250, v6, v6
	v_fmac_f32_e32 v251, v7, v7
	global_store_dwordx2 v162, v[240:241], s[70:71] offset:512
	v_cvt_pk_bf16_f32 v242, v8, v9
	v_cvt_pk_bf16_f32 v243, v10, v11
	v_fmac_f32_e32 v250, v8, v8
	v_fmac_f32_e32 v251, v9, v9
	v_fmac_f32_e32 v250, v10, v10
	v_fmac_f32_e32 v251, v11, v11
	global_store_dwordx2 v162, v[242:243], s[70:71] offset:1024
	v_cvt_pk_bf16_f32 v244, v12, v13
	v_cvt_pk_bf16_f32 v245, v14, v15
	v_fmac_f32_e32 v250, v12, v12
	v_fmac_f32_e32 v251, v13, v13
	v_fmac_f32_e32 v250, v14, v14
	v_fmac_f32_e32 v251, v15, v15
	global_store_dwordx2 v162, v[244:245], s[70:71] offset:1536
	v_cvt_pk_bf16_f32 v238, v16, v17
	v_cvt_pk_bf16_f32 v239, v18, v19
	v_fmac_f32_e32 v250, v16, v16
	v_fmac_f32_e32 v251, v17, v17
	v_fmac_f32_e32 v250, v18, v18
	v_fmac_f32_e32 v251, v19, v19
	global_store_dwordx2 v162, v[238:239], s[70:71] offset:2048
	v_cvt_pk_bf16_f32 v240, v20, v21
	v_cvt_pk_bf16_f32 v241, v22, v23
	v_fmac_f32_e32 v250, v20, v20
	v_fmac_f32_e32 v251, v21, v21
	v_fmac_f32_e32 v250, v22, v22
	v_fmac_f32_e32 v251, v23, v23
	global_store_dwordx2 v162, v[240:241], s[70:71] offset:2560
	v_cvt_pk_bf16_f32 v242, v24, v25
	v_cvt_pk_bf16_f32 v243, v26, v27
	v_fmac_f32_e32 v250, v24, v24
	v_fmac_f32_e32 v251, v25, v25
	v_fmac_f32_e32 v250, v26, v26
	v_fmac_f32_e32 v251, v27, v27
	global_store_dwordx2 v162, v[242:243], s[70:71] offset:3072
	v_cvt_pk_bf16_f32 v244, v28, v29
	v_cvt_pk_bf16_f32 v245, v30, v31
	v_fmac_f32_e32 v250, v28, v28
	v_fmac_f32_e32 v251, v29, v29
	v_fmac_f32_e32 v250, v30, v30
	v_fmac_f32_e32 v251, v31, v31
	global_store_dwordx2 v162, v[244:245], s[70:71] offset:3584
	s_add_u32 s70, s70, 0x8000
	s_addc_u32 s71, s71, 0
	v_add_f32_e32 v250, v250, v251
	s_nop 1
	v_add_f32_dpp v218, v250, v250 quad_perm:[1,0,3,2] row_mask:0xf bank_mask:0xf bound_ctrl:1
	s_nop 1
	v_add_f32_dpp v218, v218, v218 quad_perm:[2,3,0,1] row_mask:0xf bank_mask:0xf bound_ctrl:1
	s_nop 1
	v_add_f32_dpp v218, v218, v218 row_ror:4 row_mask:0xf bank_mask:0xf bound_ctrl:1
	s_nop 1
	v_add_f32_dpp v218, v218, v218 row_ror:8 row_mask:0xf bank_mask:0xf bound_ctrl:1
	s_nop 1
	v_readlane_b32 s8, v218, 0
	v_readlane_b32 s9, v218, 16
	v_readlane_b32 s10, v218, 32
	v_readlane_b32 s11, v218, 48
	s_nop 1
	v_mov_b32_e32 v218, s8
	v_add_f32_e32 v218, s9, v218
	v_mov_b32_e32 v219, s10
	v_add_f32_e32 v219, s11, v219
	v_add_f32_e32 v218, v218, v219
	v_mul_f32_e32 v218, 0x3a000000, v218
	v_add_f32_e32 v218, 0x358637bd, v218
	v_rsq_f32_e32 v218, v218
	s_nop 0
	v_mul_f32_e32 v246, v0, v218
	v_mul_f32_e32 v247, v1, v218
	v_mul_f32_e32 v248, v2, v218
	v_mul_f32_e32 v249, v3, v218
	v_fma_f32 v246, v246, v64, v96
	v_fma_f32 v247, v247, v65, v97
	v_fma_f32 v248, v248, v66, v98
	v_fma_f32 v249, v249, v67, v99
	v_cvt_pk_bf16_f32 v238, v246, v247
	v_cvt_pk_bf16_f32 v239, v248, v249
	global_store_dwordx2 v162, v[238:239], s[72:73]
	v_mul_f32_e32 v246, v4, v218
	v_mul_f32_e32 v247, v5, v218
	v_mul_f32_e32 v248, v6, v218
	v_mul_f32_e32 v249, v7, v218
	v_fma_f32 v246, v246, v68, v100
	v_fma_f32 v247, v247, v69, v101
	v_fma_f32 v248, v248, v70, v102
	v_fma_f32 v249, v249, v71, v103
	v_cvt_pk_bf16_f32 v240, v246, v247
	v_cvt_pk_bf16_f32 v241, v248, v249
	global_store_dwordx2 v162, v[240:241], s[72:73] offset:512
	v_mul_f32_e32 v246, v8, v218
	v_mul_f32_e32 v247, v9, v218
	v_mul_f32_e32 v248, v10, v218
	v_mul_f32_e32 v249, v11, v218
	v_fma_f32 v246, v246, v72, v104
	v_fma_f32 v247, v247, v73, v105
	v_fma_f32 v248, v248, v74, v106
	v_fma_f32 v249, v249, v75, v107
	v_cvt_pk_bf16_f32 v242, v246, v247
	v_cvt_pk_bf16_f32 v243, v248, v249
	global_store_dwordx2 v162, v[242:243], s[72:73] offset:1024
	v_mul_f32_e32 v246, v12, v218
	v_mul_f32_e32 v247, v13, v218
	v_mul_f32_e32 v248, v14, v218
	v_mul_f32_e32 v249, v15, v218
	v_fma_f32 v246, v246, v76, v108
	v_fma_f32 v247, v247, v77, v109
	v_fma_f32 v248, v248, v78, v110
	v_fma_f32 v249, v249, v79, v111
	v_cvt_pk_bf16_f32 v244, v246, v247
	v_cvt_pk_bf16_f32 v245, v248, v249
	global_store_dwordx2 v162, v[244:245], s[72:73] offset:1536
	v_mul_f32_e32 v246, v16, v218
	v_mul_f32_e32 v247, v17, v218
	v_mul_f32_e32 v248, v18, v218
	v_mul_f32_e32 v249, v19, v218
	v_fma_f32 v246, v246, v80, v112
	v_fma_f32 v247, v247, v81, v113
	v_fma_f32 v248, v248, v82, v114
	v_fma_f32 v249, v249, v83, v115
	v_cvt_pk_bf16_f32 v238, v246, v247
	v_cvt_pk_bf16_f32 v239, v248, v249
	global_store_dwordx2 v162, v[238:239], s[72:73] offset:2048
	v_mul_f32_e32 v246, v20, v218
	v_mul_f32_e32 v247, v21, v218
	v_mul_f32_e32 v248, v22, v218
	v_mul_f32_e32 v249, v23, v218
	v_fma_f32 v246, v246, v84, v116
	v_fma_f32 v247, v247, v85, v117
	v_fma_f32 v248, v248, v86, v118
	v_fma_f32 v249, v249, v87, v119
	v_cvt_pk_bf16_f32 v240, v246, v247
	v_cvt_pk_bf16_f32 v241, v248, v249
	global_store_dwordx2 v162, v[240:241], s[72:73] offset:2560
	v_mul_f32_e32 v246, v24, v218
	v_mul_f32_e32 v247, v25, v218
	v_mul_f32_e32 v248, v26, v218
	v_mul_f32_e32 v249, v27, v218
	v_fma_f32 v246, v246, v88, v120
	v_fma_f32 v247, v247, v89, v121
	v_fma_f32 v248, v248, v90, v122
	v_fma_f32 v249, v249, v91, v123
	v_cvt_pk_bf16_f32 v242, v246, v247
	v_cvt_pk_bf16_f32 v243, v248, v249
	global_store_dwordx2 v162, v[242:243], s[72:73] offset:3072
	v_mul_f32_e32 v246, v28, v218
	v_mul_f32_e32 v247, v29, v218
	v_mul_f32_e32 v248, v30, v218
	v_mul_f32_e32 v249, v31, v218
	v_fma_f32 v246, v246, v92, v124
	v_fma_f32 v247, v247, v93, v125
	v_fma_f32 v248, v248, v94, v126
	v_fma_f32 v249, v249, v95, v127
	v_cvt_pk_bf16_f32 v244, v246, v247
	v_cvt_pk_bf16_f32 v245, v248, v249
	global_store_dwordx2 v162, v[244:245], s[72:73] offset:3584
	s_add_u32 s72, s72, 0x8000
	s_addc_u32 s73, s73, 0
	s_branch .Lmp_done
.Lmp_V2:
	global_load_dwordx2 v[128:129], v162, s[56:57] nt
	global_load_dwordx2 v[130:131], v162, s[56:57] offset:512 nt
	global_load_dwordx2 v[132:133], v162, s[56:57] offset:1024 nt
	global_load_dwordx2 v[134:135], v162, s[56:57] offset:1536 nt
	global_load_dwordx2 v[136:137], v162, s[56:57] offset:2048 nt
	global_load_dwordx2 v[138:139], v162, s[56:57] offset:2560 nt
	global_load_dwordx2 v[140:141], v162, s[56:57] offset:3072 nt
	global_load_dwordx2 v[142:143], v162, s[56:57] offset:3584 nt
	global_load_dwordx4 v[198:201], v163, s[58:59] nt
	global_load_dwordx4 v[202:205], v163, s[58:59] offset:1024 nt
	global_load_dwordx4 v[206:209], v163, s[58:59] offset:2048 nt
	global_load_dwordx4 v[210:213], v163, s[58:59] offset:3072 nt
	s_add_u32 s10, s58, 0x1000
	s_addc_u32 s11, s59, 0
	global_load_dwordx4 v[214:217], v163, s[10:11] nt
	global_load_dwordx4 v[226:229], v163, s[10:11] offset:1024 nt
	global_load_dwordx4 v[230:233], v163, s[10:11] offset:2048 nt
	global_load_dwordx4 v[234:237], v163, s[10:11] offset:3072 nt
	s_add_u32 s58, s58, 0x10000
	s_addc_u32 s59, s59, 0
	s_add_u32 s56, s56, 0x8000
	s_addc_u32 s57, s57, 0
	global_load_dwordx2 v[166:167], v162, s[56:57] nt
	global_load_dwordx2 v[168:169], v162, s[56:57] offset:512 nt
	global_load_dwordx2 v[170:171], v162, s[56:57] offset:1024 nt
	global_load_dwordx2 v[172:173], v162, s[56:57] offset:1536 nt
	global_load_dwordx2 v[174:175], v162, s[56:57] offset:2048 nt
	global_load_dwordx2 v[176:177], v162, s[56:57] offset:2560 nt
	global_load_dwordx2 v[178:179], v162, s[56:57] offset:3072 nt
	global_load_dwordx2 v[180:181], v162, s[56:57] offset:3584 nt
	global_load_dwordx4 v[144:147], v163, s[58:59] nt
	global_load_dwordx4 v[148:151], v163, s[58:59] offset:1024 nt
	global_load_dwordx4 v[152:155], v163, s[58:59] offset:2048 nt
	global_load_dwordx4 v[156:159], v163, s[58:59] offset:3072 nt
	s_add_u32 s10, s58, 0x1000
	s_addc_u32 s11, s59, 0
	global_load_dwordx4 v[182:185], v163, s[10:11] nt
	global_load_dwordx4 v[186:189], v163, s[10:11] offset:1024 nt
	global_load_dwordx4 v[190:193], v163, s[10:11] offset:2048 nt
	global_load_dwordx4 v[194:197], v163, s[10:11] offset:3072 nt
	s_add_u32 s58, s58, 0x10000
	s_addc_u32 s59, s59, 0
	s_add_u32 s56, s56, 0x8000
	s_addc_u32 s57, s57, 0
	s_waitcnt vmcnt(16)
.Lmp_V2_loop:
	s_waitcnt vmcnt(32)
	v_mov_b32_e32 v250, 0
	v_mov_b32_e32 v251, 0
	v_lshlrev_b32_e32 v246, 16, v128
	v_and_b32_e32 v247, 0xffff0000, v128
	v_lshlrev_b32_e32 v248, 16, v129
	v_and_b32_e32 v249, 0xffff0000, v129
	v_fmac_f32_e32 v250, v246, v246
	v_fmac_f32_e32 v251, v247, v247
	v_fmac_f32_e32 v250, v248, v248
	v_fmac_f32_e32 v251, v249, v249
	v_lshlrev_b32_e32 v246, 16, v130
	v_and_b32_e32 v247, 0xffff0000, v130
	v_lshlrev_b32_e32 v248, 16, v131
	v_and_b32_e32 v249, 0xffff0000, v131
	v_fmac_f32_e32 v250, v246, v246
	v_fmac_f32_e32 v251, v247, v247
	v_fmac_f32_e32 v250, v248, v248
	v_fmac_f32_e32 v251, v249, v249
	v_lshlrev_b32_e32 v246, 16, v132
	v_and_b32_e32 v247, 0xffff0000, v132
	v_lshlrev_b32_e32 v248, 16, v133
	v_and_b32_e32 v249, 0xffff0000, v133
	v_fmac_f32_e32 v250, v246, v246
	v_fmac_f32_e32 v251, v247, v247
	v_fmac_f32_e32 v250, v248, v248
	v_fmac_f32_e32 v251, v249, v249
	v_lshlrev_b32_e32 v246, 16, v134
	v_and_b32_e32 v247, 0xffff0000, v134
	v_lshlrev_b32_e32 v248, 16, v135
	v_and_b32_e32 v249, 0xffff0000, v135
	v_fmac_f32_e32 v250, v246, v246
	v_fmac_f32_e32 v251, v247, v247
	v_fmac_f32_e32 v250, v248, v248
	v_fmac_f32_e32 v251, v249, v249
	v_lshlrev_b32_e32 v246, 16, v136
	v_and_b32_e32 v247, 0xffff0000, v136
	v_lshlrev_b32_e32 v248, 16, v137
	v_and_b32_e32 v249, 0xffff0000, v137
	v_fmac_f32_e32 v250, v246, v246
	v_fmac_f32_e32 v251, v247, v247
	v_fmac_f32_e32 v250, v248, v248
	v_fmac_f32_e32 v251, v249, v249
	v_lshlrev_b32_e32 v246, 16, v138
	v_and_b32_e32 v247, 0xffff0000, v138
	v_lshlrev_b32_e32 v248, 16, v139
	v_and_b32_e32 v249, 0xffff0000, v139
	v_fmac_f32_e32 v250, v246, v246
	v_fmac_f32_e32 v251, v247, v247
	v_fmac_f32_e32 v250, v248, v248
	v_fmac_f32_e32 v251, v249, v249
	v_lshlrev_b32_e32 v246, 16, v140
	v_and_b32_e32 v247, 0xffff0000, v140
	v_lshlrev_b32_e32 v248, 16, v141
	v_and_b32_e32 v249, 0xffff0000, v141
	v_fmac_f32_e32 v250, v246, v246
	v_fmac_f32_e32 v251, v247, v247
	v_fmac_f32_e32 v250, v248, v248
	v_fmac_f32_e32 v251, v249, v249
	v_lshlrev_b32_e32 v246, 16, v142
	v_and_b32_e32 v247, 0xffff0000, v142
	v_lshlrev_b32_e32 v248, 16, v143
	v_and_b32_e32 v249, 0xffff0000, v143
	v_fmac_f32_e32 v250, v246, v246
	v_fmac_f32_e32 v251, v247, v247
	v_fmac_f32_e32 v250, v248, v248
	v_fmac_f32_e32 v251, v249, v249
	v_add_f32_e32 v250, v250, v251
	s_nop 1
	v_add_f32_dpp v218, v250, v250 quad_perm:[1,0,3,2] row_mask:0xf bank_mask:0xf bound_ctrl:1
	s_nop 1
	v_add_f32_dpp v218, v218, v218 quad_perm:[2,3,0,1] row_mask:0xf bank_mask:0xf bound_ctrl:1
	s_nop 1
	v_add_f32_dpp v218, v218, v218 row_ror:4 row_mask:0xf bank_mask:0xf bound_ctrl:1
	s_nop 1
	v_add_f32_dpp v218, v218, v218 row_ror:8 row_mask:0xf bank_mask:0xf bound_ctrl:1
	s_nop 1
	v_readlane_b32 s8, v218, 0
	v_readlane_b32 s9, v218, 16
	v_readlane_b32 s10, v218, 32
	v_readlane_b32 s11, v218, 48
	s_nop 1
	v_mov_b32_e32 v218, s8
	v_add_f32_e32 v218, s9, v218
	v_mov_b32_e32 v219, s10
	v_add_f32_e32 v219, s11, v219
	v_add_f32_e32 v218, v218, v219
	v_mul_f32_e32 v218, 0x3a000000, v218
	v_add_f32_e32 v218, 0x358637bd, v218
	v_rsq_f32_e32 v218, v218
	s_nop 0
	v_lshlrev_b32_e32 v246, 16, v128
	v_and_b32_e32 v247, 0xffff0000, v128
	v_lshlrev_b32_e32 v248, 16, v129
	v_and_b32_e32 v249, 0xffff0000, v129
	v_mul_f32_e32 v246, v246, v218
	v_mul_f32_e32 v247, v247, v218
	v_mul_f32_e32 v248, v248, v218
	v_mul_f32_e32 v249, v249, v218
	v_fma_f32 v0, v246, v32, v198
	v_fma_f32 v1, v247, v33, v199
	v_fma_f32 v2, v248, v34, v200
	v_fma_f32 v3, v249, v35, v201
	v_lshlrev_b32_e32 v246, 16, v130
	v_and_b32_e32 v247, 0xffff0000, v130
	v_lshlrev_b32_e32 v248, 16, v131
	v_and_b32_e32 v249, 0xffff0000, v131
	v_mul_f32_e32 v246, v246, v218
	v_mul_f32_e32 v247, v247, v218
	v_mul_f32_e32 v248, v248, v218
	v_mul_f32_e32 v249, v249, v218
	v_fma_f32 v4, v246, v36, v202
	v_fma_f32 v5, v247, v37, v203
	v_fma_f32 v6, v248, v38, v204
	v_fma_f32 v7, v249, v39, v205
	v_lshlrev_b32_e32 v246, 16, v132
	v_and_b32_e32 v247, 0xffff0000, v132
	v_lshlrev_b32_e32 v248, 16, v133
	v_and_b32_e32 v249, 0xffff0000, v133
	v_mul_f32_e32 v246, v246, v218
	v_mul_f32_e32 v247, v247, v218
	v_mul_f32_e32 v248, v248, v218
	v_mul_f32_e32 v249, v249, v218
	v_fma_f32 v8, v246, v40, v206
	v_fma_f32 v9, v247, v41, v207
	v_fma_f32 v10, v248, v42, v208
	v_fma_f32 v11, v249, v43, v209
	v_lshlrev_b32_e32 v246, 16, v134
	v_and_b32_e32 v247, 0xffff0000, v134
	v_lshlrev_b32_e32 v248, 16, v135
	v_and_b32_e32 v249, 0xffff0000, v135
	v_mul_f32_e32 v246, v246, v218
	v_mul_f32_e32 v247, v247, v218
	v_mul_f32_e32 v248, v248, v218
	v_mul_f32_e32 v249, v249, v218
	v_fma_f32 v12, v246, v44, v210
	v_fma_f32 v13, v247, v45, v211
	v_fma_f32 v14, v248, v46, v212
	v_fma_f32 v15, v249, v47, v213
	v_lshlrev_b32_e32 v246, 16, v136
	v_and_b32_e32 v247, 0xffff0000, v136
	v_lshlrev_b32_e32 v248, 16, v137
	v_and_b32_e32 v249, 0xffff0000, v137
	v_mul_f32_e32 v246, v246, v218
	v_mul_f32_e32 v247, v247, v218
	v_mul_f32_e32 v248, v248, v218
	v_mul_f32_e32 v249, v249, v218
	v_fma_f32 v16, v246, v48, v214
	v_fma_f32 v17, v247, v49, v215
	v_fma_f32 v18, v248, v50, v216
	v_fma_f32 v19, v249, v51, v217
	v_lshlrev_b32_e32 v246, 16, v138
	v_and_b32_e32 v247, 0xffff0000, v138
	v_lshlrev_b32_e32 v248, 16, v139
	v_and_b32_e32 v249, 0xffff0000, v139
	v_mul_f32_e32 v246, v246, v218
	v_mul_f32_e32 v247, v247, v218
	v_mul_f32_e32 v248, v248, v218
	v_mul_f32_e32 v249, v249, v218
	v_fma_f32 v20, v246, v52, v226
	v_fma_f32 v21, v247, v53, v227
	v_fma_f32 v22, v248, v54, v228
	v_fma_f32 v23, v249, v55, v229
	v_lshlrev_b32_e32 v246, 16, v140
	v_and_b32_e32 v247, 0xffff0000, v140
	v_lshlrev_b32_e32 v248, 16, v141
	v_and_b32_e32 v249, 0xffff0000, v141
	v_mul_f32_e32 v246, v246, v218
	v_mul_f32_e32 v247, v247, v218
	v_mul_f32_e32 v248, v248, v218
	v_mul_f32_e32 v249, v249, v218
	v_fma_f32 v24, v246, v56, v230
	v_fma_f32 v25, v247, v57, v231
	v_fma_f32 v26, v248, v58, v232
	v_fma_f32 v27, v249, v59, v233
	v_lshlrev_b32_e32 v246, 16, v142
	v_and_b32_e32 v247, 0xffff0000, v142
	v_lshlrev_b32_e32 v248, 16, v143
	v_and_b32_e32 v249, 0xffff0000, v143
	v_mul_f32_e32 v246, v246, v218
	v_mul_f32_e32 v247, v247, v218
	v_mul_f32_e32 v248, v248, v218
	v_mul_f32_e32 v249, v249, v218
	v_fma_f32 v28, v246, v60, v234
	v_fma_f32 v29, v247, v61, v235
	v_fma_f32 v30, v248, v62, v236
	v_fma_f32 v31, v249, v63, v237
	global_load_dwordx2 v[128:129], v162, s[56:57] nt
	global_load_dwordx2 v[130:131], v162, s[56:57] offset:512 nt
	global_load_dwordx2 v[132:133], v162, s[56:57] offset:1024 nt
	global_load_dwordx2 v[134:135], v162, s[56:57] offset:1536 nt
	global_load_dwordx2 v[136:137], v162, s[56:57] offset:2048 nt
	global_load_dwordx2 v[138:139], v162, s[56:57] offset:2560 nt
	global_load_dwordx2 v[140:141], v162, s[56:57] offset:3072 nt
	global_load_dwordx2 v[142:143], v162, s[56:57] offset:3584 nt
	global_load_dwordx4 v[198:201], v163, s[58:59] nt
	global_load_dwordx4 v[202:205], v163, s[58:59] offset:1024 nt
	global_load_dwordx4 v[206:209], v163, s[58:59] offset:2048 nt
	global_load_dwordx4 v[210:213], v163, s[58:59] offset:3072 nt
	s_add_u32 s10, s58, 0x1000
	s_addc_u32 s11, s59, 0
	global_load_dwordx4 v[214:217], v163, s[10:11] nt
	global_load_dwordx4 v[226:229], v163, s[10:11] offset:1024 nt
	global_load_dwordx4 v[230:233], v163, s[10:11] offset:2048 nt
	global_load_dwordx4 v[234:237], v163, s[10:11] offset:3072 nt
	s_add_u32 s58, s58, 0x10000
	s_addc_u32 s59, s59, 0
	s_add_u32 s56, s56, 0x8000
	s_addc_u32 s57, s57, 0
	v_mov_b32_e32 v250, 0
	v_mov_b32_e32 v251, 0
	v_cvt_pk_bf16_f32 v238, v0, v1
	v_cvt_pk_bf16_f32 v239, v2, v3
	v_fmac_f32_e32 v250, v0, v0
	v_fmac_f32_e32 v251, v1, v1
	v_fmac_f32_e32 v250, v2, v2
	v_fmac_f32_e32 v251, v3, v3
	global_store_dwordx2 v162, v[238:239], s[70:71]
	v_cvt_pk_bf16_f32 v240, v4, v5
	v_cvt_pk_bf16_f32 v241, v6, v7
	v_fmac_f32_e32 v250, v4, v4
	v_fmac_f32_e32 v251, v5, v5
	v_fmac_f32_e32 v250, v6, v6
	v_fmac_f32_e32 v251, v7, v7
	global_store_dwordx2 v162, v[240:241], s[70:71] offset:512
	v_cvt_pk_bf16_f32 v242, v8, v9
	v_cvt_pk_bf16_f32 v243, v10, v11
	v_fmac_f32_e32 v250, v8, v8
	v_fmac_f32_e32 v251, v9, v9
	v_fmac_f32_e32 v250, v10, v10
	v_fmac_f32_e32 v251, v11, v11
	global_store_dwordx2 v162, v[242:243], s[70:71] offset:1024
	v_cvt_pk_bf16_f32 v244, v12, v13
	v_cvt_pk_bf16_f32 v245, v14, v15
	v_fmac_f32_e32 v250, v12, v12
	v_fmac_f32_e32 v251, v13, v13
	v_fmac_f32_e32 v250, v14, v14
	v_fmac_f32_e32 v251, v15, v15
	global_store_dwordx2 v162, v[244:245], s[70:71] offset:1536
	v_cvt_pk_bf16_f32 v238, v16, v17
	v_cvt_pk_bf16_f32 v239, v18, v19
	v_fmac_f32_e32 v250, v16, v16
	v_fmac_f32_e32 v251, v17, v17
	v_fmac_f32_e32 v250, v18, v18
	v_fmac_f32_e32 v251, v19, v19
	global_store_dwordx2 v162, v[238:239], s[70:71] offset:2048
	v_cvt_pk_bf16_f32 v240, v20, v21
	v_cvt_pk_bf16_f32 v241, v22, v23
	v_fmac_f32_e32 v250, v20, v20
	v_fmac_f32_e32 v251, v21, v21
	v_fmac_f32_e32 v250, v22, v22
	v_fmac_f32_e32 v251, v23, v23
	global_store_dwordx2 v162, v[240:241], s[70:71] offset:2560
	v_cvt_pk_bf16_f32 v242, v24, v25
	v_cvt_pk_bf16_f32 v243, v26, v27
	v_fmac_f32_e32 v250, v24, v24
	v_fmac_f32_e32 v251, v25, v25
	v_fmac_f32_e32 v250, v26, v26
	v_fmac_f32_e32 v251, v27, v27
	global_store_dwordx2 v162, v[242:243], s[70:71] offset:3072
	v_cvt_pk_bf16_f32 v244, v28, v29
	v_cvt_pk_bf16_f32 v245, v30, v31
	v_fmac_f32_e32 v250, v28, v28
	v_fmac_f32_e32 v251, v29, v29
	v_fmac_f32_e32 v250, v30, v30
	v_fmac_f32_e32 v251, v31, v31
	global_store_dwordx2 v162, v[244:245], s[70:71] offset:3584
	s_add_u32 s70, s70, 0x8000
	s_addc_u32 s71, s71, 0
	v_add_f32_e32 v250, v250, v251
	s_nop 1
	v_add_f32_dpp v218, v250, v250 quad_perm:[1,0,3,2] row_mask:0xf bank_mask:0xf bound_ctrl:1
	s_nop 1
	v_add_f32_dpp v218, v218, v218 quad_perm:[2,3,0,1] row_mask:0xf bank_mask:0xf bound_ctrl:1
	s_nop 1
	v_add_f32_dpp v218, v218, v218 row_ror:4 row_mask:0xf bank_mask:0xf bound_ctrl:1
	s_nop 1
	v_add_f32_dpp v218, v218, v218 row_ror:8 row_mask:0xf bank_mask:0xf bound_ctrl:1
	s_nop 1
	v_readlane_b32 s8, v218, 0
	v_readlane_b32 s9, v218, 16
	v_readlane_b32 s10, v218, 32
	v_readlane_b32 s11, v218, 48
	s_nop 1
	v_mov_b32_e32 v218, s8
	v_add_f32_e32 v218, s9, v218
	v_mov_b32_e32 v219, s10
	v_add_f32_e32 v219, s11, v219
	v_add_f32_e32 v218, v218, v219
	v_mul_f32_e32 v218, 0x3a000000, v218
	v_add_f32_e32 v218, 0x358637bd, v218
	v_rsq_f32_e32 v218, v218
	s_nop 0
	v_mul_f32_e32 v246, v0, v218
	v_mul_f32_e32 v247, v1, v218
	v_mul_f32_e32 v248, v2, v218
	v_mul_f32_e32 v249, v3, v218
	v_fma_f32 v246, v246, v64, v96
	v_fma_f32 v247, v247, v65, v97
	v_fma_f32 v248, v248, v66, v98
	v_fma_f32 v249, v249, v67, v99
	v_cvt_pk_bf16_f32 v238, v246, v247
	v_cvt_pk_bf16_f32 v239, v248, v249
	global_store_dwordx2 v162, v[238:239], s[72:73]
	v_mul_f32_e32 v246, v4, v218
	v_mul_f32_e32 v247, v5, v218
	v_mul_f32_e32 v248, v6, v218
	v_mul_f32_e32 v249, v7, v218
	v_fma_f32 v246, v246, v68, v100
	v_fma_f32 v247, v247, v69, v101
	v_fma_f32 v248, v248, v70, v102
	v_fma_f32 v249, v249, v71, v103
	v_cvt_pk_bf16_f32 v240, v246, v247
	v_cvt_pk_bf16_f32 v241, v248, v249
	global_store_dwordx2 v162, v[240:241], s[72:73] offset:512
	v_mul_f32_e32 v246, v8, v218
	v_mul_f32_e32 v247, v9, v218
	v_mul_f32_e32 v248, v10, v218
	v_mul_f32_e32 v249, v11, v218
	v_fma_f32 v246, v246, v72, v104
	v_fma_f32 v247, v247, v73, v105
	v_fma_f32 v248, v248, v74, v106
	v_fma_f32 v249, v249, v75, v107
	v_cvt_pk_bf16_f32 v242, v246, v247
	v_cvt_pk_bf16_f32 v243, v248, v249
	global_store_dwordx2 v162, v[242:243], s[72:73] offset:1024
	v_mul_f32_e32 v246, v12, v218
	v_mul_f32_e32 v247, v13, v218
	v_mul_f32_e32 v248, v14, v218
	v_mul_f32_e32 v249, v15, v218
	v_fma_f32 v246, v246, v76, v108
	v_fma_f32 v247, v247, v77, v109
	v_fma_f32 v248, v248, v78, v110
	v_fma_f32 v249, v249, v79, v111
	v_cvt_pk_bf16_f32 v244, v246, v247
	v_cvt_pk_bf16_f32 v245, v248, v249
	global_store_dwordx2 v162, v[244:245], s[72:73] offset:1536
	v_mul_f32_e32 v246, v16, v218
	v_mul_f32_e32 v247, v17, v218
	v_mul_f32_e32 v248, v18, v218
	v_mul_f32_e32 v249, v19, v218
	v_fma_f32 v246, v246, v80, v112
	v_fma_f32 v247, v247, v81, v113
	v_fma_f32 v248, v248, v82, v114
	v_fma_f32 v249, v249, v83, v115
	v_cvt_pk_bf16_f32 v238, v246, v247
	v_cvt_pk_bf16_f32 v239, v248, v249
	global_store_dwordx2 v162, v[238:239], s[72:73] offset:2048
	v_mul_f32_e32 v246, v20, v218
	v_mul_f32_e32 v247, v21, v218
	v_mul_f32_e32 v248, v22, v218
	v_mul_f32_e32 v249, v23, v218
	v_fma_f32 v246, v246, v84, v116
	v_fma_f32 v247, v247, v85, v117
	v_fma_f32 v248, v248, v86, v118
	v_fma_f32 v249, v249, v87, v119
	v_cvt_pk_bf16_f32 v240, v246, v247
	v_cvt_pk_bf16_f32 v241, v248, v249
	global_store_dwordx2 v162, v[240:241], s[72:73] offset:2560
	v_mul_f32_e32 v246, v24, v218
	v_mul_f32_e32 v247, v25, v218
	v_mul_f32_e32 v248, v26, v218
	v_mul_f32_e32 v249, v27, v218
	v_fma_f32 v246, v246, v88, v120
	v_fma_f32 v247, v247, v89, v121
	v_fma_f32 v248, v248, v90, v122
	v_fma_f32 v249, v249, v91, v123
	v_cvt_pk_bf16_f32 v242, v246, v247
	v_cvt_pk_bf16_f32 v243, v248, v249
	global_store_dwordx2 v162, v[242:243], s[72:73] offset:3072
	v_mul_f32_e32 v246, v28, v218
	v_mul_f32_e32 v247, v29, v218
	v_mul_f32_e32 v248, v30, v218
	v_mul_f32_e32 v249, v31, v218
	v_fma_f32 v246, v246, v92, v124
	v_fma_f32 v247, v247, v93, v125
	v_fma_f32 v248, v248, v94, v126
	v_fma_f32 v249, v249, v95, v127
	v_cvt_pk_bf16_f32 v244, v246, v247
	v_cvt_pk_bf16_f32 v245, v248, v249
	global_store_dwordx2 v162, v[244:245], s[72:73] offset:3584
	s_add_u32 s72, s72, 0x8000
	s_addc_u32 s73, s73, 0
	s_waitcnt vmcnt(32)
	v_mov_b32_e32 v250, 0
	v_mov_b32_e32 v251, 0
	v_lshlrev_b32_e32 v246, 16, v166
	v_and_b32_e32 v247, 0xffff0000, v166
	v_lshlrev_b32_e32 v248, 16, v167
	v_and_b32_e32 v249, 0xffff0000, v167
	v_fmac_f32_e32 v250, v246, v246
	v_fmac_f32_e32 v251, v247, v247
	v_fmac_f32_e32 v250, v248, v248
	v_fmac_f32_e32 v251, v249, v249
	v_lshlrev_b32_e32 v246, 16, v168
	v_and_b32_e32 v247, 0xffff0000, v168
	v_lshlrev_b32_e32 v248, 16, v169
	v_and_b32_e32 v249, 0xffff0000, v169
	v_fmac_f32_e32 v250, v246, v246
	v_fmac_f32_e32 v251, v247, v247
	v_fmac_f32_e32 v250, v248, v248
	v_fmac_f32_e32 v251, v249, v249
	v_lshlrev_b32_e32 v246, 16, v170
	v_and_b32_e32 v247, 0xffff0000, v170
	v_lshlrev_b32_e32 v248, 16, v171
	v_and_b32_e32 v249, 0xffff0000, v171
	v_fmac_f32_e32 v250, v246, v246
	v_fmac_f32_e32 v251, v247, v247
	v_fmac_f32_e32 v250, v248, v248
	v_fmac_f32_e32 v251, v249, v249
	v_lshlrev_b32_e32 v246, 16, v172
	v_and_b32_e32 v247, 0xffff0000, v172
	v_lshlrev_b32_e32 v248, 16, v173
	v_and_b32_e32 v249, 0xffff0000, v173
	v_fmac_f32_e32 v250, v246, v246
	v_fmac_f32_e32 v251, v247, v247
	v_fmac_f32_e32 v250, v248, v248
	v_fmac_f32_e32 v251, v249, v249
	v_lshlrev_b32_e32 v246, 16, v174
	v_and_b32_e32 v247, 0xffff0000, v174
	v_lshlrev_b32_e32 v248, 16, v175
	v_and_b32_e32 v249, 0xffff0000, v175
	v_fmac_f32_e32 v250, v246, v246
	v_fmac_f32_e32 v251, v247, v247
	v_fmac_f32_e32 v250, v248, v248
	v_fmac_f32_e32 v251, v249, v249
	v_lshlrev_b32_e32 v246, 16, v176
	v_and_b32_e32 v247, 0xffff0000, v176
	v_lshlrev_b32_e32 v248, 16, v177
	v_and_b32_e32 v249, 0xffff0000, v177
	v_fmac_f32_e32 v250, v246, v246
	v_fmac_f32_e32 v251, v247, v247
	v_fmac_f32_e32 v250, v248, v248
	v_fmac_f32_e32 v251, v249, v249
	v_lshlrev_b32_e32 v246, 16, v178
	v_and_b32_e32 v247, 0xffff0000, v178
	v_lshlrev_b32_e32 v248, 16, v179
	v_and_b32_e32 v249, 0xffff0000, v179
	v_fmac_f32_e32 v250, v246, v246
	v_fmac_f32_e32 v251, v247, v247
	v_fmac_f32_e32 v250, v248, v248
	v_fmac_f32_e32 v251, v249, v249
	v_lshlrev_b32_e32 v246, 16, v180
	v_and_b32_e32 v247, 0xffff0000, v180
	v_lshlrev_b32_e32 v248, 16, v181
	v_and_b32_e32 v249, 0xffff0000, v181
	v_fmac_f32_e32 v250, v246, v246
	v_fmac_f32_e32 v251, v247, v247
	v_fmac_f32_e32 v250, v248, v248
	v_fmac_f32_e32 v251, v249, v249
	v_add_f32_e32 v250, v250, v251
	s_nop 1
	v_add_f32_dpp v218, v250, v250 quad_perm:[1,0,3,2] row_mask:0xf bank_mask:0xf bound_ctrl:1
	s_nop 1
	v_add_f32_dpp v218, v218, v218 quad_perm:[2,3,0,1] row_mask:0xf bank_mask:0xf bound_ctrl:1
	s_nop 1
	v_add_f32_dpp v218, v218, v218 row_ror:4 row_mask:0xf bank_mask:0xf bound_ctrl:1
	s_nop 1
	v_add_f32_dpp v218, v218, v218 row_ror:8 row_mask:0xf bank_mask:0xf bound_ctrl:1
	s_nop 1
	v_readlane_b32 s8, v218, 0
	v_readlane_b32 s9, v218, 16
	v_readlane_b32 s10, v218, 32
	v_readlane_b32 s11, v218, 48
	s_nop 1
	v_mov_b32_e32 v218, s8
	v_add_f32_e32 v218, s9, v218
	v_mov_b32_e32 v219, s10
	v_add_f32_e32 v219, s11, v219
	v_add_f32_e32 v218, v218, v219
	v_mul_f32_e32 v218, 0x3a000000, v218
	v_add_f32_e32 v218, 0x358637bd, v218
	v_rsq_f32_e32 v218, v218
	s_nop 0
	v_lshlrev_b32_e32 v246, 16, v166
	v_and_b32_e32 v247, 0xffff0000, v166
	v_lshlrev_b32_e32 v248, 16, v167
	v_and_b32_e32 v249, 0xffff0000, v167
	v_mul_f32_e32 v246, v246, v218
	v_mul_f32_e32 v247, v247, v218
	v_mul_f32_e32 v248, v248, v218
	v_mul_f32_e32 v249, v249, v218
	v_fma_f32 v0, v246, v32, v144
	v_fma_f32 v1, v247, v33, v145
	v_fma_f32 v2, v248, v34, v146
	v_fma_f32 v3, v249, v35, v147
	v_lshlrev_b32_e32 v246, 16, v168
	v_and_b32_e32 v247, 0xffff0000, v168
	v_lshlrev_b32_e32 v248, 16, v169
	v_and_b32_e32 v249, 0xffff0000, v169
	v_mul_f32_e32 v246, v246, v218
	v_mul_f32_e32 v247, v247, v218
	v_mul_f32_e32 v248, v248, v218
	v_mul_f32_e32 v249, v249, v218
	v_fma_f32 v4, v246, v36, v148
	v_fma_f32 v5, v247, v37, v149
	v_fma_f32 v6, v248, v38, v150
	v_fma_f32 v7, v249, v39, v151
	v_lshlrev_b32_e32 v246, 16, v170
	v_and_b32_e32 v247, 0xffff0000, v170
	v_lshlrev_b32_e32 v248, 16, v171
	v_and_b32_e32 v249, 0xffff0000, v171
	v_mul_f32_e32 v246, v246, v218
	v_mul_f32_e32 v247, v247, v218
	v_mul_f32_e32 v248, v248, v218
	v_mul_f32_e32 v249, v249, v218
	v_fma_f32 v8, v246, v40, v152
	v_fma_f32 v9, v247, v41, v153
	v_fma_f32 v10, v248, v42, v154
	v_fma_f32 v11, v249, v43, v155
	v_lshlrev_b32_e32 v246, 16, v172
	v_and_b32_e32 v247, 0xffff0000, v172
	v_lshlrev_b32_e32 v248, 16, v173
	v_and_b32_e32 v249, 0xffff0000, v173
	v_mul_f32_e32 v246, v246, v218
	v_mul_f32_e32 v247, v247, v218
	v_mul_f32_e32 v248, v248, v218
	v_mul_f32_e32 v249, v249, v218
	v_fma_f32 v12, v246, v44, v156
	v_fma_f32 v13, v247, v45, v157
	v_fma_f32 v14, v248, v46, v158
	v_fma_f32 v15, v249, v47, v159
	v_lshlrev_b32_e32 v246, 16, v174
	v_and_b32_e32 v247, 0xffff0000, v174
	v_lshlrev_b32_e32 v248, 16, v175
	v_and_b32_e32 v249, 0xffff0000, v175
	v_mul_f32_e32 v246, v246, v218
	v_mul_f32_e32 v247, v247, v218
	v_mul_f32_e32 v248, v248, v218
	v_mul_f32_e32 v249, v249, v218
	v_fma_f32 v16, v246, v48, v182
	v_fma_f32 v17, v247, v49, v183
	v_fma_f32 v18, v248, v50, v184
	v_fma_f32 v19, v249, v51, v185
	v_lshlrev_b32_e32 v246, 16, v176
	v_and_b32_e32 v247, 0xffff0000, v176
	v_lshlrev_b32_e32 v248, 16, v177
	v_and_b32_e32 v249, 0xffff0000, v177
	v_mul_f32_e32 v246, v246, v218
	v_mul_f32_e32 v247, v247, v218
	v_mul_f32_e32 v248, v248, v218
	v_mul_f32_e32 v249, v249, v218
	v_fma_f32 v20, v246, v52, v186
	v_fma_f32 v21, v247, v53, v187
	v_fma_f32 v22, v248, v54, v188
	v_fma_f32 v23, v249, v55, v189
	v_lshlrev_b32_e32 v246, 16, v178
	v_and_b32_e32 v247, 0xffff0000, v178
	v_lshlrev_b32_e32 v248, 16, v179
	v_and_b32_e32 v249, 0xffff0000, v179
	v_mul_f32_e32 v246, v246, v218
	v_mul_f32_e32 v247, v247, v218
	v_mul_f32_e32 v248, v248, v218
	v_mul_f32_e32 v249, v249, v218
	v_fma_f32 v24, v246, v56, v190
	v_fma_f32 v25, v247, v57, v191
	v_fma_f32 v26, v248, v58, v192
	v_fma_f32 v27, v249, v59, v193
	v_lshlrev_b32_e32 v246, 16, v180
	v_and_b32_e32 v247, 0xffff0000, v180
	v_lshlrev_b32_e32 v248, 16, v181
	v_and_b32_e32 v249, 0xffff0000, v181
	v_mul_f32_e32 v246, v246, v218
	v_mul_f32_e32 v247, v247, v218
	v_mul_f32_e32 v248, v248, v218
	v_mul_f32_e32 v249, v249, v218
	v_fma_f32 v28, v246, v60, v194
	v_fma_f32 v29, v247, v61, v195
	v_fma_f32 v30, v248, v62, v196
	v_fma_f32 v31, v249, v63, v197
	global_load_dwordx2 v[166:167], v162, s[56:57] nt
	global_load_dwordx2 v[168:169], v162, s[56:57] offset:512 nt
	global_load_dwordx2 v[170:171], v162, s[56:57] offset:1024 nt
	global_load_dwordx2 v[172:173], v162, s[56:57] offset:1536 nt
	global_load_dwordx2 v[174:175], v162, s[56:57] offset:2048 nt
	global_load_dwordx2 v[176:177], v162, s[56:57] offset:2560 nt
	global_load_dwordx2 v[178:179], v162, s[56:57] offset:3072 nt
	global_load_dwordx2 v[180:181], v162, s[56:57] offset:3584 nt
	global_load_dwordx4 v[144:147], v163, s[58:59] nt
	global_load_dwordx4 v[148:151], v163, s[58:59] offset:1024 nt
	global_load_dwordx4 v[152:155], v163, s[58:59] offset:2048 nt
	global_load_dwordx4 v[156:159], v163, s[58:59] offset:3072 nt
	s_add_u32 s10, s58, 0x1000
	s_addc_u32 s11, s59, 0
	global_load_dwordx4 v[182:185], v163, s[10:11] nt
	global_load_dwordx4 v[186:189], v163, s[10:11] offset:1024 nt
	global_load_dwordx4 v[190:193], v163, s[10:11] offset:2048 nt
	global_load_dwordx4 v[194:197], v163, s[10:11] offset:3072 nt
	s_add_u32 s58, s58, 0x10000
	s_addc_u32 s59, s59, 0
	s_add_u32 s56, s56, 0x8000
	s_addc_u32 s57, s57, 0
	v_mov_b32_e32 v250, 0
	v_mov_b32_e32 v251, 0
	v_cvt_pk_bf16_f32 v238, v0, v1
	v_cvt_pk_bf16_f32 v239, v2, v3
	v_fmac_f32_e32 v250, v0, v0
	v_fmac_f32_e32 v251, v1, v1
	v_fmac_f32_e32 v250, v2, v2
	v_fmac_f32_e32 v251, v3, v3
	global_store_dwordx2 v162, v[238:239], s[70:71]
	v_cvt_pk_bf16_f32 v240, v4, v5
	v_cvt_pk_bf16_f32 v241, v6, v7
	v_fmac_f32_e32 v250, v4, v4
	v_fmac_f32_e32 v251, v5, v5
	v_fmac_f32_e32 v250, v6, v6
	v_fmac_f32_e32 v251, v7, v7
	global_store_dwordx2 v162, v[240:241], s[70:71] offset:512
	v_cvt_pk_bf16_f32 v242, v8, v9
	v_cvt_pk_bf16_f32 v243, v10, v11
	v_fmac_f32_e32 v250, v8, v8
	v_fmac_f32_e32 v251, v9, v9
	v_fmac_f32_e32 v250, v10, v10
	v_fmac_f32_e32 v251, v11, v11
	global_store_dwordx2 v162, v[242:243], s[70:71] offset:1024
	v_cvt_pk_bf16_f32 v244, v12, v13
	v_cvt_pk_bf16_f32 v245, v14, v15
	v_fmac_f32_e32 v250, v12, v12
	v_fmac_f32_e32 v251, v13, v13
	v_fmac_f32_e32 v250, v14, v14
	v_fmac_f32_e32 v251, v15, v15
	global_store_dwordx2 v162, v[244:245], s[70:71] offset:1536
	v_cvt_pk_bf16_f32 v238, v16, v17
	v_cvt_pk_bf16_f32 v239, v18, v19
	v_fmac_f32_e32 v250, v16, v16
	v_fmac_f32_e32 v251, v17, v17
	v_fmac_f32_e32 v250, v18, v18
	v_fmac_f32_e32 v251, v19, v19
	global_store_dwordx2 v162, v[238:239], s[70:71] offset:2048
	v_cvt_pk_bf16_f32 v240, v20, v21
	v_cvt_pk_bf16_f32 v241, v22, v23
	v_fmac_f32_e32 v250, v20, v20
	v_fmac_f32_e32 v251, v21, v21
	v_fmac_f32_e32 v250, v22, v22
	v_fmac_f32_e32 v251, v23, v23
	global_store_dwordx2 v162, v[240:241], s[70:71] offset:2560
	v_cvt_pk_bf16_f32 v242, v24, v25
	v_cvt_pk_bf16_f32 v243, v26, v27
	v_fmac_f32_e32 v250, v24, v24
	v_fmac_f32_e32 v251, v25, v25
	v_fmac_f32_e32 v250, v26, v26
	v_fmac_f32_e32 v251, v27, v27
	global_store_dwordx2 v162, v[242:243], s[70:71] offset:3072
	v_cvt_pk_bf16_f32 v244, v28, v29
	v_cvt_pk_bf16_f32 v245, v30, v31
	v_fmac_f32_e32 v250, v28, v28
	v_fmac_f32_e32 v251, v29, v29
	v_fmac_f32_e32 v250, v30, v30
	v_fmac_f32_e32 v251, v31, v31
	global_store_dwordx2 v162, v[244:245], s[70:71] offset:3584
	s_add_u32 s70, s70, 0x8000
	s_addc_u32 s71, s71, 0
	v_add_f32_e32 v250, v250, v251
	s_nop 1
	v_add_f32_dpp v218, v250, v250 quad_perm:[1,0,3,2] row_mask:0xf bank_mask:0xf bound_ctrl:1
	s_nop 1
	v_add_f32_dpp v218, v218, v218 quad_perm:[2,3,0,1] row_mask:0xf bank_mask:0xf bound_ctrl:1
	s_nop 1
	v_add_f32_dpp v218, v218, v218 row_ror:4 row_mask:0xf bank_mask:0xf bound_ctrl:1
	s_nop 1
	v_add_f32_dpp v218, v218, v218 row_ror:8 row_mask:0xf bank_mask:0xf bound_ctrl:1
	s_nop 1
	v_readlane_b32 s8, v218, 0
	v_readlane_b32 s9, v218, 16
	v_readlane_b32 s10, v218, 32
	v_readlane_b32 s11, v218, 48
	s_nop 1
	v_mov_b32_e32 v218, s8
	v_add_f32_e32 v218, s9, v218
	v_mov_b32_e32 v219, s10
	v_add_f32_e32 v219, s11, v219
	v_add_f32_e32 v218, v218, v219
	v_mul_f32_e32 v218, 0x3a000000, v218
	v_add_f32_e32 v218, 0x358637bd, v218
	v_rsq_f32_e32 v218, v218
	s_nop 0
	v_mul_f32_e32 v246, v0, v218
	v_mul_f32_e32 v247, v1, v218
	v_mul_f32_e32 v248, v2, v218
	v_mul_f32_e32 v249, v3, v218
	v_fma_f32 v246, v246, v64, v96
	v_fma_f32 v247, v247, v65, v97
	v_fma_f32 v248, v248, v66, v98
	v_fma_f32 v249, v249, v67, v99
	v_cvt_pk_bf16_f32 v238, v246, v247
	v_cvt_pk_bf16_f32 v239, v248, v249
	global_store_dwordx2 v162, v[238:239], s[72:73]
	v_mul_f32_e32 v246, v4, v218
	v_mul_f32_e32 v247, v5, v218
	v_mul_f32_e32 v248, v6, v218
	v_mul_f32_e32 v249, v7, v218
	v_fma_f32 v246, v246, v68, v100
	v_fma_f32 v247, v247, v69, v101
	v_fma_f32 v248, v248, v70, v102
	v_fma_f32 v249, v249, v71, v103
	v_cvt_pk_bf16_f32 v240, v246, v247
	v_cvt_pk_bf16_f32 v241, v248, v249
	global_store_dwordx2 v162, v[240:241], s[72:73] offset:512
	v_mul_f32_e32 v246, v8, v218
	v_mul_f32_e32 v247, v9, v218
	v_mul_f32_e32 v248, v10, v218
	v_mul_f32_e32 v249, v11, v218
	v_fma_f32 v246, v246, v72, v104
	v_fma_f32 v247, v247, v73, v105
	v_fma_f32 v248, v248, v74, v106
	v_fma_f32 v249, v249, v75, v107
	v_cvt_pk_bf16_f32 v242, v246, v247
	v_cvt_pk_bf16_f32 v243, v248, v249
	global_store_dwordx2 v162, v[242:243], s[72:73] offset:1024
	v_mul_f32_e32 v246, v12, v218
	v_mul_f32_e32 v247, v13, v218
	v_mul_f32_e32 v248, v14, v218
	v_mul_f32_e32 v249, v15, v218
	v_fma_f32 v246, v246, v76, v108
	v_fma_f32 v247, v247, v77, v109
	v_fma_f32 v248, v248, v78, v110
	v_fma_f32 v249, v249, v79, v111
	v_cvt_pk_bf16_f32 v244, v246, v247
	v_cvt_pk_bf16_f32 v245, v248, v249
	global_store_dwordx2 v162, v[244:245], s[72:73] offset:1536
	v_mul_f32_e32 v246, v16, v218
	v_mul_f32_e32 v247, v17, v218
	v_mul_f32_e32 v248, v18, v218
	v_mul_f32_e32 v249, v19, v218
	v_fma_f32 v246, v246, v80, v112
	v_fma_f32 v247, v247, v81, v113
	v_fma_f32 v248, v248, v82, v114
	v_fma_f32 v249, v249, v83, v115
	v_cvt_pk_bf16_f32 v238, v246, v247
	v_cvt_pk_bf16_f32 v239, v248, v249
	global_store_dwordx2 v162, v[238:239], s[72:73] offset:2048
	v_mul_f32_e32 v246, v20, v218
	v_mul_f32_e32 v247, v21, v218
	v_mul_f32_e32 v248, v22, v218
	v_mul_f32_e32 v249, v23, v218
	v_fma_f32 v246, v246, v84, v116
	v_fma_f32 v247, v247, v85, v117
	v_fma_f32 v248, v248, v86, v118
	v_fma_f32 v249, v249, v87, v119
	v_cvt_pk_bf16_f32 v240, v246, v247
	v_cvt_pk_bf16_f32 v241, v248, v249
	global_store_dwordx2 v162, v[240:241], s[72:73] offset:2560
	v_mul_f32_e32 v246, v24, v218
	v_mul_f32_e32 v247, v25, v218
	v_mul_f32_e32 v248, v26, v218
	v_mul_f32_e32 v249, v27, v218
	v_fma_f32 v246, v246, v88, v120
	v_fma_f32 v247, v247, v89, v121
	v_fma_f32 v248, v248, v90, v122
	v_fma_f32 v249, v249, v91, v123
	v_cvt_pk_bf16_f32 v242, v246, v247
	v_cvt_pk_bf16_f32 v243, v248, v249
	global_store_dwordx2 v162, v[242:243], s[72:73] offset:3072
	v_mul_f32_e32 v246, v28, v218
	v_mul_f32_e32 v247, v29, v218
	v_mul_f32_e32 v248, v30, v218
	v_mul_f32_e32 v249, v31, v218
	v_fma_f32 v246, v246, v92, v124
	v_fma_f32 v247, v247, v93, v125
	v_fma_f32 v248, v248, v94, v126
	v_fma_f32 v249, v249, v95, v127
	v_cvt_pk_bf16_f32 v244, v246, v247
	v_cvt_pk_bf16_f32 v245, v248, v249
	global_store_dwordx2 v162, v[244:245], s[72:73] offset:3584
	s_add_u32 s72, s72, 0x8000
	s_addc_u32 s73, s73, 0
	s_add_u32 s76, s76, 1
	s_cmp_lt_u32 s76, 7
	s_cbranch_scc1 .Lmp_V2_loop
	s_waitcnt vmcnt(32)
	v_mov_b32_e32 v250, 0
	v_mov_b32_e32 v251, 0
	v_lshlrev_b32_e32 v246, 16, v128
	v_and_b32_e32 v247, 0xffff0000, v128
	v_lshlrev_b32_e32 v248, 16, v129
	v_and_b32_e32 v249, 0xffff0000, v129
	v_fmac_f32_e32 v250, v246, v246
	v_fmac_f32_e32 v251, v247, v247
	v_fmac_f32_e32 v250, v248, v248
	v_fmac_f32_e32 v251, v249, v249
	v_lshlrev_b32_e32 v246, 16, v130
	v_and_b32_e32 v247, 0xffff0000, v130
	v_lshlrev_b32_e32 v248, 16, v131
	v_and_b32_e32 v249, 0xffff0000, v131
	v_fmac_f32_e32 v250, v246, v246
	v_fmac_f32_e32 v251, v247, v247
	v_fmac_f32_e32 v250, v248, v248
	v_fmac_f32_e32 v251, v249, v249
	v_lshlrev_b32_e32 v246, 16, v132
	v_and_b32_e32 v247, 0xffff0000, v132
	v_lshlrev_b32_e32 v248, 16, v133
	v_and_b32_e32 v249, 0xffff0000, v133
	v_fmac_f32_e32 v250, v246, v246
	v_fmac_f32_e32 v251, v247, v247
	v_fmac_f32_e32 v250, v248, v248
	v_fmac_f32_e32 v251, v249, v249
	v_lshlrev_b32_e32 v246, 16, v134
	v_and_b32_e32 v247, 0xffff0000, v134
	v_lshlrev_b32_e32 v248, 16, v135
	v_and_b32_e32 v249, 0xffff0000, v135
	v_fmac_f32_e32 v250, v246, v246
	v_fmac_f32_e32 v251, v247, v247
	v_fmac_f32_e32 v250, v248, v248
	v_fmac_f32_e32 v251, v249, v249
	v_lshlrev_b32_e32 v246, 16, v136
	v_and_b32_e32 v247, 0xffff0000, v136
	v_lshlrev_b32_e32 v248, 16, v137
	v_and_b32_e32 v249, 0xffff0000, v137
	v_fmac_f32_e32 v250, v246, v246
	v_fmac_f32_e32 v251, v247, v247
	v_fmac_f32_e32 v250, v248, v248
	v_fmac_f32_e32 v251, v249, v249
	v_lshlrev_b32_e32 v246, 16, v138
	v_and_b32_e32 v247, 0xffff0000, v138
	v_lshlrev_b32_e32 v248, 16, v139
	v_and_b32_e32 v249, 0xffff0000, v139
	v_fmac_f32_e32 v250, v246, v246
	v_fmac_f32_e32 v251, v247, v247
	v_fmac_f32_e32 v250, v248, v248
	v_fmac_f32_e32 v251, v249, v249
	v_lshlrev_b32_e32 v246, 16, v140
	v_and_b32_e32 v247, 0xffff0000, v140
	v_lshlrev_b32_e32 v248, 16, v141
	v_and_b32_e32 v249, 0xffff0000, v141
	v_fmac_f32_e32 v250, v246, v246
	v_fmac_f32_e32 v251, v247, v247
	v_fmac_f32_e32 v250, v248, v248
	v_fmac_f32_e32 v251, v249, v249
	v_lshlrev_b32_e32 v246, 16, v142
	v_and_b32_e32 v247, 0xffff0000, v142
	v_lshlrev_b32_e32 v248, 16, v143
	v_and_b32_e32 v249, 0xffff0000, v143
	v_fmac_f32_e32 v250, v246, v246
	v_fmac_f32_e32 v251, v247, v247
	v_fmac_f32_e32 v250, v248, v248
	v_fmac_f32_e32 v251, v249, v249
	v_add_f32_e32 v250, v250, v251
	s_nop 1
	v_add_f32_dpp v218, v250, v250 quad_perm:[1,0,3,2] row_mask:0xf bank_mask:0xf bound_ctrl:1
	s_nop 1
	v_add_f32_dpp v218, v218, v218 quad_perm:[2,3,0,1] row_mask:0xf bank_mask:0xf bound_ctrl:1
	s_nop 1
	v_add_f32_dpp v218, v218, v218 row_ror:4 row_mask:0xf bank_mask:0xf bound_ctrl:1
	s_nop 1
	v_add_f32_dpp v218, v218, v218 row_ror:8 row_mask:0xf bank_mask:0xf bound_ctrl:1
	s_nop 1
	v_readlane_b32 s8, v218, 0
	v_readlane_b32 s9, v218, 16
	v_readlane_b32 s10, v218, 32
	v_readlane_b32 s11, v218, 48
	s_nop 1
	v_mov_b32_e32 v218, s8
	v_add_f32_e32 v218, s9, v218
	v_mov_b32_e32 v219, s10
	v_add_f32_e32 v219, s11, v219
	v_add_f32_e32 v218, v218, v219
	v_mul_f32_e32 v218, 0x3a000000, v218
	v_add_f32_e32 v218, 0x358637bd, v218
	v_rsq_f32_e32 v218, v218
	s_nop 0
	v_lshlrev_b32_e32 v246, 16, v128
	v_and_b32_e32 v247, 0xffff0000, v128
	v_lshlrev_b32_e32 v248, 16, v129
	v_and_b32_e32 v249, 0xffff0000, v129
	v_mul_f32_e32 v246, v246, v218
	v_mul_f32_e32 v247, v247, v218
	v_mul_f32_e32 v248, v248, v218
	v_mul_f32_e32 v249, v249, v218
	v_fma_f32 v0, v246, v32, v198
	v_fma_f32 v1, v247, v33, v199
	v_fma_f32 v2, v248, v34, v200
	v_fma_f32 v3, v249, v35, v201
	v_lshlrev_b32_e32 v246, 16, v130
	v_and_b32_e32 v247, 0xffff0000, v130
	v_lshlrev_b32_e32 v248, 16, v131
	v_and_b32_e32 v249, 0xffff0000, v131
	v_mul_f32_e32 v246, v246, v218
	v_mul_f32_e32 v247, v247, v218
	v_mul_f32_e32 v248, v248, v218
	v_mul_f32_e32 v249, v249, v218
	v_fma_f32 v4, v246, v36, v202
	v_fma_f32 v5, v247, v37, v203
	v_fma_f32 v6, v248, v38, v204
	v_fma_f32 v7, v249, v39, v205
	v_lshlrev_b32_e32 v246, 16, v132
	v_and_b32_e32 v247, 0xffff0000, v132
	v_lshlrev_b32_e32 v248, 16, v133
	v_and_b32_e32 v249, 0xffff0000, v133
	v_mul_f32_e32 v246, v246, v218
	v_mul_f32_e32 v247, v247, v218
	v_mul_f32_e32 v248, v248, v218
	v_mul_f32_e32 v249, v249, v218
	v_fma_f32 v8, v246, v40, v206
	v_fma_f32 v9, v247, v41, v207
	v_fma_f32 v10, v248, v42, v208
	v_fma_f32 v11, v249, v43, v209
	v_lshlrev_b32_e32 v246, 16, v134
	v_and_b32_e32 v247, 0xffff0000, v134
	v_lshlrev_b32_e32 v248, 16, v135
	v_and_b32_e32 v249, 0xffff0000, v135
	v_mul_f32_e32 v246, v246, v218
	v_mul_f32_e32 v247, v247, v218
	v_mul_f32_e32 v248, v248, v218
	v_mul_f32_e32 v249, v249, v218
	v_fma_f32 v12, v246, v44, v210
	v_fma_f32 v13, v247, v45, v211
	v_fma_f32 v14, v248, v46, v212
	v_fma_f32 v15, v249, v47, v213
	v_lshlrev_b32_e32 v246, 16, v136
	v_and_b32_e32 v247, 0xffff0000, v136
	v_lshlrev_b32_e32 v248, 16, v137
	v_and_b32_e32 v249, 0xffff0000, v137
	v_mul_f32_e32 v246, v246, v218
	v_mul_f32_e32 v247, v247, v218
	v_mul_f32_e32 v248, v248, v218
	v_mul_f32_e32 v249, v249, v218
	v_fma_f32 v16, v246, v48, v214
	v_fma_f32 v17, v247, v49, v215
	v_fma_f32 v18, v248, v50, v216
	v_fma_f32 v19, v249, v51, v217
	v_lshlrev_b32_e32 v246, 16, v138
	v_and_b32_e32 v247, 0xffff0000, v138
	v_lshlrev_b32_e32 v248, 16, v139
	v_and_b32_e32 v249, 0xffff0000, v139
	v_mul_f32_e32 v246, v246, v218
	v_mul_f32_e32 v247, v247, v218
	v_mul_f32_e32 v248, v248, v218
	v_mul_f32_e32 v249, v249, v218
	v_fma_f32 v20, v246, v52, v226
	v_fma_f32 v21, v247, v53, v227
	v_fma_f32 v22, v248, v54, v228
	v_fma_f32 v23, v249, v55, v229
	v_lshlrev_b32_e32 v246, 16, v140
	v_and_b32_e32 v247, 0xffff0000, v140
	v_lshlrev_b32_e32 v248, 16, v141
	v_and_b32_e32 v249, 0xffff0000, v141
	v_mul_f32_e32 v246, v246, v218
	v_mul_f32_e32 v247, v247, v218
	v_mul_f32_e32 v248, v248, v218
	v_mul_f32_e32 v249, v249, v218
	v_fma_f32 v24, v246, v56, v230
	v_fma_f32 v25, v247, v57, v231
	v_fma_f32 v26, v248, v58, v232
	v_fma_f32 v27, v249, v59, v233
	v_lshlrev_b32_e32 v246, 16, v142
	v_and_b32_e32 v247, 0xffff0000, v142
	v_lshlrev_b32_e32 v248, 16, v143
	v_and_b32_e32 v249, 0xffff0000, v143
	v_mul_f32_e32 v246, v246, v218
	v_mul_f32_e32 v247, v247, v218
	v_mul_f32_e32 v248, v248, v218
	v_mul_f32_e32 v249, v249, v218
	v_fma_f32 v28, v246, v60, v234
	v_fma_f32 v29, v247, v61, v235
	v_fma_f32 v30, v248, v62, v236
	v_fma_f32 v31, v249, v63, v237
	v_mov_b32_e32 v250, 0
	v_mov_b32_e32 v251, 0
	v_cvt_pk_bf16_f32 v238, v0, v1
	v_cvt_pk_bf16_f32 v239, v2, v3
	v_fmac_f32_e32 v250, v0, v0
	v_fmac_f32_e32 v251, v1, v1
	v_fmac_f32_e32 v250, v2, v2
	v_fmac_f32_e32 v251, v3, v3
	global_store_dwordx2 v162, v[238:239], s[70:71]
	v_cvt_pk_bf16_f32 v240, v4, v5
	v_cvt_pk_bf16_f32 v241, v6, v7
	v_fmac_f32_e32 v250, v4, v4
	v_fmac_f32_e32 v251, v5, v5
	v_fmac_f32_e32 v250, v6, v6
	v_fmac_f32_e32 v251, v7, v7
	global_store_dwordx2 v162, v[240:241], s[70:71] offset:512
	v_cvt_pk_bf16_f32 v242, v8, v9
	v_cvt_pk_bf16_f32 v243, v10, v11
	v_fmac_f32_e32 v250, v8, v8
	v_fmac_f32_e32 v251, v9, v9
	v_fmac_f32_e32 v250, v10, v10
	v_fmac_f32_e32 v251, v11, v11
	global_store_dwordx2 v162, v[242:243], s[70:71] offset:1024
	v_cvt_pk_bf16_f32 v244, v12, v13
	v_cvt_pk_bf16_f32 v245, v14, v15
	v_fmac_f32_e32 v250, v12, v12
	v_fmac_f32_e32 v251, v13, v13
	v_fmac_f32_e32 v250, v14, v14
	v_fmac_f32_e32 v251, v15, v15
	global_store_dwordx2 v162, v[244:245], s[70:71] offset:1536
	v_cvt_pk_bf16_f32 v238, v16, v17
	v_cvt_pk_bf16_f32 v239, v18, v19
	v_fmac_f32_e32 v250, v16, v16
	v_fmac_f32_e32 v251, v17, v17
	v_fmac_f32_e32 v250, v18, v18
	v_fmac_f32_e32 v251, v19, v19
	global_store_dwordx2 v162, v[238:239], s[70:71] offset:2048
	v_cvt_pk_bf16_f32 v240, v20, v21
	v_cvt_pk_bf16_f32 v241, v22, v23
	v_fmac_f32_e32 v250, v20, v20
	v_fmac_f32_e32 v251, v21, v21
	v_fmac_f32_e32 v250, v22, v22
	v_fmac_f32_e32 v251, v23, v23
	global_store_dwordx2 v162, v[240:241], s[70:71] offset:2560
	v_cvt_pk_bf16_f32 v242, v24, v25
	v_cvt_pk_bf16_f32 v243, v26, v27
	v_fmac_f32_e32 v250, v24, v24
	v_fmac_f32_e32 v251, v25, v25
	v_fmac_f32_e32 v250, v26, v26
	v_fmac_f32_e32 v251, v27, v27
	global_store_dwordx2 v162, v[242:243], s[70:71] offset:3072
	v_cvt_pk_bf16_f32 v244, v28, v29
	v_cvt_pk_bf16_f32 v245, v30, v31
	v_fmac_f32_e32 v250, v28, v28
	v_fmac_f32_e32 v251, v29, v29
	v_fmac_f32_e32 v250, v30, v30
	v_fmac_f32_e32 v251, v31, v31
	global_store_dwordx2 v162, v[244:245], s[70:71] offset:3584
	s_add_u32 s70, s70, 0x8000
	s_addc_u32 s71, s71, 0
	v_add_f32_e32 v250, v250, v251
	s_nop 1
	v_add_f32_dpp v218, v250, v250 quad_perm:[1,0,3,2] row_mask:0xf bank_mask:0xf bound_ctrl:1
	s_nop 1
	v_add_f32_dpp v218, v218, v218 quad_perm:[2,3,0,1] row_mask:0xf bank_mask:0xf bound_ctrl:1
	s_nop 1
	v_add_f32_dpp v218, v218, v218 row_ror:4 row_mask:0xf bank_mask:0xf bound_ctrl:1
	s_nop 1
	v_add_f32_dpp v218, v218, v218 row_ror:8 row_mask:0xf bank_mask:0xf bound_ctrl:1
	s_nop 1
	v_readlane_b32 s8, v218, 0
	v_readlane_b32 s9, v218, 16
	v_readlane_b32 s10, v218, 32
	v_readlane_b32 s11, v218, 48
	s_nop 1
	v_mov_b32_e32 v218, s8
	v_add_f32_e32 v218, s9, v218
	v_mov_b32_e32 v219, s10
	v_add_f32_e32 v219, s11, v219
	v_add_f32_e32 v218, v218, v219
	v_mul_f32_e32 v218, 0x3a000000, v218
	v_add_f32_e32 v218, 0x358637bd, v218
	v_rsq_f32_e32 v218, v218
	s_nop 0
	v_mul_f32_e32 v246, v0, v218
	v_mul_f32_e32 v247, v1, v218
	v_mul_f32_e32 v248, v2, v218
	v_mul_f32_e32 v249, v3, v218
	v_fma_f32 v246, v246, v64, v96
	v_fma_f32 v247, v247, v65, v97
	v_fma_f32 v248, v248, v66, v98
	v_fma_f32 v249, v249, v67, v99
	v_cvt_pk_bf16_f32 v238, v246, v247
	v_cvt_pk_bf16_f32 v239, v248, v249
	global_store_dwordx2 v162, v[238:239], s[72:73]
	v_mul_f32_e32 v246, v4, v218
	v_mul_f32_e32 v247, v5, v218
	v_mul_f32_e32 v248, v6, v218
	v_mul_f32_e32 v249, v7, v218
	v_fma_f32 v246, v246, v68, v100
	v_fma_f32 v247, v247, v69, v101
	v_fma_f32 v248, v248, v70, v102
	v_fma_f32 v249, v249, v71, v103
	v_cvt_pk_bf16_f32 v240, v246, v247
	v_cvt_pk_bf16_f32 v241, v248, v249
	global_store_dwordx2 v162, v[240:241], s[72:73] offset:512
	v_mul_f32_e32 v246, v8, v218
	v_mul_f32_e32 v247, v9, v218
	v_mul_f32_e32 v248, v10, v218
	v_mul_f32_e32 v249, v11, v218
	v_fma_f32 v246, v246, v72, v104
	v_fma_f32 v247, v247, v73, v105
	v_fma_f32 v248, v248, v74, v106
	v_fma_f32 v249, v249, v75, v107
	v_cvt_pk_bf16_f32 v242, v246, v247
	v_cvt_pk_bf16_f32 v243, v248, v249
	global_store_dwordx2 v162, v[242:243], s[72:73] offset:1024
	v_mul_f32_e32 v246, v12, v218
	v_mul_f32_e32 v247, v13, v218
	v_mul_f32_e32 v248, v14, v218
	v_mul_f32_e32 v249, v15, v218
	v_fma_f32 v246, v246, v76, v108
	v_fma_f32 v247, v247, v77, v109
	v_fma_f32 v248, v248, v78, v110
	v_fma_f32 v249, v249, v79, v111
	v_cvt_pk_bf16_f32 v244, v246, v247
	v_cvt_pk_bf16_f32 v245, v248, v249
	global_store_dwordx2 v162, v[244:245], s[72:73] offset:1536
	v_mul_f32_e32 v246, v16, v218
	v_mul_f32_e32 v247, v17, v218
	v_mul_f32_e32 v248, v18, v218
	v_mul_f32_e32 v249, v19, v218
	v_fma_f32 v246, v246, v80, v112
	v_fma_f32 v247, v247, v81, v113
	v_fma_f32 v248, v248, v82, v114
	v_fma_f32 v249, v249, v83, v115
	v_cvt_pk_bf16_f32 v238, v246, v247
	v_cvt_pk_bf16_f32 v239, v248, v249
	global_store_dwordx2 v162, v[238:239], s[72:73] offset:2048
	v_mul_f32_e32 v246, v20, v218
	v_mul_f32_e32 v247, v21, v218
	v_mul_f32_e32 v248, v22, v218
	v_mul_f32_e32 v249, v23, v218
	v_fma_f32 v246, v246, v84, v116
	v_fma_f32 v247, v247, v85, v117
	v_fma_f32 v248, v248, v86, v118
	v_fma_f32 v249, v249, v87, v119
	v_cvt_pk_bf16_f32 v240, v246, v247
	v_cvt_pk_bf16_f32 v241, v248, v249
	global_store_dwordx2 v162, v[240:241], s[72:73] offset:2560
	v_mul_f32_e32 v246, v24, v218
	v_mul_f32_e32 v247, v25, v218
	v_mul_f32_e32 v248, v26, v218
	v_mul_f32_e32 v249, v27, v218
	v_fma_f32 v246, v246, v88, v120
	v_fma_f32 v247, v247, v89, v121
	v_fma_f32 v248, v248, v90, v122
	v_fma_f32 v249, v249, v91, v123
	v_cvt_pk_bf16_f32 v242, v246, v247
	v_cvt_pk_bf16_f32 v243, v248, v249
	global_store_dwordx2 v162, v[242:243], s[72:73] offset:3072
	v_mul_f32_e32 v246, v28, v218
	v_mul_f32_e32 v247, v29, v218
	v_mul_f32_e32 v248, v30, v218
	v_mul_f32_e32 v249, v31, v218
	v_fma_f32 v246, v246, v92, v124
	v_fma_f32 v247, v247, v93, v125
	v_fma_f32 v248, v248, v94, v126
	v_fma_f32 v249, v249, v95, v127
	v_cvt_pk_bf16_f32 v244, v246, v247
	v_cvt_pk_bf16_f32 v245, v248, v249
	global_store_dwordx2 v162, v[244:245], s[72:73] offset:3584
	s_add_u32 s72, s72, 0x8000
	s_addc_u32 s73, s73, 0
	s_waitcnt vmcnt(32)
	v_mov_b32_e32 v250, 0
	v_mov_b32_e32 v251, 0
	v_lshlrev_b32_e32 v246, 16, v166
	v_and_b32_e32 v247, 0xffff0000, v166
	v_lshlrev_b32_e32 v248, 16, v167
	v_and_b32_e32 v249, 0xffff0000, v167
	v_fmac_f32_e32 v250, v246, v246
	v_fmac_f32_e32 v251, v247, v247
	v_fmac_f32_e32 v250, v248, v248
	v_fmac_f32_e32 v251, v249, v249
	v_lshlrev_b32_e32 v246, 16, v168
	v_and_b32_e32 v247, 0xffff0000, v168
	v_lshlrev_b32_e32 v248, 16, v169
	v_and_b32_e32 v249, 0xffff0000, v169
	v_fmac_f32_e32 v250, v246, v246
	v_fmac_f32_e32 v251, v247, v247
	v_fmac_f32_e32 v250, v248, v248
	v_fmac_f32_e32 v251, v249, v249
	v_lshlrev_b32_e32 v246, 16, v170
	v_and_b32_e32 v247, 0xffff0000, v170
	v_lshlrev_b32_e32 v248, 16, v171
	v_and_b32_e32 v249, 0xffff0000, v171
	v_fmac_f32_e32 v250, v246, v246
	v_fmac_f32_e32 v251, v247, v247
	v_fmac_f32_e32 v250, v248, v248
	v_fmac_f32_e32 v251, v249, v249
	v_lshlrev_b32_e32 v246, 16, v172
	v_and_b32_e32 v247, 0xffff0000, v172
	v_lshlrev_b32_e32 v248, 16, v173
	v_and_b32_e32 v249, 0xffff0000, v173
	v_fmac_f32_e32 v250, v246, v246
	v_fmac_f32_e32 v251, v247, v247
	v_fmac_f32_e32 v250, v248, v248
	v_fmac_f32_e32 v251, v249, v249
	v_lshlrev_b32_e32 v246, 16, v174
	v_and_b32_e32 v247, 0xffff0000, v174
	v_lshlrev_b32_e32 v248, 16, v175
	v_and_b32_e32 v249, 0xffff0000, v175
	v_fmac_f32_e32 v250, v246, v246
	v_fmac_f32_e32 v251, v247, v247
	v_fmac_f32_e32 v250, v248, v248
	v_fmac_f32_e32 v251, v249, v249
	v_lshlrev_b32_e32 v246, 16, v176
	v_and_b32_e32 v247, 0xffff0000, v176
	v_lshlrev_b32_e32 v248, 16, v177
	v_and_b32_e32 v249, 0xffff0000, v177
	v_fmac_f32_e32 v250, v246, v246
	v_fmac_f32_e32 v251, v247, v247
	v_fmac_f32_e32 v250, v248, v248
	v_fmac_f32_e32 v251, v249, v249
	v_lshlrev_b32_e32 v246, 16, v178
	v_and_b32_e32 v247, 0xffff0000, v178
	v_lshlrev_b32_e32 v248, 16, v179
	v_and_b32_e32 v249, 0xffff0000, v179
	v_fmac_f32_e32 v250, v246, v246
	v_fmac_f32_e32 v251, v247, v247
	v_fmac_f32_e32 v250, v248, v248
	v_fmac_f32_e32 v251, v249, v249
	v_lshlrev_b32_e32 v246, 16, v180
	v_and_b32_e32 v247, 0xffff0000, v180
	v_lshlrev_b32_e32 v248, 16, v181
	v_and_b32_e32 v249, 0xffff0000, v181
	v_fmac_f32_e32 v250, v246, v246
	v_fmac_f32_e32 v251, v247, v247
	v_fmac_f32_e32 v250, v248, v248
	v_fmac_f32_e32 v251, v249, v249
	v_add_f32_e32 v250, v250, v251
	s_nop 1
	v_add_f32_dpp v218, v250, v250 quad_perm:[1,0,3,2] row_mask:0xf bank_mask:0xf bound_ctrl:1
	s_nop 1
	v_add_f32_dpp v218, v218, v218 quad_perm:[2,3,0,1] row_mask:0xf bank_mask:0xf bound_ctrl:1
	s_nop 1
	v_add_f32_dpp v218, v218, v218 row_ror:4 row_mask:0xf bank_mask:0xf bound_ctrl:1
	s_nop 1
	v_add_f32_dpp v218, v218, v218 row_ror:8 row_mask:0xf bank_mask:0xf bound_ctrl:1
	s_nop 1
	v_readlane_b32 s8, v218, 0
	v_readlane_b32 s9, v218, 16
	v_readlane_b32 s10, v218, 32
	v_readlane_b32 s11, v218, 48
	s_nop 1
	v_mov_b32_e32 v218, s8
	v_add_f32_e32 v218, s9, v218
	v_mov_b32_e32 v219, s10
	v_add_f32_e32 v219, s11, v219
	v_add_f32_e32 v218, v218, v219
	v_mul_f32_e32 v218, 0x3a000000, v218
	v_add_f32_e32 v218, 0x358637bd, v218
	v_rsq_f32_e32 v218, v218
	s_nop 0
	v_lshlrev_b32_e32 v246, 16, v166
	v_and_b32_e32 v247, 0xffff0000, v166
	v_lshlrev_b32_e32 v248, 16, v167
	v_and_b32_e32 v249, 0xffff0000, v167
	v_mul_f32_e32 v246, v246, v218
	v_mul_f32_e32 v247, v247, v218
	v_mul_f32_e32 v248, v248, v218
	v_mul_f32_e32 v249, v249, v218
	v_fma_f32 v0, v246, v32, v144
	v_fma_f32 v1, v247, v33, v145
	v_fma_f32 v2, v248, v34, v146
	v_fma_f32 v3, v249, v35, v147
	v_lshlrev_b32_e32 v246, 16, v168
	v_and_b32_e32 v247, 0xffff0000, v168
	v_lshlrev_b32_e32 v248, 16, v169
	v_and_b32_e32 v249, 0xffff0000, v169
	v_mul_f32_e32 v246, v246, v218
	v_mul_f32_e32 v247, v247, v218
	v_mul_f32_e32 v248, v248, v218
	v_mul_f32_e32 v249, v249, v218
	v_fma_f32 v4, v246, v36, v148
	v_fma_f32 v5, v247, v37, v149
	v_fma_f32 v6, v248, v38, v150
	v_fma_f32 v7, v249, v39, v151
	v_lshlrev_b32_e32 v246, 16, v170
	v_and_b32_e32 v247, 0xffff0000, v170
	v_lshlrev_b32_e32 v248, 16, v171
	v_and_b32_e32 v249, 0xffff0000, v171
	v_mul_f32_e32 v246, v246, v218
	v_mul_f32_e32 v247, v247, v218
	v_mul_f32_e32 v248, v248, v218
	v_mul_f32_e32 v249, v249, v218
	v_fma_f32 v8, v246, v40, v152
	v_fma_f32 v9, v247, v41, v153
	v_fma_f32 v10, v248, v42, v154
	v_fma_f32 v11, v249, v43, v155
	v_lshlrev_b32_e32 v246, 16, v172
	v_and_b32_e32 v247, 0xffff0000, v172
	v_lshlrev_b32_e32 v248, 16, v173
	v_and_b32_e32 v249, 0xffff0000, v173
	v_mul_f32_e32 v246, v246, v218
	v_mul_f32_e32 v247, v247, v218
	v_mul_f32_e32 v248, v248, v218
	v_mul_f32_e32 v249, v249, v218
	v_fma_f32 v12, v246, v44, v156
	v_fma_f32 v13, v247, v45, v157
	v_fma_f32 v14, v248, v46, v158
	v_fma_f32 v15, v249, v47, v159
	v_lshlrev_b32_e32 v246, 16, v174
	v_and_b32_e32 v247, 0xffff0000, v174
	v_lshlrev_b32_e32 v248, 16, v175
	v_and_b32_e32 v249, 0xffff0000, v175
	v_mul_f32_e32 v246, v246, v218
	v_mul_f32_e32 v247, v247, v218
	v_mul_f32_e32 v248, v248, v218
	v_mul_f32_e32 v249, v249, v218
	v_fma_f32 v16, v246, v48, v182
	v_fma_f32 v17, v247, v49, v183
	v_fma_f32 v18, v248, v50, v184
	v_fma_f32 v19, v249, v51, v185
	v_lshlrev_b32_e32 v246, 16, v176
	v_and_b32_e32 v247, 0xffff0000, v176
	v_lshlrev_b32_e32 v248, 16, v177
	v_and_b32_e32 v249, 0xffff0000, v177
	v_mul_f32_e32 v246, v246, v218
	v_mul_f32_e32 v247, v247, v218
	v_mul_f32_e32 v248, v248, v218
	v_mul_f32_e32 v249, v249, v218
	v_fma_f32 v20, v246, v52, v186
	v_fma_f32 v21, v247, v53, v187
	v_fma_f32 v22, v248, v54, v188
	v_fma_f32 v23, v249, v55, v189
	v_lshlrev_b32_e32 v246, 16, v178
	v_and_b32_e32 v247, 0xffff0000, v178
	v_lshlrev_b32_e32 v248, 16, v179
	v_and_b32_e32 v249, 0xffff0000, v179
	v_mul_f32_e32 v246, v246, v218
	v_mul_f32_e32 v247, v247, v218
	v_mul_f32_e32 v248, v248, v218
	v_mul_f32_e32 v249, v249, v218
	v_fma_f32 v24, v246, v56, v190
	v_fma_f32 v25, v247, v57, v191
	v_fma_f32 v26, v248, v58, v192
	v_fma_f32 v27, v249, v59, v193
	v_lshlrev_b32_e32 v246, 16, v180
	v_and_b32_e32 v247, 0xffff0000, v180
	v_lshlrev_b32_e32 v248, 16, v181
	v_and_b32_e32 v249, 0xffff0000, v181
	v_mul_f32_e32 v246, v246, v218
	v_mul_f32_e32 v247, v247, v218
	v_mul_f32_e32 v248, v248, v218
	v_mul_f32_e32 v249, v249, v218
	v_fma_f32 v28, v246, v60, v194
	v_fma_f32 v29, v247, v61, v195
	v_fma_f32 v30, v248, v62, v196
	v_fma_f32 v31, v249, v63, v197
	v_mov_b32_e32 v250, 0
	v_mov_b32_e32 v251, 0
	v_cvt_pk_bf16_f32 v238, v0, v1
	v_cvt_pk_bf16_f32 v239, v2, v3
	v_fmac_f32_e32 v250, v0, v0
	v_fmac_f32_e32 v251, v1, v1
	v_fmac_f32_e32 v250, v2, v2
	v_fmac_f32_e32 v251, v3, v3
	global_store_dwordx2 v162, v[238:239], s[70:71]
	v_cvt_pk_bf16_f32 v240, v4, v5
	v_cvt_pk_bf16_f32 v241, v6, v7
	v_fmac_f32_e32 v250, v4, v4
	v_fmac_f32_e32 v251, v5, v5
	v_fmac_f32_e32 v250, v6, v6
	v_fmac_f32_e32 v251, v7, v7
	global_store_dwordx2 v162, v[240:241], s[70:71] offset:512
	v_cvt_pk_bf16_f32 v242, v8, v9
	v_cvt_pk_bf16_f32 v243, v10, v11
	v_fmac_f32_e32 v250, v8, v8
	v_fmac_f32_e32 v251, v9, v9
	v_fmac_f32_e32 v250, v10, v10
	v_fmac_f32_e32 v251, v11, v11
	global_store_dwordx2 v162, v[242:243], s[70:71] offset:1024
	v_cvt_pk_bf16_f32 v244, v12, v13
	v_cvt_pk_bf16_f32 v245, v14, v15
	v_fmac_f32_e32 v250, v12, v12
	v_fmac_f32_e32 v251, v13, v13
	v_fmac_f32_e32 v250, v14, v14
	v_fmac_f32_e32 v251, v15, v15
	global_store_dwordx2 v162, v[244:245], s[70:71] offset:1536
	v_cvt_pk_bf16_f32 v238, v16, v17
	v_cvt_pk_bf16_f32 v239, v18, v19
	v_fmac_f32_e32 v250, v16, v16
	v_fmac_f32_e32 v251, v17, v17
	v_fmac_f32_e32 v250, v18, v18
	v_fmac_f32_e32 v251, v19, v19
	global_store_dwordx2 v162, v[238:239], s[70:71] offset:2048
	v_cvt_pk_bf16_f32 v240, v20, v21
	v_cvt_pk_bf16_f32 v241, v22, v23
	v_fmac_f32_e32 v250, v20, v20
	v_fmac_f32_e32 v251, v21, v21
	v_fmac_f32_e32 v250, v22, v22
	v_fmac_f32_e32 v251, v23, v23
	global_store_dwordx2 v162, v[240:241], s[70:71] offset:2560
	v_cvt_pk_bf16_f32 v242, v24, v25
	v_cvt_pk_bf16_f32 v243, v26, v27
	v_fmac_f32_e32 v250, v24, v24
	v_fmac_f32_e32 v251, v25, v25
	v_fmac_f32_e32 v250, v26, v26
	v_fmac_f32_e32 v251, v27, v27
	global_store_dwordx2 v162, v[242:243], s[70:71] offset:3072
	v_cvt_pk_bf16_f32 v244, v28, v29
	v_cvt_pk_bf16_f32 v245, v30, v31
	v_fmac_f32_e32 v250, v28, v28
	v_fmac_f32_e32 v251, v29, v29
	v_fmac_f32_e32 v250, v30, v30
	v_fmac_f32_e32 v251, v31, v31
	global_store_dwordx2 v162, v[244:245], s[70:71] offset:3584
	s_add_u32 s70, s70, 0x8000
	s_addc_u32 s71, s71, 0
	v_add_f32_e32 v250, v250, v251
	s_nop 1
	v_add_f32_dpp v218, v250, v250 quad_perm:[1,0,3,2] row_mask:0xf bank_mask:0xf bound_ctrl:1
	s_nop 1
	v_add_f32_dpp v218, v218, v218 quad_perm:[2,3,0,1] row_mask:0xf bank_mask:0xf bound_ctrl:1
	s_nop 1
	v_add_f32_dpp v218, v218, v218 row_ror:4 row_mask:0xf bank_mask:0xf bound_ctrl:1
	s_nop 1
	v_add_f32_dpp v218, v218, v218 row_ror:8 row_mask:0xf bank_mask:0xf bound_ctrl:1
	s_nop 1
	v_readlane_b32 s8, v218, 0
	v_readlane_b32 s9, v218, 16
	v_readlane_b32 s10, v218, 32
	v_readlane_b32 s11, v218, 48
	s_nop 1
	v_mov_b32_e32 v218, s8
	v_add_f32_e32 v218, s9, v218
	v_mov_b32_e32 v219, s10
	v_add_f32_e32 v219, s11, v219
	v_add_f32_e32 v218, v218, v219
	v_mul_f32_e32 v218, 0x3a000000, v218
	v_add_f32_e32 v218, 0x358637bd, v218
	v_rsq_f32_e32 v218, v218
	s_nop 0
	v_mul_f32_e32 v246, v0, v218
	v_mul_f32_e32 v247, v1, v218
	v_mul_f32_e32 v248, v2, v218
	v_mul_f32_e32 v249, v3, v218
	v_fma_f32 v246, v246, v64, v96
	v_fma_f32 v247, v247, v65, v97
	v_fma_f32 v248, v248, v66, v98
	v_fma_f32 v249, v249, v67, v99
	v_cvt_pk_bf16_f32 v238, v246, v247
	v_cvt_pk_bf16_f32 v239, v248, v249
	global_store_dwordx2 v162, v[238:239], s[72:73]
	v_mul_f32_e32 v246, v4, v218
	v_mul_f32_e32 v247, v5, v218
	v_mul_f32_e32 v248, v6, v218
	v_mul_f32_e32 v249, v7, v218
	v_fma_f32 v246, v246, v68, v100
	v_fma_f32 v247, v247, v69, v101
	v_fma_f32 v248, v248, v70, v102
	v_fma_f32 v249, v249, v71, v103
	v_cvt_pk_bf16_f32 v240, v246, v247
	v_cvt_pk_bf16_f32 v241, v248, v249
	global_store_dwordx2 v162, v[240:241], s[72:73] offset:512
	v_mul_f32_e32 v246, v8, v218
	v_mul_f32_e32 v247, v9, v218
	v_mul_f32_e32 v248, v10, v218
	v_mul_f32_e32 v249, v11, v218
	v_fma_f32 v246, v246, v72, v104
	v_fma_f32 v247, v247, v73, v105
	v_fma_f32 v248, v248, v74, v106
	v_fma_f32 v249, v249, v75, v107
	v_cvt_pk_bf16_f32 v242, v246, v247
	v_cvt_pk_bf16_f32 v243, v248, v249
	global_store_dwordx2 v162, v[242:243], s[72:73] offset:1024
	v_mul_f32_e32 v246, v12, v218
	v_mul_f32_e32 v247, v13, v218
	v_mul_f32_e32 v248, v14, v218
	v_mul_f32_e32 v249, v15, v218
	v_fma_f32 v246, v246, v76, v108
	v_fma_f32 v247, v247, v77, v109
	v_fma_f32 v248, v248, v78, v110
	v_fma_f32 v249, v249, v79, v111
	v_cvt_pk_bf16_f32 v244, v246, v247
	v_cvt_pk_bf16_f32 v245, v248, v249
	global_store_dwordx2 v162, v[244:245], s[72:73] offset:1536
	v_mul_f32_e32 v246, v16, v218
	v_mul_f32_e32 v247, v17, v218
	v_mul_f32_e32 v248, v18, v218
	v_mul_f32_e32 v249, v19, v218
	v_fma_f32 v246, v246, v80, v112
	v_fma_f32 v247, v247, v81, v113
	v_fma_f32 v248, v248, v82, v114
	v_fma_f32 v249, v249, v83, v115
	v_cvt_pk_bf16_f32 v238, v246, v247
	v_cvt_pk_bf16_f32 v239, v248, v249
	global_store_dwordx2 v162, v[238:239], s[72:73] offset:2048
	v_mul_f32_e32 v246, v20, v218
	v_mul_f32_e32 v247, v21, v218
	v_mul_f32_e32 v248, v22, v218
	v_mul_f32_e32 v249, v23, v218
	v_fma_f32 v246, v246, v84, v116
	v_fma_f32 v247, v247, v85, v117
	v_fma_f32 v248, v248, v86, v118
	v_fma_f32 v249, v249, v87, v119
	v_cvt_pk_bf16_f32 v240, v246, v247
	v_cvt_pk_bf16_f32 v241, v248, v249
	global_store_dwordx2 v162, v[240:241], s[72:73] offset:2560
	v_mul_f32_e32 v246, v24, v218
	v_mul_f32_e32 v247, v25, v218
	v_mul_f32_e32 v248, v26, v218
	v_mul_f32_e32 v249, v27, v218
	v_fma_f32 v246, v246, v88, v120
	v_fma_f32 v247, v247, v89, v121
	v_fma_f32 v248, v248, v90, v122
	v_fma_f32 v249, v249, v91, v123
	v_cvt_pk_bf16_f32 v242, v246, v247
	v_cvt_pk_bf16_f32 v243, v248, v249
	global_store_dwordx2 v162, v[242:243], s[72:73] offset:3072
	v_mul_f32_e32 v246, v28, v218
	v_mul_f32_e32 v247, v29, v218
	v_mul_f32_e32 v248, v30, v218
	v_mul_f32_e32 v249, v31, v218
	v_fma_f32 v246, v246, v92, v124
	v_fma_f32 v247, v247, v93, v125
	v_fma_f32 v248, v248, v94, v126
	v_fma_f32 v249, v249, v95, v127
	v_cvt_pk_bf16_f32 v244, v246, v247
	v_cvt_pk_bf16_f32 v245, v248, v249
	global_store_dwordx2 v162, v[244:245], s[72:73] offset:3584
	s_add_u32 s72, s72, 0x8000
	s_addc_u32 s73, s73, 0
	s_branch .Lmp_done

.Lmp_V3_loop:
	s_waitcnt vmcnt(24)
	v_mov_b32_e32 v250, 0
	v_mov_b32_e32 v251, 0
	v_lshlrev_b32_e32 v246, 16, v128
	v_and_b32_e32 v247, 0xffff0000, v128
	v_lshlrev_b32_e32 v248, 16, v129
	v_and_b32_e32 v249, 0xffff0000, v129
	v_fmac_f32_e32 v250, v246, v246
	v_fmac_f32_e32 v251, v247, v247
	v_fmac_f32_e32 v250, v248, v248
	v_fmac_f32_e32 v251, v249, v249
	v_lshlrev_b32_e32 v246, 16, v130
	v_and_b32_e32 v247, 0xffff0000, v130
	v_lshlrev_b32_e32 v248, 16, v131
	v_and_b32_e32 v249, 0xffff0000, v131
	v_fmac_f32_e32 v250, v246, v246
	v_fmac_f32_e32 v251, v247, v247
	v_fmac_f32_e32 v250, v248, v248
	v_fmac_f32_e32 v251, v249, v249
	v_lshlrev_b32_e32 v246, 16, v132
	v_and_b32_e32 v247, 0xffff0000, v132
	v_lshlrev_b32_e32 v248, 16, v133
	v_and_b32_e32 v249, 0xffff0000, v133
	v_fmac_f32_e32 v250, v246, v246
	v_fmac_f32_e32 v251, v247, v247
	v_fmac_f32_e32 v250, v248, v248
	v_fmac_f32_e32 v251, v249, v249
	v_lshlrev_b32_e32 v246, 16, v134
	v_and_b32_e32 v247, 0xffff0000, v134
	v_lshlrev_b32_e32 v248, 16, v135
	v_and_b32_e32 v249, 0xffff0000, v135
	v_fmac_f32_e32 v250, v246, v246
	v_fmac_f32_e32 v251, v247, v247
	v_fmac_f32_e32 v250, v248, v248
	v_fmac_f32_e32 v251, v249, v249
	v_lshlrev_b32_e32 v246, 16, v136
	v_and_b32_e32 v247, 0xffff0000, v136
	v_lshlrev_b32_e32 v248, 16, v137
	v_and_b32_e32 v249, 0xffff0000, v137
	v_fmac_f32_e32 v250, v246, v246
	v_fmac_f32_e32 v251, v247, v247
	v_fmac_f32_e32 v250, v248, v248
	v_fmac_f32_e32 v251, v249, v249
	v_lshlrev_b32_e32 v246, 16, v138
	v_and_b32_e32 v247, 0xffff0000, v138
	v_lshlrev_b32_e32 v248, 16, v139
	v_and_b32_e32 v249, 0xffff0000, v139
	v_fmac_f32_e32 v250, v246, v246
	v_fmac_f32_e32 v251, v247, v247
	v_fmac_f32_e32 v250, v248, v248
	v_fmac_f32_e32 v251, v249, v249
	v_lshlrev_b32_e32 v246, 16, v140
	v_and_b32_e32 v247, 0xffff0000, v140
	v_lshlrev_b32_e32 v248, 16, v141
	v_and_b32_e32 v249, 0xffff0000, v141
	v_fmac_f32_e32 v250, v246, v246
	v_fmac_f32_e32 v251, v247, v247
	v_fmac_f32_e32 v250, v248, v248
	v_fmac_f32_e32 v251, v249, v249
	v_lshlrev_b32_e32 v246, 16, v142
	v_and_b32_e32 v247, 0xffff0000, v142
	v_lshlrev_b32_e32 v248, 16, v143
	v_and_b32_e32 v249, 0xffff0000, v143
	v_fmac_f32_e32 v250, v246, v246
	v_fmac_f32_e32 v251, v247, v247
	v_fmac_f32_e32 v250, v248, v248
	v_fmac_f32_e32 v251, v249, v249
	v_add_f32_e32 v250, v250, v251
	s_nop 1
	v_add_f32_dpp v218, v250, v250 quad_perm:[1,0,3,2] row_mask:0xf bank_mask:0xf bound_ctrl:1
	s_nop 1
	v_add_f32_dpp v218, v218, v218 quad_perm:[2,3,0,1] row_mask:0xf bank_mask:0xf bound_ctrl:1
	s_nop 1
	v_add_f32_dpp v218, v218, v218 row_ror:4 row_mask:0xf bank_mask:0xf bound_ctrl:1
	s_nop 1
	v_add_f32_dpp v218, v218, v218 row_ror:8 row_mask:0xf bank_mask:0xf bound_ctrl:1
	s_nop 1
	v_readlane_b32 s8, v218, 0
	v_readlane_b32 s9, v218, 16
	v_readlane_b32 s10, v218, 32
	v_readlane_b32 s11, v218, 48
	s_nop 1
	v_mov_b32_e32 v218, s8
	v_add_f32_e32 v218, s9, v218
	v_mov_b32_e32 v219, s10
	v_add_f32_e32 v219, s11, v219
	v_add_f32_e32 v218, v218, v219
	v_mul_f32_e32 v218, 0x3a000000, v218
	v_add_f32_e32 v218, 0x358637bd, v218
	v_rsq_f32_e32 v218, v218
	s_nop 0
	v_lshlrev_b32_e32 v246, 16, v128
	v_and_b32_e32 v247, 0xffff0000, v128
	v_lshlrev_b32_e32 v248, 16, v129
	v_and_b32_e32 v249, 0xffff0000, v129
	v_mul_f32_e32 v246, v246, v218
	v_mul_f32_e32 v247, v247, v218
	v_mul_f32_e32 v248, v248, v218
	v_mul_f32_e32 v249, v249, v218
	v_lshlrev_b32_e32 v0, 16, v144
	v_and_b32_e32 v1, 0xffff0000, v144
	v_lshlrev_b32_e32 v2, 16, v145
	v_and_b32_e32 v3, 0xffff0000, v145
	v_fmac_f32_e32 v0, v246, v32
	v_fmac_f32_e32 v1, v247, v33
	v_fmac_f32_e32 v2, v248, v34
	v_fmac_f32_e32 v3, v249, v35
	v_lshlrev_b32_e32 v246, 16, v130
	v_and_b32_e32 v247, 0xffff0000, v130
	v_lshlrev_b32_e32 v248, 16, v131
	v_and_b32_e32 v249, 0xffff0000, v131
	v_mul_f32_e32 v246, v246, v218
	v_mul_f32_e32 v247, v247, v218
	v_mul_f32_e32 v248, v248, v218
	v_mul_f32_e32 v249, v249, v218
	v_lshlrev_b32_e32 v4, 16, v146
	v_and_b32_e32 v5, 0xffff0000, v146
	v_lshlrev_b32_e32 v6, 16, v147
	v_and_b32_e32 v7, 0xffff0000, v147
	v_fmac_f32_e32 v4, v246, v36
	v_fmac_f32_e32 v5, v247, v37
	v_fmac_f32_e32 v6, v248, v38
	v_fmac_f32_e32 v7, v249, v39
	v_lshlrev_b32_e32 v246, 16, v132
	v_and_b32_e32 v247, 0xffff0000, v132
	v_lshlrev_b32_e32 v248, 16, v133
	v_and_b32_e32 v249, 0xffff0000, v133
	v_mul_f32_e32 v246, v246, v218
	v_mul_f32_e32 v247, v247, v218
	v_mul_f32_e32 v248, v248, v218
	v_mul_f32_e32 v249, v249, v218
	v_lshlrev_b32_e32 v8, 16, v148
	v_and_b32_e32 v9, 0xffff0000, v148
	v_lshlrev_b32_e32 v10, 16, v149
	v_and_b32_e32 v11, 0xffff0000, v149
	v_fmac_f32_e32 v8, v246, v40
	v_fmac_f32_e32 v9, v247, v41
	v_fmac_f32_e32 v10, v248, v42
	v_fmac_f32_e32 v11, v249, v43
	v_lshlrev_b32_e32 v246, 16, v134
	v_and_b32_e32 v247, 0xffff0000, v134
	v_lshlrev_b32_e32 v248, 16, v135
	v_and_b32_e32 v249, 0xffff0000, v135
	v_mul_f32_e32 v246, v246, v218
	v_mul_f32_e32 v247, v247, v218
	v_mul_f32_e32 v248, v248, v218
	v_mul_f32_e32 v249, v249, v218
	v_lshlrev_b32_e32 v12, 16, v150
	v_and_b32_e32 v13, 0xffff0000, v150
	v_lshlrev_b32_e32 v14, 16, v151
	v_and_b32_e32 v15, 0xffff0000, v151
	v_fmac_f32_e32 v12, v246, v44
	v_fmac_f32_e32 v13, v247, v45
	v_fmac_f32_e32 v14, v248, v46
	v_fmac_f32_e32 v15, v249, v47
	v_lshlrev_b32_e32 v246, 16, v136
	v_and_b32_e32 v247, 0xffff0000, v136
	v_lshlrev_b32_e32 v248, 16, v137
	v_and_b32_e32 v249, 0xffff0000, v137
	v_mul_f32_e32 v246, v246, v218
	v_mul_f32_e32 v247, v247, v218
	v_mul_f32_e32 v248, v248, v218
	v_mul_f32_e32 v249, v249, v218
	v_lshlrev_b32_e32 v16, 16, v152
	v_and_b32_e32 v17, 0xffff0000, v152
	v_lshlrev_b32_e32 v18, 16, v153
	v_and_b32_e32 v19, 0xffff0000, v153
	v_fmac_f32_e32 v16, v246, v48
	v_fmac_f32_e32 v17, v247, v49
	v_fmac_f32_e32 v18, v248, v50
	v_fmac_f32_e32 v19, v249, v51
	v_lshlrev_b32_e32 v246, 16, v138
	v_and_b32_e32 v247, 0xffff0000, v138
	v_lshlrev_b32_e32 v248, 16, v139
	v_and_b32_e32 v249, 0xffff0000, v139
	v_mul_f32_e32 v246, v246, v218
	v_mul_f32_e32 v247, v247, v218
	v_mul_f32_e32 v248, v248, v218
	v_mul_f32_e32 v249, v249, v218
	v_lshlrev_b32_e32 v20, 16, v154
	v_and_b32_e32 v21, 0xffff0000, v154
	v_lshlrev_b32_e32 v22, 16, v155
	v_and_b32_e32 v23, 0xffff0000, v155
	v_fmac_f32_e32 v20, v246, v52
	v_fmac_f32_e32 v21, v247, v53
	v_fmac_f32_e32 v22, v248, v54
	v_fmac_f32_e32 v23, v249, v55
	v_lshlrev_b32_e32 v246, 16, v140
	v_and_b32_e32 v247, 0xffff0000, v140
	v_lshlrev_b32_e32 v248, 16, v141
	v_and_b32_e32 v249, 0xffff0000, v141
	v_mul_f32_e32 v246, v246, v218
	v_mul_f32_e32 v247, v247, v218
	v_mul_f32_e32 v248, v248, v218
	v_mul_f32_e32 v249, v249, v218
	v_lshlrev_b32_e32 v24, 16, v156
	v_and_b32_e32 v25, 0xffff0000, v156
	v_lshlrev_b32_e32 v26, 16, v157
	v_and_b32_e32 v27, 0xffff0000, v157
	v_fmac_f32_e32 v24, v246, v56
	v_fmac_f32_e32 v25, v247, v57
	v_fmac_f32_e32 v26, v248, v58
	v_fmac_f32_e32 v27, v249, v59
	v_lshlrev_b32_e32 v246, 16, v142
	v_and_b32_e32 v247, 0xffff0000, v142
	v_lshlrev_b32_e32 v248, 16, v143
	v_and_b32_e32 v249, 0xffff0000, v143
	v_mul_f32_e32 v246, v246, v218
	v_mul_f32_e32 v247, v247, v218
	v_mul_f32_e32 v248, v248, v218
	v_mul_f32_e32 v249, v249, v218
	v_lshlrev_b32_e32 v28, 16, v158
	v_and_b32_e32 v29, 0xffff0000, v158
	v_lshlrev_b32_e32 v30, 16, v159
	v_and_b32_e32 v31, 0xffff0000, v159
	v_fmac_f32_e32 v28, v246, v60
	v_fmac_f32_e32 v29, v247, v61
	v_fmac_f32_e32 v30, v248, v62
	v_fmac_f32_e32 v31, v249, v63
	global_load_dwordx2 v[128:129], v162, s[56:57] nt
	global_load_dwordx2 v[130:131], v162, s[56:57] offset:512 nt
	global_load_dwordx2 v[132:133], v162, s[56:57] offset:1024 nt
	global_load_dwordx2 v[134:135], v162, s[56:57] offset:1536 nt
	global_load_dwordx2 v[136:137], v162, s[56:57] offset:2048 nt
	global_load_dwordx2 v[138:139], v162, s[56:57] offset:2560 nt
	global_load_dwordx2 v[140:141], v162, s[56:57] offset:3072 nt
	global_load_dwordx2 v[142:143], v162, s[56:57] offset:3584 nt
	global_load_dwordx2 v[144:145], v162, s[58:59] nt
	global_load_dwordx2 v[146:147], v162, s[58:59] offset:512 nt
	global_load_dwordx2 v[148:149], v162, s[58:59] offset:1024 nt
	global_load_dwordx2 v[150:151], v162, s[58:59] offset:1536 nt
	global_load_dwordx2 v[152:153], v162, s[58:59] offset:2048 nt
	global_load_dwordx2 v[154:155], v162, s[58:59] offset:2560 nt
	global_load_dwordx2 v[156:157], v162, s[58:59] offset:3072 nt
	global_load_dwordx2 v[158:159], v162, s[58:59] offset:3584 nt
	s_add_u32 s58, s58, 0x8000
	s_addc_u32 s59, s59, 0
	s_add_u32 s56, s56, 0x8000
	s_addc_u32 s57, s57, 0
	global_store_dwordx4 v163, v[0:3], s[70:71]
	global_store_dwordx4 v163, v[4:7], s[70:71] offset:1024
	global_store_dwordx4 v163, v[8:11], s[70:71] offset:2048
	global_store_dwordx4 v163, v[12:15], s[70:71] offset:3072
	s_add_u32 s10, s70, 0x1000
	s_addc_u32 s11, s71, 0
	global_store_dwordx4 v163, v[16:19], s[10:11]
	global_store_dwordx4 v163, v[20:23], s[10:11] offset:1024
	global_store_dwordx4 v163, v[24:27], s[10:11] offset:2048
	global_store_dwordx4 v163, v[28:31], s[10:11] offset:3072
	s_add_u32 s70, s70, 0x10000
	s_addc_u32 s71, s71, 0
	s_waitcnt vmcnt(24)
	v_mov_b32_e32 v250, 0
	v_mov_b32_e32 v251, 0
	v_lshlrev_b32_e32 v246, 16, v166
	v_and_b32_e32 v247, 0xffff0000, v166
	v_lshlrev_b32_e32 v248, 16, v167
	v_and_b32_e32 v249, 0xffff0000, v167
	v_fmac_f32_e32 v250, v246, v246
	v_fmac_f32_e32 v251, v247, v247
	v_fmac_f32_e32 v250, v248, v248
	v_fmac_f32_e32 v251, v249, v249
	v_lshlrev_b32_e32 v246, 16, v168
	v_and_b32_e32 v247, 0xffff0000, v168
	v_lshlrev_b32_e32 v248, 16, v169
	v_and_b32_e32 v249, 0xffff0000, v169
	v_fmac_f32_e32 v250, v246, v246
	v_fmac_f32_e32 v251, v247, v247
	v_fmac_f32_e32 v250, v248, v248
	v_fmac_f32_e32 v251, v249, v249
	v_lshlrev_b32_e32 v246, 16, v170
	v_and_b32_e32 v247, 0xffff0000, v170
	v_lshlrev_b32_e32 v248, 16, v171
	v_and_b32_e32 v249, 0xffff0000, v171
	v_fmac_f32_e32 v250, v246, v246
	v_fmac_f32_e32 v251, v247, v247
	v_fmac_f32_e32 v250, v248, v248
	v_fmac_f32_e32 v251, v249, v249
	v_lshlrev_b32_e32 v246, 16, v172
	v_and_b32_e32 v247, 0xffff0000, v172
	v_lshlrev_b32_e32 v248, 16, v173
	v_and_b32_e32 v249, 0xffff0000, v173
	v_fmac_f32_e32 v250, v246, v246
	v_fmac_f32_e32 v251, v247, v247
	v_fmac_f32_e32 v250, v248, v248
	v_fmac_f32_e32 v251, v249, v249
	v_lshlrev_b32_e32 v246, 16, v174
	v_and_b32_e32 v247, 0xffff0000, v174
	v_lshlrev_b32_e32 v248, 16, v175
	v_and_b32_e32 v249, 0xffff0000, v175
	v_fmac_f32_e32 v250, v246, v246
	v_fmac_f32_e32 v251, v247, v247
	v_fmac_f32_e32 v250, v248, v248
	v_fmac_f32_e32 v251, v249, v249
	v_lshlrev_b32_e32 v246, 16, v176
	v_and_b32_e32 v247, 0xffff0000, v176
	v_lshlrev_b32_e32 v248, 16, v177
	v_and_b32_e32 v249, 0xffff0000, v177
	v_fmac_f32_e32 v250, v246, v246
	v_fmac_f32_e32 v251, v247, v247
	v_fmac_f32_e32 v250, v248, v248
	v_fmac_f32_e32 v251, v249, v249
	v_lshlrev_b32_e32 v246, 16, v178
	v_and_b32_e32 v247, 0xffff0000, v178
	v_lshlrev_b32_e32 v248, 16, v179
	v_and_b32_e32 v249, 0xffff0000, v179
	v_fmac_f32_e32 v250, v246, v246
	v_fmac_f32_e32 v251, v247, v247
	v_fmac_f32_e32 v250, v248, v248
	v_fmac_f32_e32 v251, v249, v249
	v_lshlrev_b32_e32 v246, 16, v180
	v_and_b32_e32 v247, 0xffff0000, v180
	v_lshlrev_b32_e32 v248, 16, v181
	v_and_b32_e32 v249, 0xffff0000, v181
	v_fmac_f32_e32 v250, v246, v246
	v_fmac_f32_e32 v251, v247, v247
	v_fmac_f32_e32 v250, v248, v248
	v_fmac_f32_e32 v251, v249, v249
	v_add_f32_e32 v250, v250, v251
	s_nop 1
	v_add_f32_dpp v218, v250, v250 quad_perm:[1,0,3,2] row_mask:0xf bank_mask:0xf bound_ctrl:1
	s_nop 1
	v_add_f32_dpp v218, v218, v218 quad_perm:[2,3,0,1] row_mask:0xf bank_mask:0xf bound_ctrl:1
	s_nop 1
	v_add_f32_dpp v218, v218, v218 row_ror:4 row_mask:0xf bank_mask:0xf bound_ctrl:1
	s_nop 1
	v_add_f32_dpp v218, v218, v218 row_ror:8 row_mask:0xf bank_mask:0xf bound_ctrl:1
	s_nop 1
	v_readlane_b32 s8, v218, 0
	v_readlane_b32 s9, v218, 16
	v_readlane_b32 s10, v218, 32
	v_readlane_b32 s11, v218, 48
	s_nop 1
	v_mov_b32_e32 v218, s8
	v_add_f32_e32 v218, s9, v218
	v_mov_b32_e32 v219, s10
	v_add_f32_e32 v219, s11, v219
	v_add_f32_e32 v218, v218, v219
	v_mul_f32_e32 v218, 0x3a000000, v218
	v_add_f32_e32 v218, 0x358637bd, v218
	v_rsq_f32_e32 v218, v218
	s_nop 0
	v_lshlrev_b32_e32 v246, 16, v166
	v_and_b32_e32 v247, 0xffff0000, v166
	v_lshlrev_b32_e32 v248, 16, v167
	v_and_b32_e32 v249, 0xffff0000, v167
	v_mul_f32_e32 v246, v246, v218
	v_mul_f32_e32 v247, v247, v218
	v_mul_f32_e32 v248, v248, v218
	v_mul_f32_e32 v249, v249, v218
	v_lshlrev_b32_e32 v0, 16, v182
	v_and_b32_e32 v1, 0xffff0000, v182
	v_lshlrev_b32_e32 v2, 16, v183
	v_and_b32_e32 v3, 0xffff0000, v183
	v_fmac_f32_e32 v0, v246, v32
	v_fmac_f32_e32 v1, v247, v33
	v_fmac_f32_e32 v2, v248, v34
	v_fmac_f32_e32 v3, v249, v35
	v_lshlrev_b32_e32 v246, 16, v168
	v_and_b32_e32 v247, 0xffff0000, v168
	v_lshlrev_b32_e32 v248, 16, v169
	v_and_b32_e32 v249, 0xffff0000, v169
	v_mul_f32_e32 v246, v246, v218
	v_mul_f32_e32 v247, v247, v218
	v_mul_f32_e32 v248, v248, v218
	v_mul_f32_e32 v249, v249, v218
	v_lshlrev_b32_e32 v4, 16, v184
	v_and_b32_e32 v5, 0xffff0000, v184
	v_lshlrev_b32_e32 v6, 16, v185
	v_and_b32_e32 v7, 0xffff0000, v185
	v_fmac_f32_e32 v4, v246, v36
	v_fmac_f32_e32 v5, v247, v37
	v_fmac_f32_e32 v6, v248, v38
	v_fmac_f32_e32 v7, v249, v39
	v_lshlrev_b32_e32 v246, 16, v170
	v_and_b32_e32 v247, 0xffff0000, v170
	v_lshlrev_b32_e32 v248, 16, v171
	v_and_b32_e32 v249, 0xffff0000, v171
	v_mul_f32_e32 v246, v246, v218
	v_mul_f32_e32 v247, v247, v218
	v_mul_f32_e32 v248, v248, v218
	v_mul_f32_e32 v249, v249, v218
	v_lshlrev_b32_e32 v8, 16, v186
	v_and_b32_e32 v9, 0xffff0000, v186
	v_lshlrev_b32_e32 v10, 16, v187
	v_and_b32_e32 v11, 0xffff0000, v187
	v_fmac_f32_e32 v8, v246, v40
	v_fmac_f32_e32 v9, v247, v41
	v_fmac_f32_e32 v10, v248, v42
	v_fmac_f32_e32 v11, v249, v43
	v_lshlrev_b32_e32 v246, 16, v172
	v_and_b32_e32 v247, 0xffff0000, v172
	v_lshlrev_b32_e32 v248, 16, v173
	v_and_b32_e32 v249, 0xffff0000, v173
	v_mul_f32_e32 v246, v246, v218
	v_mul_f32_e32 v247, v247, v218
	v_mul_f32_e32 v248, v248, v218
	v_mul_f32_e32 v249, v249, v218
	v_lshlrev_b32_e32 v12, 16, v188
	v_and_b32_e32 v13, 0xffff0000, v188
	v_lshlrev_b32_e32 v14, 16, v189
	v_and_b32_e32 v15, 0xffff0000, v189
	v_fmac_f32_e32 v12, v246, v44
	v_fmac_f32_e32 v13, v247, v45
	v_fmac_f32_e32 v14, v248, v46
	v_fmac_f32_e32 v15, v249, v47
	v_lshlrev_b32_e32 v246, 16, v174
	v_and_b32_e32 v247, 0xffff0000, v174
	v_lshlrev_b32_e32 v248, 16, v175
	v_and_b32_e32 v249, 0xffff0000, v175
	v_mul_f32_e32 v246, v246, v218
	v_mul_f32_e32 v247, v247, v218
	v_mul_f32_e32 v248, v248, v218
	v_mul_f32_e32 v249, v249, v218
	v_lshlrev_b32_e32 v16, 16, v190
	v_and_b32_e32 v17, 0xffff0000, v190
	v_lshlrev_b32_e32 v18, 16, v191
	v_and_b32_e32 v19, 0xffff0000, v191
	v_fmac_f32_e32 v16, v246, v48
	v_fmac_f32_e32 v17, v247, v49
	v_fmac_f32_e32 v18, v248, v50
	v_fmac_f32_e32 v19, v249, v51
	v_lshlrev_b32_e32 v246, 16, v176
	v_and_b32_e32 v247, 0xffff0000, v176
	v_lshlrev_b32_e32 v248, 16, v177
	v_and_b32_e32 v249, 0xffff0000, v177
	v_mul_f32_e32 v246, v246, v218
	v_mul_f32_e32 v247, v247, v218
	v_mul_f32_e32 v248, v248, v218
	v_mul_f32_e32 v249, v249, v218
	v_lshlrev_b32_e32 v20, 16, v192
	v_and_b32_e32 v21, 0xffff0000, v192
	v_lshlrev_b32_e32 v22, 16, v193
	v_and_b32_e32 v23, 0xffff0000, v193
	v_fmac_f32_e32 v20, v246, v52
	v_fmac_f32_e32 v21, v247, v53
	v_fmac_f32_e32 v22, v248, v54
	v_fmac_f32_e32 v23, v249, v55
	v_lshlrev_b32_e32 v246, 16, v178
	v_and_b32_e32 v247, 0xffff0000, v178
	v_lshlrev_b32_e32 v248, 16, v179
	v_and_b32_e32 v249, 0xffff0000, v179
	v_mul_f32_e32 v246, v246, v218
	v_mul_f32_e32 v247, v247, v218
	v_mul_f32_e32 v248, v248, v218
	v_mul_f32_e32 v249, v249, v218
	v_lshlrev_b32_e32 v24, 16, v194
	v_and_b32_e32 v25, 0xffff0000, v194
	v_lshlrev_b32_e32 v26, 16, v195
	v_and_b32_e32 v27, 0xffff0000, v195
	v_fmac_f32_e32 v24, v246, v56
	v_fmac_f32_e32 v25, v247, v57
	v_fmac_f32_e32 v26, v248, v58
	v_fmac_f32_e32 v27, v249, v59
	v_lshlrev_b32_e32 v246, 16, v180
	v_and_b32_e32 v247, 0xffff0000, v180
	v_lshlrev_b32_e32 v248, 16, v181
	v_and_b32_e32 v249, 0xffff0000, v181
	v_mul_f32_e32 v246, v246, v218
	v_mul_f32_e32 v247, v247, v218
	v_mul_f32_e32 v248, v248, v218
	v_mul_f32_e32 v249, v249, v218
	v_lshlrev_b32_e32 v28, 16, v196
	v_and_b32_e32 v29, 0xffff0000, v196
	v_lshlrev_b32_e32 v30, 16, v197
	v_and_b32_e32 v31, 0xffff0000, v197
	v_fmac_f32_e32 v28, v246, v60
	v_fmac_f32_e32 v29, v247, v61
	v_fmac_f32_e32 v30, v248, v62
	v_fmac_f32_e32 v31, v249, v63
	global_load_dwordx2 v[166:167], v162, s[56:57] nt
	global_load_dwordx2 v[168:169], v162, s[56:57] offset:512 nt
	global_load_dwordx2 v[170:171], v162, s[56:57] offset:1024 nt
	global_load_dwordx2 v[172:173], v162, s[56:57] offset:1536 nt
	global_load_dwordx2 v[174:175], v162, s[56:57] offset:2048 nt
	global_load_dwordx2 v[176:177], v162, s[56:57] offset:2560 nt
	global_load_dwordx2 v[178:179], v162, s[56:57] offset:3072 nt
	global_load_dwordx2 v[180:181], v162, s[56:57] offset:3584 nt
	global_load_dwordx2 v[182:183], v162, s[58:59] nt
	global_load_dwordx2 v[184:185], v162, s[58:59] offset:512 nt
	global_load_dwordx2 v[186:187], v162, s[58:59] offset:1024 nt
	global_load_dwordx2 v[188:189], v162, s[58:59] offset:1536 nt
	global_load_dwordx2 v[190:191], v162, s[58:59] offset:2048 nt
	global_load_dwordx2 v[192:193], v162, s[58:59] offset:2560 nt
	global_load_dwordx2 v[194:195], v162, s[58:59] offset:3072 nt
	global_load_dwordx2 v[196:197], v162, s[58:59] offset:3584 nt
	s_add_u32 s58, s58, 0x8000
	s_addc_u32 s59, s59, 0
	s_add_u32 s56, s56, 0x8000
	s_addc_u32 s57, s57, 0
	global_store_dwordx4 v163, v[0:3], s[70:71]
	global_store_dwordx4 v163, v[4:7], s[70:71] offset:1024
	global_store_dwordx4 v163, v[8:11], s[70:71] offset:2048
	global_store_dwordx4 v163, v[12:15], s[70:71] offset:3072
	s_add_u32 s10, s70, 0x1000
	s_addc_u32 s11, s71, 0
	global_store_dwordx4 v163, v[16:19], s[10:11]
	global_store_dwordx4 v163, v[20:23], s[10:11] offset:1024
	global_store_dwordx4 v163, v[24:27], s[10:11] offset:2048
	global_store_dwordx4 v163, v[28:31], s[10:11] offset:3072
	s_add_u32 s70, s70, 0x10000
	s_addc_u32 s71, s71, 0
	s_add_u32 s76, s76, 1
	s_cmp_lt_u32 s76, 7
	s_cbranch_scc1 .Lmp_V3_loop
	s_waitcnt vmcnt(24)
	v_mov_b32_e32 v250, 0
	v_mov_b32_e32 v251, 0
	v_lshlrev_b32_e32 v246, 16, v128
	v_and_b32_e32 v247, 0xffff0000, v128
	v_lshlrev_b32_e32 v248, 16, v129
	v_and_b32_e32 v249, 0xffff0000, v129
	v_fmac_f32_e32 v250, v246, v246
	v_fmac_f32_e32 v251, v247, v247
	v_fmac_f32_e32 v250, v248, v248
	v_fmac_f32_e32 v251, v249, v249
	v_lshlrev_b32_e32 v246, 16, v130
	v_and_b32_e32 v247, 0xffff0000, v130
	v_lshlrev_b32_e32 v248, 16, v131
	v_and_b32_e32 v249, 0xffff0000, v131
	v_fmac_f32_e32 v250, v246, v246
	v_fmac_f32_e32 v251, v247, v247
	v_fmac_f32_e32 v250, v248, v248
	v_fmac_f32_e32 v251, v249, v249
	v_lshlrev_b32_e32 v246, 16, v132
	v_and_b32_e32 v247, 0xffff0000, v132
	v_lshlrev_b32_e32 v248, 16, v133
	v_and_b32_e32 v249, 0xffff0000, v133
	v_fmac_f32_e32 v250, v246, v246
	v_fmac_f32_e32 v251, v247, v247
	v_fmac_f32_e32 v250, v248, v248
	v_fmac_f32_e32 v251, v249, v249
	v_lshlrev_b32_e32 v246, 16, v134
	v_and_b32_e32 v247, 0xffff0000, v134
	v_lshlrev_b32_e32 v248, 16, v135
	v_and_b32_e32 v249, 0xffff0000, v135
	v_fmac_f32_e32 v250, v246, v246
	v_fmac_f32_e32 v251, v247, v247
	v_fmac_f32_e32 v250, v248, v248
	v_fmac_f32_e32 v251, v249, v249
	v_lshlrev_b32_e32 v246, 16, v136
	v_and_b32_e32 v247, 0xffff0000, v136
	v_lshlrev_b32_e32 v248, 16, v137
	v_and_b32_e32 v249, 0xffff0000, v137
	v_fmac_f32_e32 v250, v246, v246
	v_fmac_f32_e32 v251, v247, v247
	v_fmac_f32_e32 v250, v248, v248
	v_fmac_f32_e32 v251, v249, v249
	v_lshlrev_b32_e32 v246, 16, v138
	v_and_b32_e32 v247, 0xffff0000, v138
	v_lshlrev_b32_e32 v248, 16, v139
	v_and_b32_e32 v249, 0xffff0000, v139
	v_fmac_f32_e32 v250, v246, v246
	v_fmac_f32_e32 v251, v247, v247
	v_fmac_f32_e32 v250, v248, v248
	v_fmac_f32_e32 v251, v249, v249
	v_lshlrev_b32_e32 v246, 16, v140
	v_and_b32_e32 v247, 0xffff0000, v140
	v_lshlrev_b32_e32 v248, 16, v141
	v_and_b32_e32 v249, 0xffff0000, v141
	v_fmac_f32_e32 v250, v246, v246
	v_fmac_f32_e32 v251, v247, v247
	v_fmac_f32_e32 v250, v248, v248
	v_fmac_f32_e32 v251, v249, v249
	v_lshlrev_b32_e32 v246, 16, v142
	v_and_b32_e32 v247, 0xffff0000, v142
	v_lshlrev_b32_e32 v248, 16, v143
	v_and_b32_e32 v249, 0xffff0000, v143
	v_fmac_f32_e32 v250, v246, v246
	v_fmac_f32_e32 v251, v247, v247
	v_fmac_f32_e32 v250, v248, v248
	v_fmac_f32_e32 v251, v249, v249
	v_add_f32_e32 v250, v250, v251
	s_nop 1
	v_add_f32_dpp v218, v250, v250 quad_perm:[1,0,3,2] row_mask:0xf bank_mask:0xf bound_ctrl:1
	s_nop 1
	v_add_f32_dpp v218, v218, v218 quad_perm:[2,3,0,1] row_mask:0xf bank_mask:0xf bound_ctrl:1
	s_nop 1
	v_add_f32_dpp v218, v218, v218 row_ror:4 row_mask:0xf bank_mask:0xf bound_ctrl:1
	s_nop 1
	v_add_f32_dpp v218, v218, v218 row_ror:8 row_mask:0xf bank_mask:0xf bound_ctrl:1
	s_nop 1
	v_readlane_b32 s8, v218, 0
	v_readlane_b32 s9, v218, 16
	v_readlane_b32 s10, v218, 32
	v_readlane_b32 s11, v218, 48
	s_nop 1
	v_mov_b32_e32 v218, s8
	v_add_f32_e32 v218, s9, v218
	v_mov_b32_e32 v219, s10
	v_add_f32_e32 v219, s11, v219
	v_add_f32_e32 v218, v218, v219
	v_mul_f32_e32 v218, 0x3a000000, v218
	v_add_f32_e32 v218, 0x358637bd, v218
	v_rsq_f32_e32 v218, v218
	s_nop 0
	v_lshlrev_b32_e32 v246, 16, v128
	v_and_b32_e32 v247, 0xffff0000, v128
	v_lshlrev_b32_e32 v248, 16, v129
	v_and_b32_e32 v249, 0xffff0000, v129
	v_mul_f32_e32 v246, v246, v218
	v_mul_f32_e32 v247, v247, v218
	v_mul_f32_e32 v248, v248, v218
	v_mul_f32_e32 v249, v249, v218
	v_lshlrev_b32_e32 v0, 16, v144
	v_and_b32_e32 v1, 0xffff0000, v144
	v_lshlrev_b32_e32 v2, 16, v145
	v_and_b32_e32 v3, 0xffff0000, v145
	v_fmac_f32_e32 v0, v246, v32
	v_fmac_f32_e32 v1, v247, v33
	v_fmac_f32_e32 v2, v248, v34
	v_fmac_f32_e32 v3, v249, v35
	v_lshlrev_b32_e32 v246, 16, v130
	v_and_b32_e32 v247, 0xffff0000, v130
	v_lshlrev_b32_e32 v248, 16, v131
	v_and_b32_e32 v249, 0xffff0000, v131
	v_mul_f32_e32 v246, v246, v218
	v_mul_f32_e32 v247, v247, v218
	v_mul_f32_e32 v248, v248, v218
	v_mul_f32_e32 v249, v249, v218
	v_lshlrev_b32_e32 v4, 16, v146
	v_and_b32_e32 v5, 0xffff0000, v146
	v_lshlrev_b32_e32 v6, 16, v147
	v_and_b32_e32 v7, 0xffff0000, v147
	v_fmac_f32_e32 v4, v246, v36
	v_fmac_f32_e32 v5, v247, v37
	v_fmac_f32_e32 v6, v248, v38
	v_fmac_f32_e32 v7, v249, v39
	v_lshlrev_b32_e32 v246, 16, v132
	v_and_b32_e32 v247, 0xffff0000, v132
	v_lshlrev_b32_e32 v248, 16, v133
	v_and_b32_e32 v249, 0xffff0000, v133
	v_mul_f32_e32 v246, v246, v218
	v_mul_f32_e32 v247, v247, v218
	v_mul_f32_e32 v248, v248, v218
	v_mul_f32_e32 v249, v249, v218
	v_lshlrev_b32_e32 v8, 16, v148
	v_and_b32_e32 v9, 0xffff0000, v148
	v_lshlrev_b32_e32 v10, 16, v149
	v_and_b32_e32 v11, 0xffff0000, v149
	v_fmac_f32_e32 v8, v246, v40
	v_fmac_f32_e32 v9, v247, v41
	v_fmac_f32_e32 v10, v248, v42
	v_fmac_f32_e32 v11, v249, v43
	v_lshlrev_b32_e32 v246, 16, v134
	v_and_b32_e32 v247, 0xffff0000, v134
	v_lshlrev_b32_e32 v248, 16, v135
	v_and_b32_e32 v249, 0xffff0000, v135
	v_mul_f32_e32 v246, v246, v218
	v_mul_f32_e32 v247, v247, v218
	v_mul_f32_e32 v248, v248, v218
	v_mul_f32_e32 v249, v249, v218
	v_lshlrev_b32_e32 v12, 16, v150
	v_and_b32_e32 v13, 0xffff0000, v150
	v_lshlrev_b32_e32 v14, 16, v151
	v_and_b32_e32 v15, 0xffff0000, v151
	v_fmac_f32_e32 v12, v246, v44
	v_fmac_f32_e32 v13, v247, v45
	v_fmac_f32_e32 v14, v248, v46
	v_fmac_f32_e32 v15, v249, v47
	v_lshlrev_b32_e32 v246, 16, v136
	v_and_b32_e32 v247, 0xffff0000, v136
	v_lshlrev_b32_e32 v248, 16, v137
	v_and_b32_e32 v249, 0xffff0000, v137
	v_mul_f32_e32 v246, v246, v218
	v_mul_f32_e32 v247, v247, v218
	v_mul_f32_e32 v248, v248, v218
	v_mul_f32_e32 v249, v249, v218
	v_lshlrev_b32_e32 v16, 16, v152
	v_and_b32_e32 v17, 0xffff0000, v152
	v_lshlrev_b32_e32 v18, 16, v153
	v_and_b32_e32 v19, 0xffff0000, v153
	v_fmac_f32_e32 v16, v246, v48
	v_fmac_f32_e32 v17, v247, v49
	v_fmac_f32_e32 v18, v248, v50
	v_fmac_f32_e32 v19, v249, v51
	v_lshlrev_b32_e32 v246, 16, v138
	v_and_b32_e32 v247, 0xffff0000, v138
	v_lshlrev_b32_e32 v248, 16, v139
	v_and_b32_e32 v249, 0xffff0000, v139
	v_mul_f32_e32 v246, v246, v218
	v_mul_f32_e32 v247, v247, v218
	v_mul_f32_e32 v248, v248, v218
	v_mul_f32_e32 v249, v249, v218
	v_lshlrev_b32_e32 v20, 16, v154
	v_and_b32_e32 v21, 0xffff0000, v154
	v_lshlrev_b32_e32 v22, 16, v155
	v_and_b32_e32 v23, 0xffff0000, v155
	v_fmac_f32_e32 v20, v246, v52
	v_fmac_f32_e32 v21, v247, v53
	v_fmac_f32_e32 v22, v248, v54
	v_fmac_f32_e32 v23, v249, v55
	v_lshlrev_b32_e32 v246, 16, v140
	v_and_b32_e32 v247, 0xffff0000, v140
	v_lshlrev_b32_e32 v248, 16, v141
	v_and_b32_e32 v249, 0xffff0000, v141
	v_mul_f32_e32 v246, v246, v218
	v_mul_f32_e32 v247, v247, v218
	v_mul_f32_e32 v248, v248, v218
	v_mul_f32_e32 v249, v249, v218
	v_lshlrev_b32_e32 v24, 16, v156
	v_and_b32_e32 v25, 0xffff0000, v156
	v_lshlrev_b32_e32 v26, 16, v157
	v_and_b32_e32 v27, 0xffff0000, v157
	v_fmac_f32_e32 v24, v246, v56
	v_fmac_f32_e32 v25, v247, v57
	v_fmac_f32_e32 v26, v248, v58
	v_fmac_f32_e32 v27, v249, v59
	v_lshlrev_b32_e32 v246, 16, v142
	v_and_b32_e32 v247, 0xffff0000, v142
	v_lshlrev_b32_e32 v248, 16, v143
	v_and_b32_e32 v249, 0xffff0000, v143
	v_mul_f32_e32 v246, v246, v218
	v_mul_f32_e32 v247, v247, v218
	v_mul_f32_e32 v248, v248, v218
	v_mul_f32_e32 v249, v249, v218
	v_lshlrev_b32_e32 v28, 16, v158
	v_and_b32_e32 v29, 0xffff0000, v158
	v_lshlrev_b32_e32 v30, 16, v159
	v_and_b32_e32 v31, 0xffff0000, v159
	v_fmac_f32_e32 v28, v246, v60
	v_fmac_f32_e32 v29, v247, v61
	v_fmac_f32_e32 v30, v248, v62
	v_fmac_f32_e32 v31, v249, v63
	global_store_dwordx4 v163, v[0:3], s[70:71]
	global_store_dwordx4 v163, v[4:7], s[70:71] offset:1024
	global_store_dwordx4 v163, v[8:11], s[70:71] offset:2048
	global_store_dwordx4 v163, v[12:15], s[70:71] offset:3072
	s_add_u32 s10, s70, 0x1000
	s_addc_u32 s11, s71, 0
	global_store_dwordx4 v163, v[16:19], s[10:11]
	global_store_dwordx4 v163, v[20:23], s[10:11] offset:1024
	global_store_dwordx4 v163, v[24:27], s[10:11] offset:2048
	global_store_dwordx4 v163, v[28:31], s[10:11] offset:3072
	s_add_u32 s70, s70, 0x10000
	s_addc_u32 s71, s71, 0
	s_waitcnt vmcnt(16)
	v_mov_b32_e32 v250, 0
	v_mov_b32_e32 v251, 0
	v_lshlrev_b32_e32 v246, 16, v166
	v_and_b32_e32 v247, 0xffff0000, v166
	v_lshlrev_b32_e32 v248, 16, v167
	v_and_b32_e32 v249, 0xffff0000, v167
	v_fmac_f32_e32 v250, v246, v246
	v_fmac_f32_e32 v251, v247, v247
	v_fmac_f32_e32 v250, v248, v248
	v_fmac_f32_e32 v251, v249, v249
	v_lshlrev_b32_e32 v246, 16, v168
	v_and_b32_e32 v247, 0xffff0000, v168
	v_lshlrev_b32_e32 v248, 16, v169
	v_and_b32_e32 v249, 0xffff0000, v169
	v_fmac_f32_e32 v250, v246, v246
	v_fmac_f32_e32 v251, v247, v247
	v_fmac_f32_e32 v250, v248, v248
	v_fmac_f32_e32 v251, v249, v249
	v_lshlrev_b32_e32 v246, 16, v170
	v_and_b32_e32 v247, 0xffff0000, v170
	v_lshlrev_b32_e32 v248, 16, v171
	v_and_b32_e32 v249, 0xffff0000, v171
	v_fmac_f32_e32 v250, v246, v246
	v_fmac_f32_e32 v251, v247, v247
	v_fmac_f32_e32 v250, v248, v248
	v_fmac_f32_e32 v251, v249, v249
	v_lshlrev_b32_e32 v246, 16, v172
	v_and_b32_e32 v247, 0xffff0000, v172
	v_lshlrev_b32_e32 v248, 16, v173
	v_and_b32_e32 v249, 0xffff0000, v173
	v_fmac_f32_e32 v250, v246, v246
	v_fmac_f32_e32 v251, v247, v247
	v_fmac_f32_e32 v250, v248, v248
	v_fmac_f32_e32 v251, v249, v249
	v_lshlrev_b32_e32 v246, 16, v174
	v_and_b32_e32 v247, 0xffff0000, v174
	v_lshlrev_b32_e32 v248, 16, v175
	v_and_b32_e32 v249, 0xffff0000, v175
	v_fmac_f32_e32 v250, v246, v246
	v_fmac_f32_e32 v251, v247, v247
	v_fmac_f32_e32 v250, v248, v248
	v_fmac_f32_e32 v251, v249, v249
	v_lshlrev_b32_e32 v246, 16, v176
	v_and_b32_e32 v247, 0xffff0000, v176
	v_lshlrev_b32_e32 v248, 16, v177
	v_and_b32_e32 v249, 0xffff0000, v177
	v_fmac_f32_e32 v250, v246, v246
	v_fmac_f32_e32 v251, v247, v247
	v_fmac_f32_e32 v250, v248, v248
	v_fmac_f32_e32 v251, v249, v249
	v_lshlrev_b32_e32 v246, 16, v178
	v_and_b32_e32 v247, 0xffff0000, v178
	v_lshlrev_b32_e32 v248, 16, v179
	v_and_b32_e32 v249, 0xffff0000, v179
	v_fmac_f32_e32 v250, v246, v246
	v_fmac_f32_e32 v251, v247, v247
	v_fmac_f32_e32 v250, v248, v248
	v_fmac_f32_e32 v251, v249, v249
	v_lshlrev_b32_e32 v246, 16, v180
	v_and_b32_e32 v247, 0xffff0000, v180
	v_lshlrev_b32_e32 v248, 16, v181
	v_and_b32_e32 v249, 0xffff0000, v181
	v_fmac_f32_e32 v250, v246, v246
	v_fmac_f32_e32 v251, v247, v247
	v_fmac_f32_e32 v250, v248, v248
	v_fmac_f32_e32 v251, v249, v249
	v_add_f32_e32 v250, v250, v251
	s_nop 1
	v_add_f32_dpp v218, v250, v250 quad_perm:[1,0,3,2] row_mask:0xf bank_mask:0xf bound_ctrl:1
	s_nop 1
	v_add_f32_dpp v218, v218, v218 quad_perm:[2,3,0,1] row_mask:0xf bank_mask:0xf bound_ctrl:1
	s_nop 1
	v_add_f32_dpp v218, v218, v218 row_ror:4 row_mask:0xf bank_mask:0xf bound_ctrl:1
	s_nop 1
	v_add_f32_dpp v218, v218, v218 row_ror:8 row_mask:0xf bank_mask:0xf bound_ctrl:1
	s_nop 1
	v_readlane_b32 s8, v218, 0
	v_readlane_b32 s9, v218, 16
	v_readlane_b32 s10, v218, 32
	v_readlane_b32 s11, v218, 48
	s_nop 1
	v_mov_b32_e32 v218, s8
	v_add_f32_e32 v218, s9, v218
	v_mov_b32_e32 v219, s10
	v_add_f32_e32 v219, s11, v219
	v_add_f32_e32 v218, v218, v219
	v_mul_f32_e32 v218, 0x3a000000, v218
	v_add_f32_e32 v218, 0x358637bd, v218
	v_rsq_f32_e32 v218, v218
	s_nop 0
	v_lshlrev_b32_e32 v246, 16, v166
	v_and_b32_e32 v247, 0xffff0000, v166
	v_lshlrev_b32_e32 v248, 16, v167
	v_and_b32_e32 v249, 0xffff0000, v167
	v_mul_f32_e32 v246, v246, v218
	v_mul_f32_e32 v247, v247, v218
	v_mul_f32_e32 v248, v248, v218
	v_mul_f32_e32 v249, v249, v218
	v_lshlrev_b32_e32 v0, 16, v182
	v_and_b32_e32 v1, 0xffff0000, v182
	v_lshlrev_b32_e32 v2, 16, v183
	v_and_b32_e32 v3, 0xffff0000, v183
	v_fmac_f32_e32 v0, v246, v32
	v_fmac_f32_e32 v1, v247, v33
	v_fmac_f32_e32 v2, v248, v34
	v_fmac_f32_e32 v3, v249, v35
	v_lshlrev_b32_e32 v246, 16, v168
	v_and_b32_e32 v247, 0xffff0000, v168
	v_lshlrev_b32_e32 v248, 16, v169
	v_and_b32_e32 v249, 0xffff0000, v169
	v_mul_f32_e32 v246, v246, v218
	v_mul_f32_e32 v247, v247, v218
	v_mul_f32_e32 v248, v248, v218
	v_mul_f32_e32 v249, v249, v218
	v_lshlrev_b32_e32 v4, 16, v184
	v_and_b32_e32 v5, 0xffff0000, v184
	v_lshlrev_b32_e32 v6, 16, v185
	v_and_b32_e32 v7, 0xffff0000, v185
	v_fmac_f32_e32 v4, v246, v36
	v_fmac_f32_e32 v5, v247, v37
	v_fmac_f32_e32 v6, v248, v38
	v_fmac_f32_e32 v7, v249, v39
	v_lshlrev_b32_e32 v246, 16, v170
	v_and_b32_e32 v247, 0xffff0000, v170
	v_lshlrev_b32_e32 v248, 16, v171
	v_and_b32_e32 v249, 0xffff0000, v171
	v_mul_f32_e32 v246, v246, v218
	v_mul_f32_e32 v247, v247, v218
	v_mul_f32_e32 v248, v248, v218
	v_mul_f32_e32 v249, v249, v218
	v_lshlrev_b32_e32 v8, 16, v186
	v_and_b32_e32 v9, 0xffff0000, v186
	v_lshlrev_b32_e32 v10, 16, v187
	v_and_b32_e32 v11, 0xffff0000, v187
	v_fmac_f32_e32 v8, v246, v40
	v_fmac_f32_e32 v9, v247, v41
	v_fmac_f32_e32 v10, v248, v42
	v_fmac_f32_e32 v11, v249, v43
	v_lshlrev_b32_e32 v246, 16, v172
	v_and_b32_e32 v247, 0xffff0000, v172
	v_lshlrev_b32_e32 v248, 16, v173
	v_and_b32_e32 v249, 0xffff0000, v173
	v_mul_f32_e32 v246, v246, v218
	v_mul_f32_e32 v247, v247, v218
	v_mul_f32_e32 v248, v248, v218
	v_mul_f32_e32 v249, v249, v218
	v_lshlrev_b32_e32 v12, 16, v188
	v_and_b32_e32 v13, 0xffff0000, v188
	v_lshlrev_b32_e32 v14, 16, v189
	v_and_b32_e32 v15, 0xffff0000, v189
	v_fmac_f32_e32 v12, v246, v44
	v_fmac_f32_e32 v13, v247, v45
	v_fmac_f32_e32 v14, v248, v46
	v_fmac_f32_e32 v15, v249, v47
	v_lshlrev_b32_e32 v246, 16, v174
	v_and_b32_e32 v247, 0xffff0000, v174
	v_lshlrev_b32_e32 v248, 16, v175
	v_and_b32_e32 v249, 0xffff0000, v175
	v_mul_f32_e32 v246, v246, v218
	v_mul_f32_e32 v247, v247, v218
	v_mul_f32_e32 v248, v248, v218
	v_mul_f32_e32 v249, v249, v218
	v_lshlrev_b32_e32 v16, 16, v190
	v_and_b32_e32 v17, 0xffff0000, v190
	v_lshlrev_b32_e32 v18, 16, v191
	v_and_b32_e32 v19, 0xffff0000, v191
	v_fmac_f32_e32 v16, v246, v48
	v_fmac_f32_e32 v17, v247, v49
	v_fmac_f32_e32 v18, v248, v50
	v_fmac_f32_e32 v19, v249, v51
	v_lshlrev_b32_e32 v246, 16, v176
	v_and_b32_e32 v247, 0xffff0000, v176
	v_lshlrev_b32_e32 v248, 16, v177
	v_and_b32_e32 v249, 0xffff0000, v177
	v_mul_f32_e32 v246, v246, v218
	v_mul_f32_e32 v247, v247, v218
	v_mul_f32_e32 v248, v248, v218
	v_mul_f32_e32 v249, v249, v218
	v_lshlrev_b32_e32 v20, 16, v192
	v_and_b32_e32 v21, 0xffff0000, v192
	v_lshlrev_b32_e32 v22, 16, v193
	v_and_b32_e32 v23, 0xffff0000, v193
	v_fmac_f32_e32 v20, v246, v52
	v_fmac_f32_e32 v21, v247, v53
	v_fmac_f32_e32 v22, v248, v54
	v_fmac_f32_e32 v23, v249, v55
	v_lshlrev_b32_e32 v246, 16, v178
	v_and_b32_e32 v247, 0xffff0000, v178
	v_lshlrev_b32_e32 v248, 16, v179
	v_and_b32_e32 v249, 0xffff0000, v179
	v_mul_f32_e32 v246, v246, v218
	v_mul_f32_e32 v247, v247, v218
	v_mul_f32_e32 v248, v248, v218
	v_mul_f32_e32 v249, v249, v218
	v_lshlrev_b32_e32 v24, 16, v194
	v_and_b32_e32 v25, 0xffff0000, v194
	v_lshlrev_b32_e32 v26, 16, v195
	v_and_b32_e32 v27, 0xffff0000, v195
	v_fmac_f32_e32 v24, v246, v56
	v_fmac_f32_e32 v25, v247, v57
	v_fmac_f32_e32 v26, v248, v58
	v_fmac_f32_e32 v27, v249, v59
	v_lshlrev_b32_e32 v246, 16, v180
	v_and_b32_e32 v247, 0xffff0000, v180
	v_lshlrev_b32_e32 v248, 16, v181
	v_and_b32_e32 v249, 0xffff0000, v181
	v_mul_f32_e32 v246, v246, v218
	v_mul_f32_e32 v247, v247, v218
	v_mul_f32_e32 v248, v248, v218
	v_mul_f32_e32 v249, v249, v218
	v_lshlrev_b32_e32 v28, 16, v196
	v_and_b32_e32 v29, 0xffff0000, v196
	v_lshlrev_b32_e32 v30, 16, v197
	v_and_b32_e32 v31, 0xffff0000, v197
	v_fmac_f32_e32 v28, v246, v60
	v_fmac_f32_e32 v29, v247, v61
	v_fmac_f32_e32 v30, v248, v62
	v_fmac_f32_e32 v31, v249, v63
	global_store_dwordx4 v163, v[0:3], s[70:71]
	global_store_dwordx4 v163, v[4:7], s[70:71] offset:1024
	global_store_dwordx4 v163, v[8:11], s[70:71] offset:2048
	global_store_dwordx4 v163, v[12:15], s[70:71] offset:3072
	s_add_u32 s10, s70, 0x1000
	s_addc_u32 s11, s71, 0
	global_store_dwordx4 v163, v[16:19], s[10:11]
	global_store_dwordx4 v163, v[20:23], s[10:11] offset:1024
	global_store_dwordx4 v163, v[24:27], s[10:11] offset:2048
	global_store_dwordx4 v163, v[28:31], s[10:11] offset:3072
	s_add_u32 s70, s70, 0x10000
	s_addc_u32 s71, s71, 0
	s_branch .Lmp_done
